# K-loops: dropped the second lgkmcnt(0) wait after the pre-MFMA barrier (the same wait runs right before the barrier)
# baseline (speedup 1.0000x reference)
.LBB0_276:
	s_or_b64 exec, exec, s[60:61]
	s_add_u32 s62, s56, 0x10000
	s_addc_u32 s63, s57, 0
	s_and_b64 s[60:61], s[34:35], exec
	s_cselect_b32 s67, s51, s63
	s_cselect_b32 s66, s50, s62
	s_add_u32 s62, s58, 0x10000
	s_addc_u32 s63, s59, 0
	s_and_b64 s[60:61], s[34:35], exec
	s_cselect_b32 s63, s53, s63
	s_cselect_b32 s62, s52, s62
	s_add_u32 s60, s66, 0x8000
	s_addc_u32 s61, s67, 0
	s_add_u32 s64, s62, 0x8000
	s_addc_u32 s65, s63, 0
	s_add_i32 s84, 0, 0x10000
	s_add_i32 s85, 0, 0x14000
	v_add_u32_e32 v132, s84, v141
	v_add_u32_e32 v133, s85, v141
	ds_read_b128 v[2:5], v132
	ds_read_b128 v[6:9], v132 offset:1024
	ds_read_b128 v[10:13], v132 offset:2048
	ds_read_b128 v[14:17], v132 offset:3072
	ds_read_b128 v[18:21], v133
	ds_read_b128 v[22:25], v133 offset:1024
	ds_read_b128 v[26:29], v133 offset:2048
	ds_read_b128 v[30:33], v133 offset:3072
	s_add_u32 s82, s56, 0xc000
	s_addc_u32 s83, s57, 0
	s_add_i32 s80, s15, 0xc000
	s_mov_b32 m0, s80
	s_add_i32 s81, s15, 0xe000
	ds_read_b128 v[34:37], v143
	ds_read_b128 v[38:41], v143 offset:1024
	ds_read_b128 v[42:45], v143 offset:2048
	ds_read_b128 v[46:49], v143 offset:3072
	ds_read_b128 v[50:53], v143 offset:4096
	ds_read_b128 v[54:57], v143 offset:5120
	ds_read_b128 v[58:61], v143 offset:6144
	ds_read_b128 v[62:65], v143 offset:7168
	s_nop 0
	global_load_lds_dwordx4 v137, s[82:83]
	s_mov_b32 m0, s81
	s_nop 0
	global_load_lds_dwordx4 v139, s[82:83]
	s_waitcnt vmcnt(8)
	s_waitcnt lgkmcnt(0)
	s_setprio 1
	s_barrier
	v_mfma_f32_16x16x32_bf16 v[86:89], v[10:13], v[50:53], 0
	v_mfma_f32_16x16x32_bf16 v[90:93], v[14:17], v[54:57], v[86:89]
	v_mfma_f32_16x16x32_bf16 v[86:89], v[2:5], v[58:61], 0
	v_mfma_f32_16x16x32_bf16 v[66:69], v[2:5], v[34:37], 0
	v_mfma_f32_16x16x32_bf16 v[70:73], v[10:13], v[34:37], 0
	v_mfma_f32_16x16x32_bf16 v[74:77], v[2:5], v[42:45], 0
	v_mfma_f32_16x16x32_bf16 v[78:81], v[10:13], v[42:45], 0
	v_mfma_f32_16x16x32_bf16 v[82:85], v[2:5], v[50:53], 0
	v_mfma_f32_16x16x32_bf16 v[94:97], v[6:9], v[62:65], v[86:89]
	v_mfma_f32_16x16x32_bf16 v[86:89], v[10:13], v[58:61], 0
	v_mfma_f32_16x16x32_bf16 v[66:69], v[6:9], v[38:41], v[66:69]
	v_mfma_f32_16x16x32_bf16 v[70:73], v[14:17], v[38:41], v[70:73]
	v_mfma_f32_16x16x32_bf16 v[74:77], v[6:9], v[46:49], v[74:77]
	v_mfma_f32_16x16x32_bf16 v[78:81], v[14:17], v[46:49], v[78:81]
	v_mfma_f32_16x16x32_bf16 v[82:85], v[6:9], v[54:57], v[82:85]
	v_mfma_f32_16x16x32_bf16 v[106:109], v[14:17], v[62:65], v[86:89]
	s_setprio 0
	s_setprio 1
	v_mfma_f32_16x16x32_bf16 v[86:89], v[18:21], v[34:37], 0
	v_mfma_f32_16x16x32_bf16 v[34:37], v[26:29], v[34:37], 0
	v_mfma_f32_16x16x32_bf16 v[110:113], v[22:25], v[38:41], v[86:89]
	v_mfma_f32_16x16x32_bf16 v[34:37], v[30:33], v[38:41], v[34:37]
	v_mfma_f32_16x16x32_bf16 v[38:41], v[18:21], v[42:45], 0
	v_mfma_f32_16x16x32_bf16 v[42:45], v[26:29], v[42:45], 0
	v_mfma_f32_16x16x32_bf16 v[38:41], v[22:25], v[46:49], v[38:41]
	v_mfma_f32_16x16x32_bf16 v[42:45], v[30:33], v[46:49], v[42:45]
	v_mfma_f32_16x16x32_bf16 v[46:49], v[18:21], v[50:53], 0
	v_mfma_f32_16x16x32_bf16 v[50:53], v[26:29], v[50:53], 0
	v_mfma_f32_16x16x32_bf16 v[46:49], v[22:25], v[54:57], v[46:49]
	v_mfma_f32_16x16x32_bf16 v[50:53], v[30:33], v[54:57], v[50:53]
	v_mfma_f32_16x16x32_bf16 v[54:57], v[18:21], v[58:61], 0
	v_mfma_f32_16x16x32_bf16 v[144:147], v[22:25], v[62:65], v[54:57]
	v_mfma_f32_16x16x32_bf16 v[54:57], v[26:29], v[58:61], 0
	v_mfma_f32_16x16x32_bf16 v[58:61], v[30:33], v[62:65], v[54:57]
	s_barrier
	s_setprio 0
	s_add_i32 s82, s84, s14
	s_add_i32 s83, s82, 0x2000
	s_mov_b32 m0, s82
	s_add_u32 s86, s62, 0x4000
	s_nop 0
	ds_read_b128 v[54:57], v143 offset:16384
	ds_read_b128 v[62:65], v143 offset:17408
	ds_read_b128 v[86:89], v143 offset:18432
	ds_read_b128 v[98:101], v143 offset:19456
	ds_read_b128 v[102:105], v143 offset:20480
	ds_read_b128 v[114:117], v143 offset:21504
	ds_read_b128 v[118:121], v143 offset:22528
	ds_read_b128 v[122:125], v143 offset:23552
	s_addc_u32 s87, s63, 0
	global_load_lds_dwordx4 v138, s[62:63]
	s_mov_b32 m0, s83
	s_add_i32 s84, s85, s14
	s_add_i32 s85, s84, 0x2000
	global_load_lds_dwordx4 v140, s[62:63]
	s_mov_b32 m0, s84
	s_nop 0
	global_load_lds_dwordx4 v138, s[86:87]
	s_mov_b32 m0, s85
	s_nop 0
	global_load_lds_dwordx4 v140, s[86:87]
	s_mov_b32 m0, s15
	s_nop 0
	global_load_lds_dwordx4 v137, s[66:67]
	s_mov_b32 m0, s18
	s_nop 0
	global_load_lds_dwordx4 v139, s[66:67]
	s_waitcnt vmcnt(8)
	s_waitcnt lgkmcnt(0)
	s_setprio 1
	s_barrier
	v_mfma_f32_16x16x32_bf16 v[126:129], v[2:5], v[54:57], 0
	v_mfma_f32_16x16x32_bf16 v[148:151], v[6:9], v[62:65], v[126:129]
	v_mfma_f32_16x16x32_bf16 v[126:129], v[10:13], v[54:57], 0
	v_mfma_f32_16x16x32_bf16 v[152:155], v[14:17], v[62:65], v[126:129]
	v_mfma_f32_16x16x32_bf16 v[126:129], v[2:5], v[86:89], 0
	v_mfma_f32_16x16x32_bf16 v[156:159], v[6:9], v[98:101], v[126:129]
	v_mfma_f32_16x16x32_bf16 v[126:129], v[10:13], v[86:89], 0
	v_mfma_f32_16x16x32_bf16 v[160:163], v[14:17], v[98:101], v[126:129]
	v_mfma_f32_16x16x32_bf16 v[126:129], v[2:5], v[102:105], 0
	v_mfma_f32_16x16x32_bf16 v[2:5], v[2:5], v[118:121], 0
	v_mfma_f32_16x16x32_bf16 v[164:167], v[6:9], v[114:117], v[126:129]
	v_mfma_f32_16x16x32_bf16 v[2:5], v[6:9], v[122:125], v[2:5]
	v_mfma_f32_16x16x32_bf16 v[6:9], v[10:13], v[118:121], 0
	v_mfma_f32_16x16x32_bf16 v[126:129], v[10:13], v[102:105], 0
	v_mfma_f32_16x16x32_bf16 v[10:13], v[14:17], v[122:125], v[6:9]
	v_mfma_f32_16x16x32_bf16 v[168:171], v[14:17], v[114:117], v[126:129]
	s_setprio 0
	s_setprio 1
	v_mfma_f32_16x16x32_bf16 v[6:9], v[18:21], v[54:57], 0
	v_mfma_f32_16x16x32_bf16 v[14:17], v[22:25], v[62:65], v[6:9]
	v_mfma_f32_16x16x32_bf16 v[6:9], v[26:29], v[54:57], 0
	v_mfma_f32_16x16x32_bf16 v[172:175], v[30:33], v[62:65], v[6:9]
	v_mfma_f32_16x16x32_bf16 v[6:9], v[18:21], v[86:89], 0
	v_mfma_f32_16x16x32_bf16 v[176:179], v[22:25], v[98:101], v[6:9]
	v_mfma_f32_16x16x32_bf16 v[6:9], v[26:29], v[86:89], 0
	v_mfma_f32_16x16x32_bf16 v[180:183], v[30:33], v[98:101], v[6:9]
	v_mfma_f32_16x16x32_bf16 v[6:9], v[18:21], v[102:105], 0
	v_mfma_f32_16x16x32_bf16 v[184:187], v[22:25], v[114:117], v[6:9]
	v_mfma_f32_16x16x32_bf16 v[6:9], v[26:29], v[102:105], 0
	v_mfma_f32_16x16x32_bf16 v[210:213], v[30:33], v[114:117], v[6:9]
	v_mfma_f32_16x16x32_bf16 v[6:9], v[18:21], v[118:121], 0
	v_mfma_f32_16x16x32_bf16 v[214:217], v[22:25], v[122:125], v[6:9]
	v_mfma_f32_16x16x32_bf16 v[6:9], v[26:29], v[118:121], 0
	v_mfma_f32_16x16x32_bf16 v[218:221], v[30:33], v[122:125], v[6:9]
	s_barrier
	s_setprio 0
	s_add_i32 s86, 0, 0x18000
	s_add_i32 s87, 0, 0x1c000
	v_add_u32_e32 v134, s86, v141
	v_add_u32_e32 v135, s87, v141
	s_nop 0
	ds_read_b128 v[6:9], v134
	ds_read_b128 v[26:29], v134 offset:1024
	ds_read_b128 v[30:33], v134 offset:2048
	ds_read_b128 v[222:225], v134 offset:3072
	ds_read_b128 v[236:239], v135
	ds_read_b128 v[240:243], v135 offset:1024
	ds_read_b128 v[244:247], v135 offset:2048
	ds_read_b128 v[232:235], v135 offset:3072
	s_add_u32 s66, s66, 0x4000
	s_addc_u32 s67, s67, 0
	s_mov_b32 m0, s20
	ds_read_b128 v[18:21], v143 offset:32768
	ds_read_b128 v[22:25], v143 offset:33792
	ds_read_b128 v[194:197], v143 offset:34816
	ds_read_b128 v[202:205], v143 offset:35840
	ds_read_b128 v[188:191], v143 offset:36864
	ds_read_b128 v[206:209], v143 offset:37888
	ds_read_b128 v[198:201], v143 offset:38912
	ds_read_b128 v[226:229], v143 offset:39936
	s_nop 0
	global_load_lds_dwordx4 v137, s[66:67]
	s_mov_b32 m0, s21
	s_nop 0
	global_load_lds_dwordx4 v139, s[66:67]
	s_waitcnt vmcnt(8)
	s_waitcnt lgkmcnt(0)
	s_setprio 1
	s_barrier
	v_mfma_f32_16x16x32_bf16 v[54:57], v[6:9], v[18:21], v[66:69]
	v_mfma_f32_16x16x32_bf16 v[118:121], v[26:29], v[22:25], v[54:57]
	v_mfma_f32_16x16x32_bf16 v[54:57], v[30:33], v[18:21], v[70:73]
	v_mfma_f32_16x16x32_bf16 v[114:117], v[222:225], v[22:25], v[54:57]
	v_mfma_f32_16x16x32_bf16 v[54:57], v[6:9], v[194:197], v[74:77]
	v_mfma_f32_16x16x32_bf16 v[102:105], v[26:29], v[202:205], v[54:57]
	v_mfma_f32_16x16x32_bf16 v[54:57], v[30:33], v[194:197], v[78:81]
	v_mfma_f32_16x16x32_bf16 v[98:101], v[222:225], v[202:205], v[54:57]
	v_mfma_f32_16x16x32_bf16 v[54:57], v[6:9], v[188:191], v[82:85]
	v_mfma_f32_16x16x32_bf16 v[86:89], v[26:29], v[206:209], v[54:57]
	v_mfma_f32_16x16x32_bf16 v[54:57], v[30:33], v[188:191], v[90:93]
	v_mfma_f32_16x16x32_bf16 v[82:85], v[222:225], v[206:209], v[54:57]
	v_mfma_f32_16x16x32_bf16 v[54:57], v[6:9], v[198:201], v[94:97]
	v_mfma_f32_16x16x32_bf16 v[62:65], v[26:29], v[226:229], v[54:57]
	v_mfma_f32_16x16x32_bf16 v[54:57], v[30:33], v[198:201], v[106:109]
	v_mfma_f32_16x16x32_bf16 v[54:57], v[222:225], v[226:229], v[54:57]
	s_setprio 0
	s_setprio 1
	v_mfma_f32_16x16x32_bf16 v[66:69], v[236:239], v[18:21], v[110:113]
	v_mfma_f32_16x16x32_bf16 v[18:21], v[244:247], v[18:21], v[34:37]
	v_mfma_f32_16x16x32_bf16 v[122:125], v[232:235], v[22:25], v[18:21]
	v_mfma_f32_16x16x32_bf16 v[18:21], v[236:239], v[194:197], v[38:41]
	v_mfma_f32_16x16x32_bf16 v[110:113], v[240:243], v[202:205], v[18:21]
	v_mfma_f32_16x16x32_bf16 v[18:21], v[244:247], v[194:197], v[42:45]
	v_mfma_f32_16x16x32_bf16 v[106:109], v[232:235], v[202:205], v[18:21]
	v_mfma_f32_16x16x32_bf16 v[18:21], v[236:239], v[188:191], v[46:49]
	v_mfma_f32_16x16x32_bf16 v[94:97], v[240:243], v[206:209], v[18:21]
	v_mfma_f32_16x16x32_bf16 v[18:21], v[244:247], v[188:191], v[50:53]
	v_mfma_f32_16x16x32_bf16 v[90:93], v[232:235], v[206:209], v[18:21]
	v_mfma_f32_16x16x32_bf16 v[18:21], v[236:239], v[198:201], v[144:147]
	v_mfma_f32_16x16x32_bf16 v[78:81], v[240:243], v[226:229], v[18:21]
	v_mfma_f32_16x16x32_bf16 v[18:21], v[244:247], v[198:201], v[58:61]
	v_mfma_f32_16x16x32_bf16 v[126:129], v[240:243], v[22:25], v[66:69]
	v_mfma_f32_16x16x32_bf16 v[70:73], v[232:235], v[226:229], v[18:21]
	s_barrier
	s_setprio 0
	s_add_i32 s66, s86, s14
	s_add_i32 s67, s66, 0x2000
	s_mov_b32 m0, s66
	s_add_u32 s62, s62, 0xc000
	ds_read_b128 v[42:45], v143 offset:49152
	ds_read_b128 v[46:49], v143 offset:50176
	ds_read_b128 v[144:147], v143 offset:51200
	ds_read_b128 v[188:191], v143 offset:52224
	ds_read_b128 v[194:197], v143 offset:53248
	ds_read_b128 v[198:201], v143 offset:54272
	ds_read_b128 v[202:205], v143 offset:55296
	ds_read_b128 v[206:209], v143 offset:56320
	s_addc_u32 s63, s63, 0
	global_load_lds_dwordx4 v138, s[64:65]
	s_mov_b32 m0, s67
	s_add_i32 s86, s87, s14
	s_add_i32 s87, s86, 0x2000
	global_load_lds_dwordx4 v140, s[64:65]
	s_mov_b32 m0, s86
	s_nop 0
	global_load_lds_dwordx4 v138, s[62:63]
	s_mov_b32 m0, s87
	s_nop 0
	global_load_lds_dwordx4 v140, s[62:63]
	s_mov_b32 m0, s69
	s_nop 0
	global_load_lds_dwordx4 v137, s[60:61]
	s_mov_b32 m0, s70
	s_nop 0
	global_load_lds_dwordx4 v139, s[60:61]
	s_waitcnt vmcnt(8)
	s_waitcnt lgkmcnt(0)
	s_setprio 1
	s_barrier
	v_mfma_f32_16x16x32_bf16 v[18:21], v[6:9], v[42:45], v[148:151]
	v_mfma_f32_16x16x32_bf16 v[58:61], v[26:29], v[46:49], v[18:21]
	v_mfma_f32_16x16x32_bf16 v[18:21], v[30:33], v[42:45], v[152:155]
	v_mfma_f32_16x16x32_bf16 v[50:53], v[222:225], v[46:49], v[18:21]
	v_mfma_f32_16x16x32_bf16 v[18:21], v[6:9], v[144:147], v[156:159]
	v_mfma_f32_16x16x32_bf16 v[38:41], v[26:29], v[188:191], v[18:21]
	v_mfma_f32_16x16x32_bf16 v[18:21], v[30:33], v[144:147], v[160:163]
	v_mfma_f32_16x16x32_bf16 v[34:37], v[222:225], v[188:191], v[18:21]
	v_mfma_f32_16x16x32_bf16 v[18:21], v[6:9], v[194:197], v[164:167]
	v_mfma_f32_16x16x32_bf16 v[2:5], v[6:9], v[202:205], v[2:5]
	v_mfma_f32_16x16x32_bf16 v[22:25], v[26:29], v[198:201], v[18:21]
	v_mfma_f32_16x16x32_bf16 v[18:21], v[30:33], v[194:197], v[168:171]
	v_mfma_f32_16x16x32_bf16 v[6:9], v[26:29], v[206:209], v[2:5]
	v_mfma_f32_16x16x32_bf16 v[2:5], v[30:33], v[202:205], v[10:13]
	v_mfma_f32_16x16x32_bf16 v[18:21], v[222:225], v[198:201], v[18:21]
	v_mfma_f32_16x16x32_bf16 v[2:5], v[222:225], v[206:209], v[2:5]
	s_setprio 0
	s_setprio 1
	v_mfma_f32_16x16x32_bf16 v[10:13], v[236:239], v[42:45], v[14:17]
	v_mfma_f32_16x16x32_bf16 v[74:77], v[240:243], v[46:49], v[10:13]
	v_mfma_f32_16x16x32_bf16 v[10:13], v[244:247], v[42:45], v[172:175]
	v_mfma_f32_16x16x32_bf16 v[66:69], v[232:235], v[46:49], v[10:13]
	v_mfma_f32_16x16x32_bf16 v[10:13], v[236:239], v[144:147], v[176:179]
	v_mfma_f32_16x16x32_bf16 v[46:49], v[240:243], v[188:191], v[10:13]
	v_mfma_f32_16x16x32_bf16 v[10:13], v[244:247], v[144:147], v[180:183]
	v_mfma_f32_16x16x32_bf16 v[42:45], v[232:235], v[188:191], v[10:13]
	v_mfma_f32_16x16x32_bf16 v[10:13], v[236:239], v[194:197], v[184:187]
	v_mfma_f32_16x16x32_bf16 v[30:33], v[240:243], v[198:201], v[10:13]
	v_mfma_f32_16x16x32_bf16 v[10:13], v[244:247], v[194:197], v[210:213]
	v_mfma_f32_16x16x32_bf16 v[26:29], v[232:235], v[198:201], v[10:13]
	v_mfma_f32_16x16x32_bf16 v[10:13], v[236:239], v[202:205], v[214:217]
	v_mfma_f32_16x16x32_bf16 v[14:17], v[240:243], v[206:209], v[10:13]
	v_mfma_f32_16x16x32_bf16 v[10:13], v[244:247], v[202:205], v[218:221]
	v_mfma_f32_16x16x32_bf16 v[10:13], v[232:235], v[206:209], v[10:13]
	s_barrier
	s_setprio 0
	s_andn2_b64 vcc, exec, s[44:45]
	s_cbranch_vccnz .LBB0_282
	s_lshl_b32 s60, s74, 10
	s_xor_b32 s88, s60, 0x400
	s_add_u32 s89, s58, 0x20000
	s_addc_u32 s90, s59, 0
	v_ashrrev_i32_e32 v131, 31, v130
	s_add_u32 s56, s56, 0x1c000
	v_lshl_add_u64 v[130:131], v[130:131], 3, s[26:27]
	s_addc_u32 s57, s57, 0
	s_mov_b32 s91, 4

.LBB0_280:
	s_or_b64 exec, exec, s[60:61]
	ds_read_b128 v[144:147], v132
	ds_read_b128 v[148:151], v132 offset:1024
	ds_read_b128 v[152:155], v132 offset:2048
	ds_read_b128 v[156:159], v132 offset:3072
	ds_read_b128 v[160:163], v133
	ds_read_b128 v[164:167], v133 offset:1024
	ds_read_b128 v[168:171], v133 offset:2048
	ds_read_b128 v[172:175], v133 offset:3072
	s_add_u32 s60, s56, 0x4000
	s_addc_u32 s61, s57, 0
	s_and_b64 s[58:59], s[58:59], exec
	s_cselect_b32 s64, s50, s60
	s_cselect_b32 s65, s51, s61
	s_cselect_b32 s61, s53, s90
	s_cselect_b32 s60, s52, s89
	s_add_u32 s58, s64, 0x8000
	s_addc_u32 s59, s65, 0
	s_add_u32 s62, s60, 0x8000
	s_addc_u32 s63, s61, 0
	s_mov_b32 m0, s80
	ds_read_b128 v[176:179], v143
	ds_read_b128 v[180:183], v143 offset:1024
	ds_read_b128 v[184:187], v143 offset:2048
	ds_read_b128 v[188:191], v143 offset:3072
	ds_read_b128 v[194:197], v143 offset:4096
	ds_read_b128 v[198:201], v143 offset:5120
	ds_read_b128 v[202:205], v143 offset:6144
	ds_read_b128 v[206:209], v143 offset:7168
	s_nop 0
	global_load_lds_dwordx4 v137, s[56:57]
	s_mov_b32 m0, s81
	s_nop 0
	global_load_lds_dwordx4 v139, s[56:57]
	s_waitcnt vmcnt(8)
	s_waitcnt lgkmcnt(0)
	s_setprio 1
	s_barrier
	v_mfma_f32_16x16x32_bf16 v[118:121], v[144:147], v[176:179], v[118:121]
	v_mfma_f32_16x16x32_bf16 v[114:117], v[152:155], v[176:179], v[114:117]
	v_mfma_f32_16x16x32_bf16 v[102:105], v[144:147], v[184:187], v[102:105]
	v_mfma_f32_16x16x32_bf16 v[98:101], v[152:155], v[184:187], v[98:101]
	v_mfma_f32_16x16x32_bf16 v[86:89], v[144:147], v[194:197], v[86:89]
	v_mfma_f32_16x16x32_bf16 v[82:85], v[152:155], v[194:197], v[82:85]
	v_mfma_f32_16x16x32_bf16 v[62:65], v[144:147], v[202:205], v[62:65]
	v_mfma_f32_16x16x32_bf16 v[54:57], v[152:155], v[202:205], v[54:57]
	v_mfma_f32_16x16x32_bf16 v[118:121], v[148:151], v[180:183], v[118:121]
	v_mfma_f32_16x16x32_bf16 v[114:117], v[156:159], v[180:183], v[114:117]
	v_mfma_f32_16x16x32_bf16 v[102:105], v[148:151], v[188:191], v[102:105]
	v_mfma_f32_16x16x32_bf16 v[98:101], v[156:159], v[188:191], v[98:101]
	v_mfma_f32_16x16x32_bf16 v[86:89], v[148:151], v[198:201], v[86:89]
	v_mfma_f32_16x16x32_bf16 v[82:85], v[156:159], v[198:201], v[82:85]
	v_mfma_f32_16x16x32_bf16 v[62:65], v[148:151], v[206:209], v[62:65]
	v_mfma_f32_16x16x32_bf16 v[54:57], v[156:159], v[206:209], v[54:57]
	s_setprio 0
	s_setprio 1
	v_mfma_f32_16x16x32_bf16 v[126:129], v[160:163], v[176:179], v[126:129]
	v_mfma_f32_16x16x32_bf16 v[122:125], v[168:171], v[176:179], v[122:125]
	v_mfma_f32_16x16x32_bf16 v[110:113], v[160:163], v[184:187], v[110:113]
	v_mfma_f32_16x16x32_bf16 v[106:109], v[168:171], v[184:187], v[106:109]
	v_mfma_f32_16x16x32_bf16 v[94:97], v[160:163], v[194:197], v[94:97]
	v_mfma_f32_16x16x32_bf16 v[90:93], v[168:171], v[194:197], v[90:93]
	v_mfma_f32_16x16x32_bf16 v[78:81], v[160:163], v[202:205], v[78:81]
	v_mfma_f32_16x16x32_bf16 v[70:73], v[168:171], v[202:205], v[70:73]
	v_mfma_f32_16x16x32_bf16 v[126:129], v[164:167], v[180:183], v[126:129]
	v_mfma_f32_16x16x32_bf16 v[122:125], v[172:175], v[180:183], v[122:125]
	v_mfma_f32_16x16x32_bf16 v[110:113], v[164:167], v[188:191], v[110:113]
	v_mfma_f32_16x16x32_bf16 v[106:109], v[172:175], v[188:191], v[106:109]
	v_mfma_f32_16x16x32_bf16 v[94:97], v[164:167], v[198:201], v[94:97]
	v_mfma_f32_16x16x32_bf16 v[90:93], v[172:175], v[198:201], v[90:93]
	v_mfma_f32_16x16x32_bf16 v[78:81], v[164:167], v[206:209], v[78:81]
	v_mfma_f32_16x16x32_bf16 v[70:73], v[172:175], v[206:209], v[70:73]
	s_barrier
	s_setprio 0
	s_mov_b32 m0, s82
	ds_read_b128 v[176:179], v143 offset:16384
	ds_read_b128 v[180:183], v143 offset:17408
	ds_read_b128 v[184:187], v143 offset:18432
	ds_read_b128 v[188:191], v143 offset:19456
	ds_read_b128 v[194:197], v143 offset:20480
	ds_read_b128 v[198:201], v143 offset:21504
	ds_read_b128 v[202:205], v143 offset:22528
	ds_read_b128 v[206:209], v143 offset:23552
	s_add_u32 s92, s60, 0x4000
	global_load_lds_dwordx4 v138, s[60:61]
	s_mov_b32 m0, s83
	s_addc_u32 s93, s61, 0
	global_load_lds_dwordx4 v140, s[60:61]
	s_mov_b32 m0, s84
	s_nop 0
	global_load_lds_dwordx4 v138, s[92:93]
	s_mov_b32 m0, s85
	s_nop 0
	global_load_lds_dwordx4 v140, s[92:93]
	s_mov_b32 m0, s15
	s_nop 0
	global_load_lds_dwordx4 v137, s[64:65]
	s_mov_b32 m0, s18
	s_nop 0
	global_load_lds_dwordx4 v139, s[64:65]
	s_waitcnt vmcnt(8)
	s_waitcnt lgkmcnt(0)
	s_setprio 1
	s_barrier
	v_mfma_f32_16x16x32_bf16 v[58:61], v[144:147], v[176:179], v[58:61]
	v_mfma_f32_16x16x32_bf16 v[50:53], v[152:155], v[176:179], v[50:53]
	v_mfma_f32_16x16x32_bf16 v[38:41], v[144:147], v[184:187], v[38:41]
	v_mfma_f32_16x16x32_bf16 v[34:37], v[152:155], v[184:187], v[34:37]
	v_mfma_f32_16x16x32_bf16 v[22:25], v[144:147], v[194:197], v[22:25]
	v_mfma_f32_16x16x32_bf16 v[18:21], v[152:155], v[194:197], v[18:21]
	v_mfma_f32_16x16x32_bf16 v[6:9], v[144:147], v[202:205], v[6:9]
	v_mfma_f32_16x16x32_bf16 v[2:5], v[152:155], v[202:205], v[2:5]
	v_mfma_f32_16x16x32_bf16 v[58:61], v[148:151], v[180:183], v[58:61]
	v_mfma_f32_16x16x32_bf16 v[50:53], v[156:159], v[180:183], v[50:53]
	v_mfma_f32_16x16x32_bf16 v[38:41], v[148:151], v[188:191], v[38:41]
	v_mfma_f32_16x16x32_bf16 v[34:37], v[156:159], v[188:191], v[34:37]
	v_mfma_f32_16x16x32_bf16 v[22:25], v[148:151], v[198:201], v[22:25]
	v_mfma_f32_16x16x32_bf16 v[18:21], v[156:159], v[198:201], v[18:21]
	v_mfma_f32_16x16x32_bf16 v[6:9], v[148:151], v[206:209], v[6:9]
	v_mfma_f32_16x16x32_bf16 v[2:5], v[156:159], v[206:209], v[2:5]
	s_setprio 0
	s_setprio 1
	v_mfma_f32_16x16x32_bf16 v[74:77], v[160:163], v[176:179], v[74:77]
	v_mfma_f32_16x16x32_bf16 v[66:69], v[168:171], v[176:179], v[66:69]
	v_mfma_f32_16x16x32_bf16 v[46:49], v[160:163], v[184:187], v[46:49]
	v_mfma_f32_16x16x32_bf16 v[42:45], v[168:171], v[184:187], v[42:45]
	v_mfma_f32_16x16x32_bf16 v[30:33], v[160:163], v[194:197], v[30:33]
	v_mfma_f32_16x16x32_bf16 v[26:29], v[168:171], v[194:197], v[26:29]
	v_mfma_f32_16x16x32_bf16 v[14:17], v[160:163], v[202:205], v[14:17]
	v_mfma_f32_16x16x32_bf16 v[10:13], v[168:171], v[202:205], v[10:13]
	v_mfma_f32_16x16x32_bf16 v[74:77], v[164:167], v[180:183], v[74:77]
	v_mfma_f32_16x16x32_bf16 v[66:69], v[172:175], v[180:183], v[66:69]
	v_mfma_f32_16x16x32_bf16 v[46:49], v[164:167], v[188:191], v[46:49]
	v_mfma_f32_16x16x32_bf16 v[42:45], v[172:175], v[188:191], v[42:45]
	v_mfma_f32_16x16x32_bf16 v[30:33], v[164:167], v[198:201], v[30:33]
	v_mfma_f32_16x16x32_bf16 v[26:29], v[172:175], v[198:201], v[26:29]
	v_mfma_f32_16x16x32_bf16 v[14:17], v[164:167], v[206:209], v[14:17]
	v_mfma_f32_16x16x32_bf16 v[10:13], v[172:175], v[206:209], v[10:13]
	s_barrier
	s_setprio 0
	ds_read_b128 v[144:147], v134
	ds_read_b128 v[148:151], v134 offset:1024
	ds_read_b128 v[152:155], v134 offset:2048
	ds_read_b128 v[156:159], v134 offset:3072
	ds_read_b128 v[160:163], v135
	ds_read_b128 v[164:167], v135 offset:1024
	ds_read_b128 v[168:171], v135 offset:2048
	ds_read_b128 v[172:175], v135 offset:3072
	s_add_u32 s64, s64, 0x4000
	s_addc_u32 s65, s65, 0
	s_mov_b32 m0, s20
	ds_read_b128 v[176:179], v143 offset:32768
	ds_read_b128 v[180:183], v143 offset:33792
	ds_read_b128 v[184:187], v143 offset:34816
	ds_read_b128 v[188:191], v143 offset:35840
	ds_read_b128 v[194:197], v143 offset:36864
	ds_read_b128 v[198:201], v143 offset:37888
	ds_read_b128 v[202:205], v143 offset:38912
	ds_read_b128 v[206:209], v143 offset:39936
	s_nop 0
	global_load_lds_dwordx4 v137, s[64:65]
	s_mov_b32 m0, s21
	s_nop 0
	global_load_lds_dwordx4 v139, s[64:65]
	s_waitcnt vmcnt(8)
	s_waitcnt lgkmcnt(0)
	s_setprio 1
	s_barrier
	v_mfma_f32_16x16x32_bf16 v[118:121], v[144:147], v[176:179], v[118:121]
	v_mfma_f32_16x16x32_bf16 v[114:117], v[152:155], v[176:179], v[114:117]
	v_mfma_f32_16x16x32_bf16 v[102:105], v[144:147], v[184:187], v[102:105]
	v_mfma_f32_16x16x32_bf16 v[98:101], v[152:155], v[184:187], v[98:101]
	v_mfma_f32_16x16x32_bf16 v[86:89], v[144:147], v[194:197], v[86:89]
	v_mfma_f32_16x16x32_bf16 v[82:85], v[152:155], v[194:197], v[82:85]
	v_mfma_f32_16x16x32_bf16 v[62:65], v[144:147], v[202:205], v[62:65]
	v_mfma_f32_16x16x32_bf16 v[54:57], v[152:155], v[202:205], v[54:57]
	v_mfma_f32_16x16x32_bf16 v[118:121], v[148:151], v[180:183], v[118:121]
	v_mfma_f32_16x16x32_bf16 v[114:117], v[156:159], v[180:183], v[114:117]
	v_mfma_f32_16x16x32_bf16 v[102:105], v[148:151], v[188:191], v[102:105]
	v_mfma_f32_16x16x32_bf16 v[98:101], v[156:159], v[188:191], v[98:101]
	v_mfma_f32_16x16x32_bf16 v[86:89], v[148:151], v[198:201], v[86:89]
	v_mfma_f32_16x16x32_bf16 v[82:85], v[156:159], v[198:201], v[82:85]
	v_mfma_f32_16x16x32_bf16 v[62:65], v[148:151], v[206:209], v[62:65]
	v_mfma_f32_16x16x32_bf16 v[54:57], v[156:159], v[206:209], v[54:57]
	s_setprio 0
	s_setprio 1
	v_mfma_f32_16x16x32_bf16 v[126:129], v[160:163], v[176:179], v[126:129]
	v_mfma_f32_16x16x32_bf16 v[122:125], v[168:171], v[176:179], v[122:125]
	v_mfma_f32_16x16x32_bf16 v[110:113], v[160:163], v[184:187], v[110:113]
	v_mfma_f32_16x16x32_bf16 v[106:109], v[168:171], v[184:187], v[106:109]
	v_mfma_f32_16x16x32_bf16 v[94:97], v[160:163], v[194:197], v[94:97]
	v_mfma_f32_16x16x32_bf16 v[90:93], v[168:171], v[194:197], v[90:93]
	v_mfma_f32_16x16x32_bf16 v[78:81], v[160:163], v[202:205], v[78:81]
	v_mfma_f32_16x16x32_bf16 v[70:73], v[168:171], v[202:205], v[70:73]
	v_mfma_f32_16x16x32_bf16 v[126:129], v[164:167], v[180:183], v[126:129]
	v_mfma_f32_16x16x32_bf16 v[122:125], v[172:175], v[180:183], v[122:125]
	v_mfma_f32_16x16x32_bf16 v[110:113], v[164:167], v[188:191], v[110:113]
	v_mfma_f32_16x16x32_bf16 v[106:109], v[172:175], v[188:191], v[106:109]
	v_mfma_f32_16x16x32_bf16 v[94:97], v[164:167], v[198:201], v[94:97]
	v_mfma_f32_16x16x32_bf16 v[90:93], v[172:175], v[198:201], v[90:93]
	v_mfma_f32_16x16x32_bf16 v[78:81], v[164:167], v[206:209], v[78:81]
	v_mfma_f32_16x16x32_bf16 v[70:73], v[172:175], v[206:209], v[70:73]
	s_barrier
	s_setprio 0
	s_mov_b32 m0, s66
	ds_read_b128 v[176:179], v143 offset:49152
	ds_read_b128 v[180:183], v143 offset:50176
	ds_read_b128 v[184:187], v143 offset:51200
	ds_read_b128 v[188:191], v143 offset:52224
	ds_read_b128 v[194:197], v143 offset:53248
	ds_read_b128 v[198:201], v143 offset:54272
	ds_read_b128 v[202:205], v143 offset:55296
	ds_read_b128 v[206:209], v143 offset:56320
	s_add_u32 s60, s60, 0xc000
	global_load_lds_dwordx4 v138, s[62:63]
	s_mov_b32 m0, s67
	s_addc_u32 s61, s61, 0
	global_load_lds_dwordx4 v140, s[62:63]
	s_mov_b32 m0, s86
	s_nop 0
	global_load_lds_dwordx4 v138, s[60:61]
	s_mov_b32 m0, s87
	s_nop 0
	global_load_lds_dwordx4 v140, s[60:61]
	s_mov_b32 m0, s69
	s_nop 0
	global_load_lds_dwordx4 v137, s[58:59]
	s_mov_b32 m0, s70
	s_nop 0
	global_load_lds_dwordx4 v139, s[58:59]
	s_waitcnt vmcnt(8)
	s_waitcnt lgkmcnt(0)
	s_setprio 1
	s_barrier
	v_mfma_f32_16x16x32_bf16 v[58:61], v[144:147], v[176:179], v[58:61]
	v_mfma_f32_16x16x32_bf16 v[50:53], v[152:155], v[176:179], v[50:53]
	v_mfma_f32_16x16x32_bf16 v[38:41], v[144:147], v[184:187], v[38:41]
	v_mfma_f32_16x16x32_bf16 v[34:37], v[152:155], v[184:187], v[34:37]
	v_mfma_f32_16x16x32_bf16 v[22:25], v[144:147], v[194:197], v[22:25]
	v_mfma_f32_16x16x32_bf16 v[18:21], v[152:155], v[194:197], v[18:21]
	v_mfma_f32_16x16x32_bf16 v[6:9], v[144:147], v[202:205], v[6:9]
	v_mfma_f32_16x16x32_bf16 v[2:5], v[152:155], v[202:205], v[2:5]
	v_mfma_f32_16x16x32_bf16 v[58:61], v[148:151], v[180:183], v[58:61]
	v_mfma_f32_16x16x32_bf16 v[50:53], v[156:159], v[180:183], v[50:53]
	v_mfma_f32_16x16x32_bf16 v[38:41], v[148:151], v[188:191], v[38:41]
	v_mfma_f32_16x16x32_bf16 v[34:37], v[156:159], v[188:191], v[34:37]
	v_mfma_f32_16x16x32_bf16 v[22:25], v[148:151], v[198:201], v[22:25]
	v_mfma_f32_16x16x32_bf16 v[18:21], v[156:159], v[198:201], v[18:21]
	v_mfma_f32_16x16x32_bf16 v[6:9], v[148:151], v[206:209], v[6:9]
	v_mfma_f32_16x16x32_bf16 v[2:5], v[156:159], v[206:209], v[2:5]
	s_setprio 0
	s_setprio 1
	v_mfma_f32_16x16x32_bf16 v[74:77], v[160:163], v[176:179], v[74:77]
	v_mfma_f32_16x16x32_bf16 v[66:69], v[168:171], v[176:179], v[66:69]
	v_mfma_f32_16x16x32_bf16 v[46:49], v[160:163], v[184:187], v[46:49]
	v_mfma_f32_16x16x32_bf16 v[42:45], v[168:171], v[184:187], v[42:45]
	v_mfma_f32_16x16x32_bf16 v[30:33], v[160:163], v[194:197], v[30:33]
	v_mfma_f32_16x16x32_bf16 v[26:29], v[168:171], v[194:197], v[26:29]
	v_mfma_f32_16x16x32_bf16 v[14:17], v[160:163], v[202:205], v[14:17]
	v_mfma_f32_16x16x32_bf16 v[10:13], v[168:171], v[202:205], v[10:13]
	v_mfma_f32_16x16x32_bf16 v[74:77], v[164:167], v[180:183], v[74:77]
	v_mfma_f32_16x16x32_bf16 v[66:69], v[172:175], v[180:183], v[66:69]
	v_mfma_f32_16x16x32_bf16 v[46:49], v[164:167], v[188:191], v[46:49]
	v_mfma_f32_16x16x32_bf16 v[42:45], v[172:175], v[188:191], v[42:45]
	v_mfma_f32_16x16x32_bf16 v[30:33], v[164:167], v[198:201], v[30:33]
	v_mfma_f32_16x16x32_bf16 v[26:29], v[172:175], v[198:201], v[26:29]
	v_mfma_f32_16x16x32_bf16 v[14:17], v[164:167], v[206:209], v[14:17]
	v_mfma_f32_16x16x32_bf16 v[10:13], v[172:175], v[206:209], v[10:13]
	s_barrier
	s_setprio 0
	s_add_i32 s58, s91, 2
	s_add_u32 s89, s89, 0x10000
	s_addc_u32 s90, s90, 0
	s_add_u32 s56, s56, 0x10000
	s_addc_u32 s57, s57, 0
	s_cmp_lt_i32 s91, s25
	s_cbranch_scc0 .LBB0_282
	s_mov_b32 s91, s58
	s_branch .LBB0_278

.LBB0_306:
	s_add_i32 s68, s50, 2
	s_add_u32 s48, s46, 0x100
	s_addc_u32 s49, s47, 0
	s_add_i32 s69, 0, 0x10000
	s_cmp_eq_u32 s60, s50
	s_cselect_b32 s51, s41, s49
	s_cselect_b32 s50, s40, s48
	v_add_u32_e32 v131, s69, v133
	s_cselect_b32 s53, s43, s67
	s_cselect_b32 s52, s42, s45
	s_add_i32 s70, 0, 0x14000
	ds_read_b128 v[138:141], v131
	ds_read_b128 v[142:145], v131 offset:1024
	ds_read_b128 v[146:149], v131 offset:2048
	ds_read_b128 v[150:153], v131 offset:3072
	v_add_u32_e32 v131, s70, v133
	ds_read_b128 v[154:157], v131
	ds_read_b128 v[158:161], v131 offset:1024
	ds_read_b128 v[162:165], v131 offset:2048
	ds_read_b128 v[166:169], v131 offset:3072
	s_add_u32 s46, s46, s61
	s_addc_u32 s47, s47, s62
	s_add_i32 m0, s15, 0xc000
	ds_read_b128 v[170:173], v136
	ds_read_b128 v[174:177], v136 offset:1024
	ds_read_b128 v[178:181], v136 offset:2048
	ds_read_b128 v[182:185], v136 offset:3072
	ds_read_b128 v[186:189], v136 offset:4096
	ds_read_b128 v[194:197], v136 offset:5120
	ds_read_b128 v[198:201], v136 offset:6144
	ds_read_b128 v[202:205], v136 offset:7168
	s_nop 0
	global_load_lds_dwordx4 v0, s[46:47]
	s_add_i32 m0, s15, 0xe000
	s_nop 0
	global_load_lds_dwordx4 v130, s[46:47]
	s_waitcnt vmcnt(8)
	s_waitcnt lgkmcnt(0)
	s_setprio 1
	s_barrier
	v_mfma_f32_16x16x32_bf16 v[126:129], v[138:141], v[170:173], v[126:129]
	v_mfma_f32_16x16x32_bf16 v[118:121], v[146:149], v[170:173], v[118:121]
	v_mfma_f32_16x16x32_bf16 v[110:113], v[138:141], v[178:181], v[110:113]
	v_mfma_f32_16x16x32_bf16 v[102:105], v[146:149], v[178:181], v[102:105]
	v_mfma_f32_16x16x32_bf16 v[94:97], v[138:141], v[186:189], v[94:97]
	v_mfma_f32_16x16x32_bf16 v[86:89], v[146:149], v[186:189], v[86:89]
	v_mfma_f32_16x16x32_bf16 v[78:81], v[138:141], v[198:201], v[78:81]
	v_mfma_f32_16x16x32_bf16 v[70:73], v[146:149], v[198:201], v[70:73]
	v_mfma_f32_16x16x32_bf16 v[126:129], v[142:145], v[174:177], v[126:129]
	v_mfma_f32_16x16x32_bf16 v[118:121], v[150:153], v[174:177], v[118:121]
	v_mfma_f32_16x16x32_bf16 v[110:113], v[142:145], v[182:185], v[110:113]
	v_mfma_f32_16x16x32_bf16 v[102:105], v[150:153], v[182:185], v[102:105]
	v_mfma_f32_16x16x32_bf16 v[94:97], v[142:145], v[194:197], v[94:97]
	v_mfma_f32_16x16x32_bf16 v[86:89], v[150:153], v[194:197], v[86:89]
	v_mfma_f32_16x16x32_bf16 v[78:81], v[142:145], v[202:205], v[78:81]
	v_mfma_f32_16x16x32_bf16 v[70:73], v[150:153], v[202:205], v[70:73]
	s_setprio 0
	s_setprio 1
	v_mfma_f32_16x16x32_bf16 v[54:57], v[154:157], v[170:173], v[54:57]
	v_mfma_f32_16x16x32_bf16 v[46:49], v[162:165], v[170:173], v[46:49]
	v_mfma_f32_16x16x32_bf16 v[38:41], v[154:157], v[178:181], v[38:41]
	v_mfma_f32_16x16x32_bf16 v[30:33], v[162:165], v[178:181], v[30:33]
	v_mfma_f32_16x16x32_bf16 v[22:25], v[154:157], v[186:189], v[22:25]
	v_mfma_f32_16x16x32_bf16 v[14:17], v[162:165], v[186:189], v[14:17]
	v_mfma_f32_16x16x32_bf16 v[6:9], v[154:157], v[198:201], v[6:9]
	v_mfma_f32_16x16x32_bf16 v[2:5], v[162:165], v[198:201], v[2:5]
	v_mfma_f32_16x16x32_bf16 v[54:57], v[158:161], v[174:177], v[54:57]
	v_mfma_f32_16x16x32_bf16 v[46:49], v[166:169], v[174:177], v[46:49]
	v_mfma_f32_16x16x32_bf16 v[38:41], v[158:161], v[182:185], v[38:41]
	v_mfma_f32_16x16x32_bf16 v[30:33], v[166:169], v[182:185], v[30:33]
	v_mfma_f32_16x16x32_bf16 v[22:25], v[158:161], v[194:197], v[22:25]
	v_mfma_f32_16x16x32_bf16 v[14:17], v[166:169], v[194:197], v[14:17]
	v_mfma_f32_16x16x32_bf16 v[6:9], v[158:161], v[202:205], v[6:9]
	v_mfma_f32_16x16x32_bf16 v[2:5], v[166:169], v[202:205], v[2:5]
	s_barrier
	s_setprio 0
	s_add_i32 s46, s69, s14
	s_mov_b32 m0, s46
	ds_read_b128 v[170:173], v136 offset:16384
	ds_read_b128 v[174:177], v136 offset:17408
	ds_read_b128 v[178:181], v136 offset:18432
	ds_read_b128 v[182:185], v136 offset:19456
	ds_read_b128 v[186:189], v136 offset:20480
	ds_read_b128 v[194:197], v136 offset:21504
	ds_read_b128 v[198:201], v136 offset:22528
	ds_read_b128 v[202:205], v136 offset:23552
	s_nop 0
	global_load_lds_dwordx4 v135, s[52:53]
	s_add_i32 m0, s46, 0x2000
	s_add_u32 s46, s52, 0x4000
	s_addc_u32 s47, s53, 0
	s_add_i32 s69, s70, s14
	s_nop 0
	global_load_lds_dwordx4 v134, s[52:53]
	s_mov_b32 m0, s69
	s_nop 0
	global_load_lds_dwordx4 v135, s[46:47]
	s_add_i32 m0, s69, 0x2000
	s_nop 0
	global_load_lds_dwordx4 v134, s[46:47]
	s_mov_b32 m0, s15
	s_nop 0
	global_load_lds_dwordx4 v0, s[50:51]
	s_mov_b32 m0, s18
	s_nop 0
	global_load_lds_dwordx4 v130, s[50:51]
	s_waitcnt vmcnt(8)
	s_waitcnt lgkmcnt(0)
	s_setprio 1
	s_barrier
	v_mfma_f32_16x16x32_bf16 v[122:125], v[138:141], v[170:173], v[122:125]
	v_mfma_f32_16x16x32_bf16 v[114:117], v[146:149], v[170:173], v[114:117]
	v_mfma_f32_16x16x32_bf16 v[106:109], v[138:141], v[178:181], v[106:109]
	v_mfma_f32_16x16x32_bf16 v[98:101], v[146:149], v[178:181], v[98:101]
	v_mfma_f32_16x16x32_bf16 v[90:93], v[138:141], v[186:189], v[90:93]
	v_mfma_f32_16x16x32_bf16 v[82:85], v[146:149], v[186:189], v[82:85]
	v_mfma_f32_16x16x32_bf16 v[74:77], v[138:141], v[198:201], v[74:77]
	v_mfma_f32_16x16x32_bf16 v[66:69], v[146:149], v[198:201], v[66:69]
	v_mfma_f32_16x16x32_bf16 v[122:125], v[142:145], v[174:177], v[122:125]
	v_mfma_f32_16x16x32_bf16 v[114:117], v[150:153], v[174:177], v[114:117]
	v_mfma_f32_16x16x32_bf16 v[106:109], v[142:145], v[182:185], v[106:109]
	v_mfma_f32_16x16x32_bf16 v[98:101], v[150:153], v[182:185], v[98:101]
	v_mfma_f32_16x16x32_bf16 v[90:93], v[142:145], v[194:197], v[90:93]
	v_mfma_f32_16x16x32_bf16 v[82:85], v[150:153], v[194:197], v[82:85]
	v_mfma_f32_16x16x32_bf16 v[74:77], v[142:145], v[202:205], v[74:77]
	v_mfma_f32_16x16x32_bf16 v[66:69], v[150:153], v[202:205], v[66:69]
	s_setprio 0
	s_setprio 1
	v_mfma_f32_16x16x32_bf16 v[50:53], v[154:157], v[170:173], v[50:53]
	v_mfma_f32_16x16x32_bf16 v[42:45], v[162:165], v[170:173], v[42:45]
	v_mfma_f32_16x16x32_bf16 v[34:37], v[154:157], v[178:181], v[34:37]
	v_mfma_f32_16x16x32_bf16 v[26:29], v[162:165], v[178:181], v[26:29]
	v_mfma_f32_16x16x32_bf16 v[18:21], v[154:157], v[186:189], v[18:21]
	v_mfma_f32_16x16x32_bf16 v[10:13], v[162:165], v[186:189], v[10:13]
	v_mfma_f32_16x16x32_bf16 v[58:61], v[154:157], v[198:201], v[58:61]
	v_mfma_f32_16x16x32_bf16 v[62:65], v[162:165], v[198:201], v[62:65]
	v_mfma_f32_16x16x32_bf16 v[50:53], v[158:161], v[174:177], v[50:53]
	v_mfma_f32_16x16x32_bf16 v[42:45], v[166:169], v[174:177], v[42:45]
	v_mfma_f32_16x16x32_bf16 v[34:37], v[158:161], v[182:185], v[34:37]
	v_mfma_f32_16x16x32_bf16 v[26:29], v[166:169], v[182:185], v[26:29]
	v_mfma_f32_16x16x32_bf16 v[18:21], v[158:161], v[194:197], v[18:21]
	v_mfma_f32_16x16x32_bf16 v[10:13], v[166:169], v[194:197], v[10:13]
	v_mfma_f32_16x16x32_bf16 v[58:61], v[158:161], v[202:205], v[58:61]
	v_mfma_f32_16x16x32_bf16 v[62:65], v[166:169], v[202:205], v[62:65]
	s_barrier
	s_setprio 0
	s_add_i32 s69, 0, 0x18000
	v_add_u32_e32 v131, s69, v133
	s_add_i32 s70, 0, 0x1c000
	ds_read_b128 v[138:141], v131
	ds_read_b128 v[142:145], v131 offset:1024
	ds_read_b128 v[146:149], v131 offset:2048
	ds_read_b128 v[150:153], v131 offset:3072
	v_add_u32_e32 v131, s70, v133
	ds_read_b128 v[154:157], v131
	ds_read_b128 v[158:161], v131 offset:1024
	ds_read_b128 v[162:165], v131 offset:2048
	ds_read_b128 v[166:169], v131 offset:3072
	s_add_u32 s46, s50, s26
	s_addc_u32 s47, s51, s27
	s_mov_b32 m0, s20
	ds_read_b128 v[170:173], v136 offset:32768
	ds_read_b128 v[174:177], v136 offset:33792
	ds_read_b128 v[178:181], v136 offset:34816
	ds_read_b128 v[182:185], v136 offset:35840
	ds_read_b128 v[186:189], v136 offset:36864
	ds_read_b128 v[194:197], v136 offset:37888
	ds_read_b128 v[198:201], v136 offset:38912
	ds_read_b128 v[202:205], v136 offset:39936
	s_nop 0
	global_load_lds_dwordx4 v0, s[46:47]
	s_mov_b32 m0, s21
	s_nop 0
	global_load_lds_dwordx4 v130, s[46:47]
	s_waitcnt vmcnt(8)
	s_waitcnt lgkmcnt(0)
	s_setprio 1
	s_barrier
	v_mfma_f32_16x16x32_bf16 v[126:129], v[138:141], v[170:173], v[126:129]
	v_mfma_f32_16x16x32_bf16 v[118:121], v[146:149], v[170:173], v[118:121]
	v_mfma_f32_16x16x32_bf16 v[110:113], v[138:141], v[178:181], v[110:113]
	v_mfma_f32_16x16x32_bf16 v[102:105], v[146:149], v[178:181], v[102:105]
	v_mfma_f32_16x16x32_bf16 v[94:97], v[138:141], v[186:189], v[94:97]
	v_mfma_f32_16x16x32_bf16 v[86:89], v[146:149], v[186:189], v[86:89]
	v_mfma_f32_16x16x32_bf16 v[78:81], v[138:141], v[198:201], v[78:81]
	v_mfma_f32_16x16x32_bf16 v[70:73], v[146:149], v[198:201], v[70:73]
	v_mfma_f32_16x16x32_bf16 v[126:129], v[142:145], v[174:177], v[126:129]
	v_mfma_f32_16x16x32_bf16 v[118:121], v[150:153], v[174:177], v[118:121]
	v_mfma_f32_16x16x32_bf16 v[110:113], v[142:145], v[182:185], v[110:113]
	v_mfma_f32_16x16x32_bf16 v[102:105], v[150:153], v[182:185], v[102:105]
	v_mfma_f32_16x16x32_bf16 v[94:97], v[142:145], v[194:197], v[94:97]
	v_mfma_f32_16x16x32_bf16 v[86:89], v[150:153], v[194:197], v[86:89]
	v_mfma_f32_16x16x32_bf16 v[78:81], v[142:145], v[202:205], v[78:81]
	v_mfma_f32_16x16x32_bf16 v[70:73], v[150:153], v[202:205], v[70:73]
	s_setprio 0
	s_setprio 1
	v_mfma_f32_16x16x32_bf16 v[54:57], v[154:157], v[170:173], v[54:57]
	v_mfma_f32_16x16x32_bf16 v[46:49], v[162:165], v[170:173], v[46:49]
	v_mfma_f32_16x16x32_bf16 v[38:41], v[154:157], v[178:181], v[38:41]
	v_mfma_f32_16x16x32_bf16 v[30:33], v[162:165], v[178:181], v[30:33]
	v_mfma_f32_16x16x32_bf16 v[22:25], v[154:157], v[186:189], v[22:25]
	v_mfma_f32_16x16x32_bf16 v[14:17], v[162:165], v[186:189], v[14:17]
	v_mfma_f32_16x16x32_bf16 v[6:9], v[154:157], v[198:201], v[6:9]
	v_mfma_f32_16x16x32_bf16 v[2:5], v[162:165], v[198:201], v[2:5]
	v_mfma_f32_16x16x32_bf16 v[54:57], v[158:161], v[174:177], v[54:57]
	v_mfma_f32_16x16x32_bf16 v[46:49], v[166:169], v[174:177], v[46:49]
	v_mfma_f32_16x16x32_bf16 v[38:41], v[158:161], v[182:185], v[38:41]
	v_mfma_f32_16x16x32_bf16 v[30:33], v[166:169], v[182:185], v[30:33]
	v_mfma_f32_16x16x32_bf16 v[22:25], v[158:161], v[194:197], v[22:25]
	v_mfma_f32_16x16x32_bf16 v[14:17], v[166:169], v[194:197], v[14:17]
	v_mfma_f32_16x16x32_bf16 v[6:9], v[158:161], v[202:205], v[6:9]
	v_mfma_f32_16x16x32_bf16 v[2:5], v[166:169], v[202:205], v[2:5]
	s_barrier
	s_setprio 0
	s_add_u32 s46, s52, 0x8000
	s_addc_u32 s47, s53, 0
	s_add_i32 s69, s69, s14
	s_mov_b32 m0, s69
	ds_read_b128 v[170:173], v136 offset:49152
	ds_read_b128 v[174:177], v136 offset:50176
	ds_read_b128 v[178:181], v136 offset:51200
	ds_read_b128 v[182:185], v136 offset:52224
	ds_read_b128 v[186:189], v136 offset:53248
	ds_read_b128 v[194:197], v136 offset:54272
	ds_read_b128 v[198:201], v136 offset:55296
	ds_read_b128 v[202:205], v136 offset:56320
	v_mov_b32_e32 v131, v1
	global_load_lds_dwordx4 v135, s[46:47]
	s_add_i32 m0, s69, 0x2000
	s_nop 0
	global_load_lds_dwordx4 v134, s[46:47]
	s_add_u32 s46, s52, 0xc000
	s_addc_u32 s47, s53, 0
	s_add_i32 s52, s70, s14
	s_mov_b32 m0, s52
	s_nop 0
	global_load_lds_dwordx4 v135, s[46:47]
	s_add_i32 m0, s52, 0x2000
	s_nop 0
	global_load_lds_dwordx4 v134, s[46:47]
	s_mov_b32 m0, s58
	v_lshl_add_u64 v[190:191], s[50:51], 0, v[0:1]
	v_lshl_add_u64 v[190:191], v[190:191], 0, s[16:17]
	global_load_lds_dwordx4 v[190:191], off
	s_mov_b32 m0, s59
	v_lshl_add_u64 v[190:191], s[50:51], 0, v[130:131]
	v_lshl_add_u64 v[190:191], v[190:191], 0, s[16:17]
	global_load_lds_dwordx4 v[190:191], off
	s_waitcnt vmcnt(8)
	s_waitcnt lgkmcnt(0)
	s_setprio 1
	s_barrier
	v_mfma_f32_16x16x32_bf16 v[122:125], v[138:141], v[170:173], v[122:125]
	v_mfma_f32_16x16x32_bf16 v[114:117], v[146:149], v[170:173], v[114:117]
	v_mfma_f32_16x16x32_bf16 v[106:109], v[138:141], v[178:181], v[106:109]
	v_mfma_f32_16x16x32_bf16 v[98:101], v[146:149], v[178:181], v[98:101]
	v_mfma_f32_16x16x32_bf16 v[90:93], v[138:141], v[186:189], v[90:93]
	v_mfma_f32_16x16x32_bf16 v[82:85], v[146:149], v[186:189], v[82:85]
	v_mfma_f32_16x16x32_bf16 v[74:77], v[138:141], v[198:201], v[74:77]
	v_mfma_f32_16x16x32_bf16 v[66:69], v[146:149], v[198:201], v[66:69]
	v_mfma_f32_16x16x32_bf16 v[122:125], v[142:145], v[174:177], v[122:125]
	v_mfma_f32_16x16x32_bf16 v[114:117], v[150:153], v[174:177], v[114:117]
	v_mfma_f32_16x16x32_bf16 v[106:109], v[142:145], v[182:185], v[106:109]
	v_mfma_f32_16x16x32_bf16 v[98:101], v[150:153], v[182:185], v[98:101]
	v_mfma_f32_16x16x32_bf16 v[90:93], v[142:145], v[194:197], v[90:93]
	v_mfma_f32_16x16x32_bf16 v[82:85], v[150:153], v[194:197], v[82:85]
	v_mfma_f32_16x16x32_bf16 v[74:77], v[142:145], v[202:205], v[74:77]
	v_mfma_f32_16x16x32_bf16 v[66:69], v[150:153], v[202:205], v[66:69]
	s_setprio 0
	s_setprio 1
	v_mfma_f32_16x16x32_bf16 v[50:53], v[154:157], v[170:173], v[50:53]
	v_mfma_f32_16x16x32_bf16 v[42:45], v[162:165], v[170:173], v[42:45]
	v_mfma_f32_16x16x32_bf16 v[34:37], v[154:157], v[178:181], v[34:37]
	v_mfma_f32_16x16x32_bf16 v[26:29], v[162:165], v[178:181], v[26:29]
	v_mfma_f32_16x16x32_bf16 v[18:21], v[154:157], v[186:189], v[18:21]
	v_mfma_f32_16x16x32_bf16 v[10:13], v[162:165], v[186:189], v[10:13]
	v_mfma_f32_16x16x32_bf16 v[58:61], v[154:157], v[198:201], v[58:61]
	v_mfma_f32_16x16x32_bf16 v[62:65], v[162:165], v[198:201], v[62:65]
	v_mfma_f32_16x16x32_bf16 v[50:53], v[158:161], v[174:177], v[50:53]
	v_mfma_f32_16x16x32_bf16 v[42:45], v[166:169], v[174:177], v[42:45]
	v_mfma_f32_16x16x32_bf16 v[34:37], v[158:161], v[182:185], v[34:37]
	v_mfma_f32_16x16x32_bf16 v[26:29], v[166:169], v[182:185], v[26:29]
	v_mfma_f32_16x16x32_bf16 v[18:21], v[158:161], v[194:197], v[18:21]
	v_mfma_f32_16x16x32_bf16 v[10:13], v[166:169], v[194:197], v[10:13]
	v_mfma_f32_16x16x32_bf16 v[58:61], v[158:161], v[202:205], v[58:61]
	v_mfma_f32_16x16x32_bf16 v[62:65], v[166:169], v[202:205], v[62:65]
	s_barrier
	s_setprio 0
	s_add_u32 s45, s45, 0x10000
	s_addc_u32 s67, s67, 0
	s_cmp_ge_i32 s68, s55
	s_mov_b64 s[46:47], s[48:49]
	s_mov_b32 s50, s68
	s_cbranch_scc0 .LBB0_306

.LBB0_379:
	s_add_u32 s34, s26, 0x10000
	s_addc_u32 s35, s27, 0
	s_and_b64 s[30:31], s[46:47], exec
	s_cselect_b32 s53, s43, s35
	s_cselect_b32 s52, s42, s34
	s_add_u32 s65, s28, 0x10000
	s_addc_u32 s66, s29, 0
	s_add_u32 s30, s52, 0x8000
	s_addc_u32 s31, s53, 0
	s_add_i32 s67, 0, 0x10000
	s_and_b64 s[34:35], s[46:47], exec
	s_cselect_b32 s35, s45, s66
	s_cselect_b32 s34, s44, s65
	s_add_i32 s70, 0, 0x14000
	v_add_u32_e32 v114, s67, v236
	v_add_u32_e32 v115, s70, v236
	ds_read_b128 v[2:5], v114
	s_waitcnt lgkmcnt(0)
	ds_read_b128 v[6:9], v114 offset:1024
	ds_read_b128 v[10:13], v114 offset:2048
	ds_read_b128 v[14:17], v114 offset:3072
	ds_read_b128 v[18:21], v115
	ds_read_b128 v[22:25], v115 offset:1024
	ds_read_b128 v[26:29], v115 offset:2048
	ds_read_b128 v[30:33], v115 offset:3072
	s_add_u32 s68, s26, 0xc000
	s_addc_u32 s69, s27, 0
	s_add_i32 s65, s20, 0xc000
	s_mov_b32 m0, s65
	s_add_i32 s66, s20, 0xe000
	ds_read_b128 v[34:37], v237
	ds_read_b128 v[38:41], v237 offset:1024
	ds_read_b128 v[42:45], v237 offset:2048
	ds_read_b128 v[46:49], v237 offset:3072
	ds_read_b128 v[50:53], v237 offset:4096
	ds_read_b128 v[54:57], v237 offset:5120
	ds_read_b128 v[58:61], v237 offset:6144
	ds_read_b128 v[62:65], v237 offset:7168
	s_nop 0
	global_load_lds_dwordx4 v235, s[68:69]
	s_mov_b32 m0, s66
	s_nop 0
	global_load_lds_dwordx4 v226, s[68:69]
	s_waitcnt vmcnt(8)
	s_waitcnt lgkmcnt(0)
	s_setprio 1
	s_barrier
	v_mfma_f32_16x16x32_bf16 v[90:93], v[2:5], v[58:61], 0
	v_mfma_f32_16x16x32_bf16 v[66:69], v[2:5], v[34:37], 0
	v_mfma_f32_16x16x32_bf16 v[70:73], v[10:13], v[34:37], 0
	v_mfma_f32_16x16x32_bf16 v[74:77], v[2:5], v[42:45], 0
	v_mfma_f32_16x16x32_bf16 v[78:81], v[10:13], v[42:45], 0
	v_mfma_f32_16x16x32_bf16 v[82:85], v[2:5], v[50:53], 0
	v_mfma_f32_16x16x32_bf16 v[86:89], v[10:13], v[50:53], 0
	v_mfma_f32_16x16x32_bf16 v[98:101], v[6:9], v[62:65], v[90:93]
	v_mfma_f32_16x16x32_bf16 v[90:93], v[10:13], v[58:61], 0
	v_mfma_f32_16x16x32_bf16 v[66:69], v[6:9], v[38:41], v[66:69]
	v_mfma_f32_16x16x32_bf16 v[70:73], v[14:17], v[38:41], v[70:73]
	v_mfma_f32_16x16x32_bf16 v[74:77], v[6:9], v[46:49], v[74:77]
	v_mfma_f32_16x16x32_bf16 v[78:81], v[14:17], v[46:49], v[78:81]
	v_mfma_f32_16x16x32_bf16 v[82:85], v[6:9], v[54:57], v[82:85]
	v_mfma_f32_16x16x32_bf16 v[86:89], v[14:17], v[54:57], v[86:89]
	v_mfma_f32_16x16x32_bf16 v[102:105], v[14:17], v[62:65], v[90:93]
	s_setprio 0
	s_setprio 1
	v_mfma_f32_16x16x32_bf16 v[90:93], v[18:21], v[34:37], 0
	v_mfma_f32_16x16x32_bf16 v[34:37], v[26:29], v[34:37], 0
	v_mfma_f32_16x16x32_bf16 v[118:121], v[22:25], v[38:41], v[90:93]
	v_mfma_f32_16x16x32_bf16 v[34:37], v[30:33], v[38:41], v[34:37]
	v_mfma_f32_16x16x32_bf16 v[38:41], v[18:21], v[42:45], 0
	v_mfma_f32_16x16x32_bf16 v[42:45], v[26:29], v[42:45], 0
	v_mfma_f32_16x16x32_bf16 v[38:41], v[22:25], v[46:49], v[38:41]
	v_mfma_f32_16x16x32_bf16 v[42:45], v[30:33], v[46:49], v[42:45]
	v_mfma_f32_16x16x32_bf16 v[46:49], v[18:21], v[50:53], 0
	v_mfma_f32_16x16x32_bf16 v[50:53], v[26:29], v[50:53], 0
	v_mfma_f32_16x16x32_bf16 v[46:49], v[22:25], v[54:57], v[46:49]
	v_mfma_f32_16x16x32_bf16 v[50:53], v[30:33], v[54:57], v[50:53]
	v_mfma_f32_16x16x32_bf16 v[54:57], v[18:21], v[58:61], 0
	v_mfma_f32_16x16x32_bf16 v[58:61], v[26:29], v[58:61], 0
	v_mfma_f32_16x16x32_bf16 v[54:57], v[22:25], v[62:65], v[54:57]
	v_mfma_f32_16x16x32_bf16 v[58:61], v[30:33], v[62:65], v[58:61]
	s_barrier
	s_setprio 0
	s_add_i32 s67, s67, s18
	s_add_i32 s68, s67, 0x2000
	s_mov_b32 m0, s67
	s_add_u32 s72, s34, 0x4000
	ds_read_b128 v[62:65], v237 offset:16384
	ds_read_b128 v[90:93], v237 offset:17408
	ds_read_b128 v[94:97], v237 offset:18432
	ds_read_b128 v[106:109], v237 offset:19456
	ds_read_b128 v[110:113], v237 offset:20480
	ds_read_b128 v[122:125], v237 offset:21504
	ds_read_b128 v[126:129], v237 offset:22528
	ds_read_b128 v[130:133], v237 offset:23552
	s_addc_u32 s73, s35, 0
	global_load_lds_dwordx4 v227, s[34:35]
	s_mov_b32 m0, s68
	s_add_i32 s69, s70, s18
	s_add_i32 s70, s69, 0x2000
	global_load_lds_dwordx4 v0, s[34:35]
	s_mov_b32 m0, s69
	s_nop 0
	global_load_lds_dwordx4 v227, s[72:73]
	s_mov_b32 m0, s70
	s_nop 0
	global_load_lds_dwordx4 v0, s[72:73]
	s_mov_b32 m0, s20
	s_nop 0
	global_load_lds_dwordx4 v235, s[52:53]
	s_mov_b32 m0, s25
	s_nop 0
	global_load_lds_dwordx4 v226, s[52:53]
	s_waitcnt vmcnt(8)
	s_waitcnt lgkmcnt(0)
	s_setprio 1
	s_barrier
	v_mfma_f32_16x16x32_bf16 v[134:137], v[2:5], v[62:65], 0
	v_mfma_f32_16x16x32_bf16 v[142:145], v[2:5], v[94:97], 0
	v_mfma_f32_16x16x32_bf16 v[150:153], v[2:5], v[110:113], 0
	v_mfma_f32_16x16x32_bf16 v[2:5], v[2:5], v[126:129], 0
	v_mfma_f32_16x16x32_bf16 v[134:137], v[6:9], v[90:93], v[134:137]
	v_mfma_f32_16x16x32_bf16 v[142:145], v[6:9], v[106:109], v[142:145]
	v_mfma_f32_16x16x32_bf16 v[150:153], v[6:9], v[122:125], v[150:153]
	v_mfma_f32_16x16x32_bf16 v[2:5], v[6:9], v[130:133], v[2:5]
	v_mfma_f32_16x16x32_bf16 v[6:9], v[10:13], v[126:129], 0
	v_mfma_f32_16x16x32_bf16 v[138:141], v[10:13], v[62:65], 0
	v_mfma_f32_16x16x32_bf16 v[146:149], v[10:13], v[94:97], 0
	v_mfma_f32_16x16x32_bf16 v[154:157], v[10:13], v[110:113], 0
	v_mfma_f32_16x16x32_bf16 v[6:9], v[14:17], v[130:133], v[6:9]
	v_mfma_f32_16x16x32_bf16 v[138:141], v[14:17], v[90:93], v[138:141]
	v_mfma_f32_16x16x32_bf16 v[146:149], v[14:17], v[106:109], v[146:149]
	v_mfma_f32_16x16x32_bf16 v[154:157], v[14:17], v[122:125], v[154:157]
	s_setprio 0
	s_setprio 1
	v_mfma_f32_16x16x32_bf16 v[10:13], v[18:21], v[62:65], 0
	v_mfma_f32_16x16x32_bf16 v[158:161], v[22:25], v[90:93], v[10:13]
	v_mfma_f32_16x16x32_bf16 v[10:13], v[26:29], v[62:65], 0
	v_mfma_f32_16x16x32_bf16 v[162:165], v[30:33], v[90:93], v[10:13]
	v_mfma_f32_16x16x32_bf16 v[10:13], v[18:21], v[94:97], 0
	v_mfma_f32_16x16x32_bf16 v[174:177], v[22:25], v[106:109], v[10:13]
	v_mfma_f32_16x16x32_bf16 v[10:13], v[26:29], v[94:97], 0
	v_mfma_f32_16x16x32_bf16 v[178:181], v[30:33], v[106:109], v[10:13]
	v_mfma_f32_16x16x32_bf16 v[10:13], v[18:21], v[110:113], 0
	v_mfma_f32_16x16x32_bf16 v[182:185], v[22:25], v[122:125], v[10:13]
	v_mfma_f32_16x16x32_bf16 v[10:13], v[26:29], v[110:113], 0
	v_mfma_f32_16x16x32_bf16 v[122:125], v[30:33], v[122:125], v[10:13]
	v_mfma_f32_16x16x32_bf16 v[10:13], v[18:21], v[126:129], 0
	v_mfma_f32_16x16x32_bf16 v[186:189], v[22:25], v[130:133], v[10:13]
	v_mfma_f32_16x16x32_bf16 v[10:13], v[26:29], v[126:129], 0
	v_mfma_f32_16x16x32_bf16 v[130:133], v[30:33], v[130:133], v[10:13]
	s_barrier
	s_setprio 0
	s_add_i32 s71, 0, 0x18000
	s_add_i32 s74, 0, 0x1c000
	v_add_u32_e32 v116, s71, v236
	v_add_u32_e32 v117, s74, v236
	s_nop 0
	ds_read_b128 v[10:13], v116
	ds_read_b128 v[14:17], v116 offset:1024
	ds_read_b128 v[18:21], v116 offset:2048
	ds_read_b128 v[22:25], v116 offset:3072
	ds_read_b128 v[194:197], v117
	ds_read_b128 v[198:201], v117 offset:1024
	ds_read_b128 v[202:205], v117 offset:2048
	ds_read_b128 v[206:209], v117 offset:3072
	s_add_u32 s52, s52, 0x4000
	s_addc_u32 s53, s53, 0
	s_mov_b32 m0, s54
	ds_read_b128 v[26:29], v237 offset:32768
	ds_read_b128 v[30:33], v237 offset:33792
	ds_read_b128 v[62:65], v237 offset:34816
	ds_read_b128 v[210:213], v237 offset:35840
	ds_read_b128 v[214:217], v237 offset:36864
	ds_read_b128 v[218:221], v237 offset:37888
	ds_read_b128 v[222:225], v237 offset:38912
	ds_read_b128 v[238:241], v237 offset:39936
	s_nop 0
	global_load_lds_dwordx4 v235, s[52:53]
	s_mov_b32 m0, s55
	s_nop 0
	global_load_lds_dwordx4 v226, s[52:53]
	s_waitcnt vmcnt(8)
	s_waitcnt lgkmcnt(0)
	s_setprio 1
	s_barrier
	v_mfma_f32_16x16x32_bf16 v[66:69], v[10:13], v[26:29], v[66:69]
	v_mfma_f32_16x16x32_bf16 v[166:169], v[14:17], v[30:33], v[66:69]
	v_mfma_f32_16x16x32_bf16 v[66:69], v[18:21], v[26:29], v[70:73]
	v_mfma_f32_16x16x32_bf16 v[170:173], v[22:25], v[30:33], v[66:69]
	v_mfma_f32_16x16x32_bf16 v[66:69], v[10:13], v[62:65], v[74:77]
	v_mfma_f32_16x16x32_bf16 v[110:113], v[14:17], v[210:213], v[66:69]
	v_mfma_f32_16x16x32_bf16 v[66:69], v[18:21], v[62:65], v[78:81]
	v_mfma_f32_16x16x32_bf16 v[106:109], v[22:25], v[210:213], v[66:69]
	v_mfma_f32_16x16x32_bf16 v[66:69], v[10:13], v[214:217], v[82:85]
	v_mfma_f32_16x16x32_bf16 v[94:97], v[14:17], v[218:221], v[66:69]
	v_mfma_f32_16x16x32_bf16 v[66:69], v[18:21], v[214:217], v[86:89]
	v_mfma_f32_16x16x32_bf16 v[90:93], v[22:25], v[218:221], v[66:69]
	v_mfma_f32_16x16x32_bf16 v[66:69], v[10:13], v[222:225], v[98:101]
	v_mfma_f32_16x16x32_bf16 v[78:81], v[14:17], v[238:241], v[66:69]
	v_mfma_f32_16x16x32_bf16 v[66:69], v[18:21], v[222:225], v[102:105]
	v_mfma_f32_16x16x32_bf16 v[70:73], v[22:25], v[238:241], v[66:69]
	s_setprio 0
	s_setprio 1
	v_mfma_f32_16x16x32_bf16 v[66:69], v[194:197], v[26:29], v[118:121]
	v_mfma_f32_16x16x32_bf16 v[26:29], v[202:205], v[26:29], v[34:37]
	v_mfma_f32_16x16x32_bf16 v[118:121], v[206:209], v[30:33], v[26:29]
	v_mfma_f32_16x16x32_bf16 v[26:29], v[194:197], v[62:65], v[38:41]
	v_mfma_f32_16x16x32_bf16 v[102:105], v[198:201], v[210:213], v[26:29]
	v_mfma_f32_16x16x32_bf16 v[26:29], v[202:205], v[62:65], v[42:45]
	v_mfma_f32_16x16x32_bf16 v[98:101], v[206:209], v[210:213], v[26:29]
	v_mfma_f32_16x16x32_bf16 v[26:29], v[194:197], v[214:217], v[46:49]
	v_mfma_f32_16x16x32_bf16 v[86:89], v[198:201], v[218:221], v[26:29]
	v_mfma_f32_16x16x32_bf16 v[26:29], v[202:205], v[214:217], v[50:53]
	v_mfma_f32_16x16x32_bf16 v[82:85], v[206:209], v[218:221], v[26:29]
	v_mfma_f32_16x16x32_bf16 v[26:29], v[194:197], v[222:225], v[54:57]
	v_mfma_f32_16x16x32_bf16 v[62:65], v[198:201], v[238:241], v[26:29]
	v_mfma_f32_16x16x32_bf16 v[26:29], v[202:205], v[222:225], v[58:61]
	v_mfma_f32_16x16x32_bf16 v[126:129], v[198:201], v[30:33], v[66:69]
	v_mfma_f32_16x16x32_bf16 v[54:57], v[206:209], v[238:241], v[26:29]
	s_barrier
	s_setprio 0
	s_add_u32 s72, s34, 0x8000
	s_addc_u32 s73, s35, 0
	s_add_i32 s52, s71, s18
	s_add_i32 s53, s52, 0x2000
	s_mov_b32 m0, s52
	s_add_u32 s34, s34, 0xc000
	ds_read_b128 v[34:37], v237 offset:49152
	ds_read_b128 v[38:41], v237 offset:50176
	ds_read_b128 v[210:213], v237 offset:51200
	ds_read_b128 v[214:217], v237 offset:52224
	ds_read_b128 v[218:221], v237 offset:53248
	ds_read_b128 v[222:225], v237 offset:54272
	ds_read_b128 v[238:241], v237 offset:55296
	ds_read_b128 v[242:245], v237 offset:56320
	s_addc_u32 s35, s35, 0
	global_load_lds_dwordx4 v227, s[72:73]
	s_mov_b32 m0, s53
	s_add_i32 s71, s74, s18
	s_nop 0
	global_load_lds_dwordx4 v0, s[72:73]
	s_mov_b32 m0, s71
	s_add_i32 s72, s71, 0x2000
	s_nop 0
	global_load_lds_dwordx4 v227, s[34:35]
	s_mov_b32 m0, s72
	s_nop 0
	global_load_lds_dwordx4 v0, s[34:35]
	s_mov_b32 m0, s58
	s_nop 0
	global_load_lds_dwordx4 v235, s[30:31]
	s_mov_b32 m0, s59
	s_nop 0
	global_load_lds_dwordx4 v226, s[30:31]
	s_waitcnt vmcnt(8)
	s_waitcnt lgkmcnt(0)
	s_setprio 1
	s_barrier
	v_mfma_f32_16x16x32_bf16 v[26:29], v[10:13], v[34:37], v[134:137]
	v_mfma_f32_16x16x32_bf16 v[74:77], v[14:17], v[38:41], v[26:29]
	v_mfma_f32_16x16x32_bf16 v[26:29], v[18:21], v[34:37], v[138:141]
	v_mfma_f32_16x16x32_bf16 v[66:69], v[22:25], v[38:41], v[26:29]
	v_mfma_f32_16x16x32_bf16 v[26:29], v[10:13], v[210:213], v[142:145]
	v_mfma_f32_16x16x32_bf16 v[46:49], v[14:17], v[214:217], v[26:29]
	v_mfma_f32_16x16x32_bf16 v[26:29], v[18:21], v[210:213], v[146:149]
	v_mfma_f32_16x16x32_bf16 v[42:45], v[22:25], v[214:217], v[26:29]
	v_mfma_f32_16x16x32_bf16 v[26:29], v[10:13], v[218:221], v[150:153]
	v_mfma_f32_16x16x32_bf16 v[2:5], v[10:13], v[238:241], v[2:5]
	v_mfma_f32_16x16x32_bf16 v[30:33], v[14:17], v[222:225], v[26:29]
	v_mfma_f32_16x16x32_bf16 v[26:29], v[18:21], v[218:221], v[154:157]
	v_mfma_f32_16x16x32_bf16 v[14:17], v[14:17], v[242:245], v[2:5]
	v_mfma_f32_16x16x32_bf16 v[2:5], v[18:21], v[238:241], v[6:9]
	v_mfma_f32_16x16x32_bf16 v[26:29], v[22:25], v[222:225], v[26:29]
	v_mfma_f32_16x16x32_bf16 v[10:13], v[22:25], v[242:245], v[2:5]
	s_setprio 0
	s_setprio 1
	v_mfma_f32_16x16x32_bf16 v[2:5], v[194:197], v[34:37], v[158:161]
	v_mfma_f32_16x16x32_bf16 v[58:61], v[198:201], v[38:41], v[2:5]
	v_mfma_f32_16x16x32_bf16 v[2:5], v[202:205], v[34:37], v[162:165]
	v_mfma_f32_16x16x32_bf16 v[50:53], v[206:209], v[38:41], v[2:5]
	v_mfma_f32_16x16x32_bf16 v[2:5], v[194:197], v[210:213], v[174:177]
	v_mfma_f32_16x16x32_bf16 v[38:41], v[198:201], v[214:217], v[2:5]
	v_mfma_f32_16x16x32_bf16 v[2:5], v[202:205], v[210:213], v[178:181]
	v_mfma_f32_16x16x32_bf16 v[34:37], v[206:209], v[214:217], v[2:5]
	v_mfma_f32_16x16x32_bf16 v[2:5], v[194:197], v[218:221], v[182:185]
	v_mfma_f32_16x16x32_bf16 v[22:25], v[198:201], v[222:225], v[2:5]
	v_mfma_f32_16x16x32_bf16 v[2:5], v[202:205], v[218:221], v[122:125]
	v_mfma_f32_16x16x32_bf16 v[18:21], v[206:209], v[222:225], v[2:5]
	v_mfma_f32_16x16x32_bf16 v[2:5], v[194:197], v[238:241], v[186:189]
	v_mfma_f32_16x16x32_bf16 v[6:9], v[198:201], v[242:245], v[2:5]
	v_mfma_f32_16x16x32_bf16 v[2:5], v[202:205], v[238:241], v[130:133]
	v_mfma_f32_16x16x32_bf16 v[2:5], v[206:209], v[242:245], v[2:5]
	s_barrier
	s_setprio 0
	s_andn2_b64 vcc, exec, s[48:49]
	s_cbranch_vccnz .LBB0_382
	s_add_u32 s73, s28, 0x20000
	s_addc_u32 s74, s29, 0
	s_add_u32 s26, s26, 0x1c000
	s_addc_u32 s27, s27, 0
	s_mov_b32 s75, 4
.LBB0_381:
	ds_read_b128 v[122:125], v114
	ds_read_b128 v[130:133], v114 offset:1024
	ds_read_b128 v[134:137], v114 offset:2048
	ds_read_b128 v[138:141], v114 offset:3072
	ds_read_b128 v[142:145], v115
	ds_read_b128 v[146:149], v115 offset:1024
	ds_read_b128 v[150:153], v115 offset:2048
	ds_read_b128 v[154:157], v115 offset:3072
	s_add_u32 s28, s26, 0x4000
	s_addc_u32 s29, s27, 0
	s_cmp_eq_u32 s56, s75
	s_cselect_b32 s34, s42, s28
	s_cselect_b32 s35, s43, s29
	s_cselect_b32 s30, s44, s73
	s_cselect_b32 s31, s45, s74
	s_add_u32 s28, s34, 0x8000
	s_addc_u32 s29, s35, 0
	s_mov_b32 m0, s65
	ds_read_b128 v[158:161], v237
	ds_read_b128 v[162:165], v237 offset:1024
	ds_read_b128 v[174:177], v237 offset:2048
	ds_read_b128 v[178:181], v237 offset:3072
	ds_read_b128 v[182:185], v237 offset:4096
	ds_read_b128 v[186:189], v237 offset:5120
	ds_read_b128 v[194:197], v237 offset:6144
	ds_read_b128 v[198:201], v237 offset:7168
	s_nop 0
	global_load_lds_dwordx4 v235, s[26:27]
	s_mov_b32 m0, s66
	s_nop 0
	global_load_lds_dwordx4 v226, s[26:27]
	s_waitcnt vmcnt(8)
	s_waitcnt lgkmcnt(0)
	s_setprio 1
	s_barrier
	v_mfma_f32_16x16x32_bf16 v[166:169], v[122:125], v[158:161], v[166:169]
	v_mfma_f32_16x16x32_bf16 v[170:173], v[134:137], v[158:161], v[170:173]
	v_mfma_f32_16x16x32_bf16 v[110:113], v[122:125], v[174:177], v[110:113]
	v_mfma_f32_16x16x32_bf16 v[106:109], v[134:137], v[174:177], v[106:109]
	v_mfma_f32_16x16x32_bf16 v[94:97], v[122:125], v[182:185], v[94:97]
	v_mfma_f32_16x16x32_bf16 v[90:93], v[134:137], v[182:185], v[90:93]
	v_mfma_f32_16x16x32_bf16 v[78:81], v[122:125], v[194:197], v[78:81]
	v_mfma_f32_16x16x32_bf16 v[70:73], v[134:137], v[194:197], v[70:73]
	v_mfma_f32_16x16x32_bf16 v[166:169], v[130:133], v[162:165], v[166:169]
	v_mfma_f32_16x16x32_bf16 v[170:173], v[138:141], v[162:165], v[170:173]
	v_mfma_f32_16x16x32_bf16 v[110:113], v[130:133], v[178:181], v[110:113]
	v_mfma_f32_16x16x32_bf16 v[106:109], v[138:141], v[178:181], v[106:109]
	v_mfma_f32_16x16x32_bf16 v[94:97], v[130:133], v[186:189], v[94:97]
	v_mfma_f32_16x16x32_bf16 v[90:93], v[138:141], v[186:189], v[90:93]
	v_mfma_f32_16x16x32_bf16 v[78:81], v[130:133], v[198:201], v[78:81]
	v_mfma_f32_16x16x32_bf16 v[70:73], v[138:141], v[198:201], v[70:73]
	s_setprio 0
	s_setprio 1
	v_mfma_f32_16x16x32_bf16 v[126:129], v[142:145], v[158:161], v[126:129]
	v_mfma_f32_16x16x32_bf16 v[118:121], v[150:153], v[158:161], v[118:121]
	v_mfma_f32_16x16x32_bf16 v[102:105], v[142:145], v[174:177], v[102:105]
	v_mfma_f32_16x16x32_bf16 v[98:101], v[150:153], v[174:177], v[98:101]
	v_mfma_f32_16x16x32_bf16 v[86:89], v[142:145], v[182:185], v[86:89]
	v_mfma_f32_16x16x32_bf16 v[82:85], v[150:153], v[182:185], v[82:85]
	v_mfma_f32_16x16x32_bf16 v[62:65], v[142:145], v[194:197], v[62:65]
	v_mfma_f32_16x16x32_bf16 v[54:57], v[150:153], v[194:197], v[54:57]
	v_mfma_f32_16x16x32_bf16 v[126:129], v[146:149], v[162:165], v[126:129]
	v_mfma_f32_16x16x32_bf16 v[118:121], v[154:157], v[162:165], v[118:121]
	v_mfma_f32_16x16x32_bf16 v[102:105], v[146:149], v[178:181], v[102:105]
	v_mfma_f32_16x16x32_bf16 v[98:101], v[154:157], v[178:181], v[98:101]
	v_mfma_f32_16x16x32_bf16 v[86:89], v[146:149], v[186:189], v[86:89]
	v_mfma_f32_16x16x32_bf16 v[82:85], v[154:157], v[186:189], v[82:85]
	v_mfma_f32_16x16x32_bf16 v[62:65], v[146:149], v[198:201], v[62:65]
	v_mfma_f32_16x16x32_bf16 v[54:57], v[154:157], v[198:201], v[54:57]
	s_barrier
	s_setprio 0
	s_mov_b32 m0, s67
	ds_read_b128 v[158:161], v237 offset:16384
	ds_read_b128 v[162:165], v237 offset:17408
	ds_read_b128 v[174:177], v237 offset:18432
	ds_read_b128 v[178:181], v237 offset:19456
	ds_read_b128 v[182:185], v237 offset:20480
	ds_read_b128 v[186:189], v237 offset:21504
	ds_read_b128 v[194:197], v237 offset:22528
	ds_read_b128 v[198:201], v237 offset:23552
	s_add_u32 s76, s30, 0x4000
	global_load_lds_dwordx4 v227, s[30:31]
	s_mov_b32 m0, s68
	s_addc_u32 s77, s31, 0
	global_load_lds_dwordx4 v0, s[30:31]
	s_mov_b32 m0, s69
	s_nop 0
	global_load_lds_dwordx4 v227, s[76:77]
	s_mov_b32 m0, s70
	s_nop 0
	global_load_lds_dwordx4 v0, s[76:77]
	s_mov_b32 m0, s20
	s_nop 0
	global_load_lds_dwordx4 v235, s[34:35]
	s_mov_b32 m0, s25
	s_nop 0
	global_load_lds_dwordx4 v226, s[34:35]
	s_waitcnt vmcnt(8)
	s_waitcnt lgkmcnt(0)
	s_setprio 1
	s_barrier
	v_mfma_f32_16x16x32_bf16 v[74:77], v[122:125], v[158:161], v[74:77]
	v_mfma_f32_16x16x32_bf16 v[66:69], v[134:137], v[158:161], v[66:69]
	v_mfma_f32_16x16x32_bf16 v[46:49], v[122:125], v[174:177], v[46:49]
	v_mfma_f32_16x16x32_bf16 v[42:45], v[134:137], v[174:177], v[42:45]
	v_mfma_f32_16x16x32_bf16 v[30:33], v[122:125], v[182:185], v[30:33]
	v_mfma_f32_16x16x32_bf16 v[26:29], v[134:137], v[182:185], v[26:29]
	v_mfma_f32_16x16x32_bf16 v[14:17], v[122:125], v[194:197], v[14:17]
	v_mfma_f32_16x16x32_bf16 v[10:13], v[134:137], v[194:197], v[10:13]
	v_mfma_f32_16x16x32_bf16 v[74:77], v[130:133], v[162:165], v[74:77]
	v_mfma_f32_16x16x32_bf16 v[66:69], v[138:141], v[162:165], v[66:69]
	v_mfma_f32_16x16x32_bf16 v[46:49], v[130:133], v[178:181], v[46:49]
	v_mfma_f32_16x16x32_bf16 v[42:45], v[138:141], v[178:181], v[42:45]
	v_mfma_f32_16x16x32_bf16 v[30:33], v[130:133], v[186:189], v[30:33]
	v_mfma_f32_16x16x32_bf16 v[26:29], v[138:141], v[186:189], v[26:29]
	v_mfma_f32_16x16x32_bf16 v[14:17], v[130:133], v[198:201], v[14:17]
	v_mfma_f32_16x16x32_bf16 v[10:13], v[138:141], v[198:201], v[10:13]
	s_setprio 0
	s_setprio 1
	v_mfma_f32_16x16x32_bf16 v[58:61], v[142:145], v[158:161], v[58:61]
	v_mfma_f32_16x16x32_bf16 v[50:53], v[150:153], v[158:161], v[50:53]
	v_mfma_f32_16x16x32_bf16 v[38:41], v[142:145], v[174:177], v[38:41]
	v_mfma_f32_16x16x32_bf16 v[34:37], v[150:153], v[174:177], v[34:37]
	v_mfma_f32_16x16x32_bf16 v[22:25], v[142:145], v[182:185], v[22:25]
	v_mfma_f32_16x16x32_bf16 v[18:21], v[150:153], v[182:185], v[18:21]
	v_mfma_f32_16x16x32_bf16 v[6:9], v[142:145], v[194:197], v[6:9]
	v_mfma_f32_16x16x32_bf16 v[2:5], v[150:153], v[194:197], v[2:5]
	v_mfma_f32_16x16x32_bf16 v[58:61], v[146:149], v[162:165], v[58:61]
	v_mfma_f32_16x16x32_bf16 v[50:53], v[154:157], v[162:165], v[50:53]
	v_mfma_f32_16x16x32_bf16 v[38:41], v[146:149], v[178:181], v[38:41]
	v_mfma_f32_16x16x32_bf16 v[34:37], v[154:157], v[178:181], v[34:37]
	v_mfma_f32_16x16x32_bf16 v[22:25], v[146:149], v[186:189], v[22:25]
	v_mfma_f32_16x16x32_bf16 v[18:21], v[154:157], v[186:189], v[18:21]
	v_mfma_f32_16x16x32_bf16 v[6:9], v[146:149], v[198:201], v[6:9]
	v_mfma_f32_16x16x32_bf16 v[2:5], v[154:157], v[198:201], v[2:5]
	s_barrier
	s_setprio 0
	ds_read_b128 v[122:125], v116
	ds_read_b128 v[130:133], v116 offset:1024
	ds_read_b128 v[134:137], v116 offset:2048
	ds_read_b128 v[138:141], v116 offset:3072
	ds_read_b128 v[142:145], v117
	ds_read_b128 v[146:149], v117 offset:1024
	ds_read_b128 v[150:153], v117 offset:2048
	ds_read_b128 v[154:157], v117 offset:3072
	s_add_u32 s34, s34, 0x4000
	s_addc_u32 s35, s35, 0
	s_mov_b32 m0, s54
	ds_read_b128 v[158:161], v237 offset:32768
	ds_read_b128 v[162:165], v237 offset:33792
	ds_read_b128 v[174:177], v237 offset:34816
	ds_read_b128 v[178:181], v237 offset:35840
	ds_read_b128 v[182:185], v237 offset:36864
	ds_read_b128 v[186:189], v237 offset:37888
	ds_read_b128 v[194:197], v237 offset:38912
	ds_read_b128 v[198:201], v237 offset:39936
	s_nop 0
	global_load_lds_dwordx4 v235, s[34:35]
	s_mov_b32 m0, s55
	s_nop 0
	global_load_lds_dwordx4 v226, s[34:35]
	s_waitcnt vmcnt(8)
	s_waitcnt lgkmcnt(0)
	s_setprio 1
	s_barrier
	v_mfma_f32_16x16x32_bf16 v[166:169], v[122:125], v[158:161], v[166:169]
	v_mfma_f32_16x16x32_bf16 v[170:173], v[134:137], v[158:161], v[170:173]
	v_mfma_f32_16x16x32_bf16 v[110:113], v[122:125], v[174:177], v[110:113]
	v_mfma_f32_16x16x32_bf16 v[106:109], v[134:137], v[174:177], v[106:109]
	v_mfma_f32_16x16x32_bf16 v[94:97], v[122:125], v[182:185], v[94:97]
	v_mfma_f32_16x16x32_bf16 v[90:93], v[134:137], v[182:185], v[90:93]
	v_mfma_f32_16x16x32_bf16 v[78:81], v[122:125], v[194:197], v[78:81]
	v_mfma_f32_16x16x32_bf16 v[70:73], v[134:137], v[194:197], v[70:73]
	v_mfma_f32_16x16x32_bf16 v[166:169], v[130:133], v[162:165], v[166:169]
	v_mfma_f32_16x16x32_bf16 v[170:173], v[138:141], v[162:165], v[170:173]
	v_mfma_f32_16x16x32_bf16 v[110:113], v[130:133], v[178:181], v[110:113]
	v_mfma_f32_16x16x32_bf16 v[106:109], v[138:141], v[178:181], v[106:109]
	v_mfma_f32_16x16x32_bf16 v[94:97], v[130:133], v[186:189], v[94:97]
	v_mfma_f32_16x16x32_bf16 v[90:93], v[138:141], v[186:189], v[90:93]
	v_mfma_f32_16x16x32_bf16 v[78:81], v[130:133], v[198:201], v[78:81]
	v_mfma_f32_16x16x32_bf16 v[70:73], v[138:141], v[198:201], v[70:73]
	s_setprio 0
	s_setprio 1
	v_mfma_f32_16x16x32_bf16 v[126:129], v[142:145], v[158:161], v[126:129]
	v_mfma_f32_16x16x32_bf16 v[118:121], v[150:153], v[158:161], v[118:121]
	v_mfma_f32_16x16x32_bf16 v[102:105], v[142:145], v[174:177], v[102:105]
	v_mfma_f32_16x16x32_bf16 v[98:101], v[150:153], v[174:177], v[98:101]
	v_mfma_f32_16x16x32_bf16 v[86:89], v[142:145], v[182:185], v[86:89]
	v_mfma_f32_16x16x32_bf16 v[82:85], v[150:153], v[182:185], v[82:85]
	v_mfma_f32_16x16x32_bf16 v[62:65], v[142:145], v[194:197], v[62:65]
	v_mfma_f32_16x16x32_bf16 v[54:57], v[150:153], v[194:197], v[54:57]
	v_mfma_f32_16x16x32_bf16 v[126:129], v[146:149], v[162:165], v[126:129]
	v_mfma_f32_16x16x32_bf16 v[118:121], v[154:157], v[162:165], v[118:121]
	v_mfma_f32_16x16x32_bf16 v[102:105], v[146:149], v[178:181], v[102:105]
	v_mfma_f32_16x16x32_bf16 v[98:101], v[154:157], v[178:181], v[98:101]
	v_mfma_f32_16x16x32_bf16 v[86:89], v[146:149], v[186:189], v[86:89]
	v_mfma_f32_16x16x32_bf16 v[82:85], v[154:157], v[186:189], v[82:85]
	v_mfma_f32_16x16x32_bf16 v[62:65], v[146:149], v[198:201], v[62:65]
	v_mfma_f32_16x16x32_bf16 v[54:57], v[154:157], v[198:201], v[54:57]
	s_barrier
	s_setprio 0
	s_add_u32 s34, s30, 0x8000
	s_mov_b32 m0, s52
	s_addc_u32 s35, s31, 0
	ds_read_b128 v[158:161], v237 offset:49152
	ds_read_b128 v[162:165], v237 offset:50176
	ds_read_b128 v[174:177], v237 offset:51200
	ds_read_b128 v[178:181], v237 offset:52224
	ds_read_b128 v[182:185], v237 offset:53248
	ds_read_b128 v[186:189], v237 offset:54272
	ds_read_b128 v[194:197], v237 offset:55296
	ds_read_b128 v[198:201], v237 offset:56320
	s_add_u32 s30, s30, 0xc000
	global_load_lds_dwordx4 v227, s[34:35]
	s_mov_b32 m0, s53
	s_addc_u32 s31, s31, 0
	global_load_lds_dwordx4 v0, s[34:35]
	s_mov_b32 m0, s71
	s_nop 0
	global_load_lds_dwordx4 v227, s[30:31]
	s_mov_b32 m0, s72
	s_nop 0
	global_load_lds_dwordx4 v0, s[30:31]
	s_mov_b32 m0, s58
	s_nop 0
	global_load_lds_dwordx4 v235, s[28:29]
	s_mov_b32 m0, s59
	s_nop 0
	global_load_lds_dwordx4 v226, s[28:29]
	s_waitcnt vmcnt(8)
	s_waitcnt lgkmcnt(0)
	s_setprio 1
	s_barrier
	v_mfma_f32_16x16x32_bf16 v[74:77], v[122:125], v[158:161], v[74:77]
	v_mfma_f32_16x16x32_bf16 v[66:69], v[134:137], v[158:161], v[66:69]
	v_mfma_f32_16x16x32_bf16 v[46:49], v[122:125], v[174:177], v[46:49]
	v_mfma_f32_16x16x32_bf16 v[42:45], v[134:137], v[174:177], v[42:45]
	v_mfma_f32_16x16x32_bf16 v[30:33], v[122:125], v[182:185], v[30:33]
	v_mfma_f32_16x16x32_bf16 v[26:29], v[134:137], v[182:185], v[26:29]
	v_mfma_f32_16x16x32_bf16 v[14:17], v[122:125], v[194:197], v[14:17]
	v_mfma_f32_16x16x32_bf16 v[10:13], v[134:137], v[194:197], v[10:13]
	v_mfma_f32_16x16x32_bf16 v[74:77], v[130:133], v[162:165], v[74:77]
	v_mfma_f32_16x16x32_bf16 v[66:69], v[138:141], v[162:165], v[66:69]
	v_mfma_f32_16x16x32_bf16 v[46:49], v[130:133], v[178:181], v[46:49]
	v_mfma_f32_16x16x32_bf16 v[42:45], v[138:141], v[178:181], v[42:45]
	v_mfma_f32_16x16x32_bf16 v[30:33], v[130:133], v[186:189], v[30:33]
	v_mfma_f32_16x16x32_bf16 v[26:29], v[138:141], v[186:189], v[26:29]
	v_mfma_f32_16x16x32_bf16 v[14:17], v[130:133], v[198:201], v[14:17]
	v_mfma_f32_16x16x32_bf16 v[10:13], v[138:141], v[198:201], v[10:13]
	s_setprio 0
	s_setprio 1
	v_mfma_f32_16x16x32_bf16 v[58:61], v[142:145], v[158:161], v[58:61]
	v_mfma_f32_16x16x32_bf16 v[50:53], v[150:153], v[158:161], v[50:53]
	v_mfma_f32_16x16x32_bf16 v[38:41], v[142:145], v[174:177], v[38:41]
	v_mfma_f32_16x16x32_bf16 v[34:37], v[150:153], v[174:177], v[34:37]
	v_mfma_f32_16x16x32_bf16 v[22:25], v[142:145], v[182:185], v[22:25]
	v_mfma_f32_16x16x32_bf16 v[18:21], v[150:153], v[182:185], v[18:21]
	v_mfma_f32_16x16x32_bf16 v[6:9], v[142:145], v[194:197], v[6:9]
	v_mfma_f32_16x16x32_bf16 v[2:5], v[150:153], v[194:197], v[2:5]
	v_mfma_f32_16x16x32_bf16 v[58:61], v[146:149], v[162:165], v[58:61]
	v_mfma_f32_16x16x32_bf16 v[50:53], v[154:157], v[162:165], v[50:53]
	v_mfma_f32_16x16x32_bf16 v[38:41], v[146:149], v[178:181], v[38:41]
	v_mfma_f32_16x16x32_bf16 v[34:37], v[154:157], v[178:181], v[34:37]
	v_mfma_f32_16x16x32_bf16 v[22:25], v[146:149], v[186:189], v[22:25]
	v_mfma_f32_16x16x32_bf16 v[18:21], v[154:157], v[186:189], v[18:21]
	v_mfma_f32_16x16x32_bf16 v[6:9], v[146:149], v[198:201], v[6:9]
	v_mfma_f32_16x16x32_bf16 v[2:5], v[154:157], v[198:201], v[2:5]
	s_barrier
	s_setprio 0
	s_add_i32 s28, s75, 2
	s_add_u32 s73, s73, 0x10000
	s_addc_u32 s74, s74, 0
	s_add_u32 s26, s26, 0x10000
	s_addc_u32 s27, s27, 0
	s_cmp_lt_i32 s75, s56
	s_mov_b32 s75, s28
	s_cbranch_scc1 .LBB0_381

.LBB0_454:
	s_or_b64 exec, exec, s[34:35]
	s_add_i32 s11, s11, 2
	s_add_u32 s18, s28, 0x4000
	s_addc_u32 s20, s29, 0
	s_and_b64 s[14:15], s[30:31], exec
	s_cselect_b32 s64, s18, s46
	s_cselect_b32 s65, s20, s47
	s_cselect_b32 s35, s2, s63
	s_cselect_b32 s34, s1, s62
	s_add_u32 s30, s64, 0x8000
	s_addc_u32 s31, s65, 0
	s_add_u32 s38, s34, 0x8000
	s_addc_u32 s39, s35, 0
	s_add_i32 s14, 0, 0x10000
	v_add_u32_e32 v149, s14, v146
	s_add_i32 s18, 0, 0x14000
	ds_read_b128 v[132:135], v149
	ds_read_b128 v[136:139], v149 offset:1024
	ds_read_b128 v[150:153], v149 offset:2048
	ds_read_b128 v[154:157], v149 offset:3072
	v_add_u32_e32 v149, s18, v146
	ds_read_b128 v[158:161], v149
	ds_read_b128 v[162:165], v149 offset:1024
	ds_read_b128 v[166:169], v149 offset:2048
	ds_read_b128 v[170:173], v149 offset:3072
	s_add_i32 m0, s71, 0xc000
	ds_read_b128 v[174:177], v148
	ds_read_b128 v[178:181], v148 offset:1024
	ds_read_b128 v[182:185], v148 offset:2048
	ds_read_b128 v[186:189], v148 offset:3072
	ds_read_b128 v[194:197], v148 offset:4096
	ds_read_b128 v[198:201], v148 offset:5120
	ds_read_b128 v[202:205], v148 offset:6144
	ds_read_b128 v[206:209], v148 offset:7168
	s_nop 0
	global_load_lds_dwordx4 v142, s[28:29]
	s_add_i32 m0, s71, 0xe000
	s_nop 0
	global_load_lds_dwordx4 v144, s[28:29]
	s_waitcnt vmcnt(8)
	s_waitcnt lgkmcnt(0)
	s_setprio 1
	s_barrier
	v_mfma_f32_16x16x32_bf16 v[66:69], v[132:135], v[174:177], v[66:69]
	v_mfma_f32_16x16x32_bf16 v[70:73], v[150:153], v[174:177], v[70:73]
	v_mfma_f32_16x16x32_bf16 v[58:61], v[132:135], v[182:185], v[58:61]
	v_mfma_f32_16x16x32_bf16 v[62:65], v[150:153], v[182:185], v[62:65]
	v_mfma_f32_16x16x32_bf16 v[50:53], v[132:135], v[194:197], v[50:53]
	v_mfma_f32_16x16x32_bf16 v[54:57], v[150:153], v[194:197], v[54:57]
	v_mfma_f32_16x16x32_bf16 v[42:45], v[132:135], v[202:205], v[42:45]
	v_mfma_f32_16x16x32_bf16 v[46:49], v[150:153], v[202:205], v[46:49]
	v_mfma_f32_16x16x32_bf16 v[66:69], v[136:139], v[178:181], v[66:69]
	v_mfma_f32_16x16x32_bf16 v[70:73], v[154:157], v[178:181], v[70:73]
	v_mfma_f32_16x16x32_bf16 v[58:61], v[136:139], v[186:189], v[58:61]
	v_mfma_f32_16x16x32_bf16 v[62:65], v[154:157], v[186:189], v[62:65]
	v_mfma_f32_16x16x32_bf16 v[50:53], v[136:139], v[198:201], v[50:53]
	v_mfma_f32_16x16x32_bf16 v[54:57], v[154:157], v[198:201], v[54:57]
	v_mfma_f32_16x16x32_bf16 v[42:45], v[136:139], v[206:209], v[42:45]
	v_mfma_f32_16x16x32_bf16 v[46:49], v[154:157], v[206:209], v[46:49]
	s_setprio 0
	s_setprio 1
	v_mfma_f32_16x16x32_bf16 v[126:129], v[158:161], v[174:177], v[126:129]
	v_mfma_f32_16x16x32_bf16 v[122:125], v[166:169], v[174:177], v[122:125]
	v_mfma_f32_16x16x32_bf16 v[118:121], v[158:161], v[182:185], v[118:121]
	v_mfma_f32_16x16x32_bf16 v[114:117], v[166:169], v[182:185], v[114:117]
	v_mfma_f32_16x16x32_bf16 v[110:113], v[158:161], v[194:197], v[110:113]
	v_mfma_f32_16x16x32_bf16 v[106:109], v[166:169], v[194:197], v[106:109]
	v_mfma_f32_16x16x32_bf16 v[94:97], v[158:161], v[202:205], v[94:97]
	v_mfma_f32_16x16x32_bf16 v[90:93], v[166:169], v[202:205], v[90:93]
	v_mfma_f32_16x16x32_bf16 v[126:129], v[162:165], v[178:181], v[126:129]
	v_mfma_f32_16x16x32_bf16 v[122:125], v[170:173], v[178:181], v[122:125]
	v_mfma_f32_16x16x32_bf16 v[118:121], v[162:165], v[186:189], v[118:121]
	v_mfma_f32_16x16x32_bf16 v[114:117], v[170:173], v[186:189], v[114:117]
	v_mfma_f32_16x16x32_bf16 v[110:113], v[162:165], v[198:201], v[110:113]
	v_mfma_f32_16x16x32_bf16 v[106:109], v[170:173], v[198:201], v[106:109]
	v_mfma_f32_16x16x32_bf16 v[94:97], v[162:165], v[206:209], v[94:97]
	v_mfma_f32_16x16x32_bf16 v[90:93], v[170:173], v[206:209], v[90:93]
	s_barrier
	s_setprio 0
	s_add_i32 s14, s14, s70
	s_mov_b32 m0, s14
	ds_read_b128 v[174:177], v148 offset:16384
	ds_read_b128 v[178:181], v148 offset:17408
	ds_read_b128 v[182:185], v148 offset:18432
	ds_read_b128 v[186:189], v148 offset:19456
	ds_read_b128 v[194:197], v148 offset:20480
	ds_read_b128 v[198:201], v148 offset:21504
	ds_read_b128 v[202:205], v148 offset:22528
	ds_read_b128 v[206:209], v148 offset:23552
	s_nop 0
	global_load_lds_dwordx4 v143, s[34:35]
	s_add_i32 m0, s14, 0x2000
	s_add_u32 s14, s34, 0x4000
	s_addc_u32 s15, s35, 0
	s_add_i32 s18, s18, s70
	s_nop 0
	global_load_lds_dwordx4 v145, s[34:35]
	s_mov_b32 m0, s18
	s_nop 0
	global_load_lds_dwordx4 v143, s[14:15]
	s_add_i32 m0, s18, 0x2000
	s_nop 0
	global_load_lds_dwordx4 v145, s[14:15]
	s_mov_b32 m0, s71
	s_nop 0
	global_load_lds_dwordx4 v142, s[64:65]
	s_mov_b32 m0, s72
	s_nop 0
	global_load_lds_dwordx4 v144, s[64:65]
	s_waitcnt vmcnt(8)
	s_waitcnt lgkmcnt(0)
	s_setprio 1
	s_barrier
	v_mfma_f32_16x16x32_bf16 v[26:29], v[132:135], v[174:177], v[26:29]
	v_mfma_f32_16x16x32_bf16 v[30:33], v[150:153], v[174:177], v[30:33]
	v_mfma_f32_16x16x32_bf16 v[18:21], v[132:135], v[182:185], v[18:21]
	v_mfma_f32_16x16x32_bf16 v[22:25], v[150:153], v[182:185], v[22:25]
	v_mfma_f32_16x16x32_bf16 v[10:13], v[132:135], v[194:197], v[10:13]
	v_mfma_f32_16x16x32_bf16 v[14:17], v[150:153], v[194:197], v[14:17]
	v_mfma_f32_16x16x32_bf16 v[2:5], v[132:135], v[202:205], v[2:5]
	v_mfma_f32_16x16x32_bf16 v[6:9], v[150:153], v[202:205], v[6:9]
	v_mfma_f32_16x16x32_bf16 v[26:29], v[136:139], v[178:181], v[26:29]
	v_mfma_f32_16x16x32_bf16 v[30:33], v[154:157], v[178:181], v[30:33]
	v_mfma_f32_16x16x32_bf16 v[18:21], v[136:139], v[186:189], v[18:21]
	v_mfma_f32_16x16x32_bf16 v[22:25], v[154:157], v[186:189], v[22:25]
	v_mfma_f32_16x16x32_bf16 v[10:13], v[136:139], v[198:201], v[10:13]
	v_mfma_f32_16x16x32_bf16 v[14:17], v[154:157], v[198:201], v[14:17]
	v_mfma_f32_16x16x32_bf16 v[2:5], v[136:139], v[206:209], v[2:5]
	v_mfma_f32_16x16x32_bf16 v[6:9], v[154:157], v[206:209], v[6:9]
	s_setprio 0
	s_setprio 1
	v_mfma_f32_16x16x32_bf16 v[102:105], v[158:161], v[174:177], v[102:105]
	v_mfma_f32_16x16x32_bf16 v[98:101], v[166:169], v[174:177], v[98:101]
	v_mfma_f32_16x16x32_bf16 v[82:85], v[158:161], v[182:185], v[82:85]
	v_mfma_f32_16x16x32_bf16 v[86:89], v[166:169], v[182:185], v[86:89]
	v_mfma_f32_16x16x32_bf16 v[78:81], v[158:161], v[194:197], v[78:81]
	v_mfma_f32_16x16x32_bf16 v[74:77], v[166:169], v[194:197], v[74:77]
	v_mfma_f32_16x16x32_bf16 v[34:37], v[158:161], v[202:205], v[34:37]
	v_mfma_f32_16x16x32_bf16 v[38:41], v[166:169], v[202:205], v[38:41]
	v_mfma_f32_16x16x32_bf16 v[102:105], v[162:165], v[178:181], v[102:105]
	v_mfma_f32_16x16x32_bf16 v[98:101], v[170:173], v[178:181], v[98:101]
	v_mfma_f32_16x16x32_bf16 v[82:85], v[162:165], v[186:189], v[82:85]
	v_mfma_f32_16x16x32_bf16 v[86:89], v[170:173], v[186:189], v[86:89]
	v_mfma_f32_16x16x32_bf16 v[78:81], v[162:165], v[198:201], v[78:81]
	v_mfma_f32_16x16x32_bf16 v[74:77], v[170:173], v[198:201], v[74:77]
	v_mfma_f32_16x16x32_bf16 v[34:37], v[162:165], v[206:209], v[34:37]
	v_mfma_f32_16x16x32_bf16 v[38:41], v[170:173], v[206:209], v[38:41]
	s_barrier
	s_setprio 0
	s_add_i32 s18, 0, 0x18000
	v_add_u32_e32 v149, s18, v146
	s_add_i32 s20, 0, 0x1c000
	ds_read_b128 v[132:135], v149
	ds_read_b128 v[136:139], v149 offset:1024
	ds_read_b128 v[150:153], v149 offset:2048
	ds_read_b128 v[154:157], v149 offset:3072
	v_add_u32_e32 v149, s20, v146
	ds_read_b128 v[158:161], v149
	ds_read_b128 v[162:165], v149 offset:1024
	ds_read_b128 v[166:169], v149 offset:2048
	ds_read_b128 v[170:173], v149 offset:3072
	s_add_u32 s14, s64, 0x4000
	s_addc_u32 s15, s65, 0
	s_mov_b32 m0, s73
	ds_read_b128 v[174:177], v148 offset:32768
	ds_read_b128 v[178:181], v148 offset:33792
	ds_read_b128 v[182:185], v148 offset:34816
	ds_read_b128 v[186:189], v148 offset:35840
	ds_read_b128 v[194:197], v148 offset:36864
	ds_read_b128 v[198:201], v148 offset:37888
	ds_read_b128 v[202:205], v148 offset:38912
	ds_read_b128 v[206:209], v148 offset:39936
	s_nop 0
	global_load_lds_dwordx4 v142, s[14:15]
	s_mov_b32 m0, s74
	s_nop 0
	global_load_lds_dwordx4 v144, s[14:15]
	s_waitcnt vmcnt(8)
	s_waitcnt lgkmcnt(0)
	s_setprio 1
	s_barrier
	v_mfma_f32_16x16x32_bf16 v[66:69], v[132:135], v[174:177], v[66:69]
	v_mfma_f32_16x16x32_bf16 v[70:73], v[150:153], v[174:177], v[70:73]
	v_mfma_f32_16x16x32_bf16 v[58:61], v[132:135], v[182:185], v[58:61]
	v_mfma_f32_16x16x32_bf16 v[62:65], v[150:153], v[182:185], v[62:65]
	v_mfma_f32_16x16x32_bf16 v[50:53], v[132:135], v[194:197], v[50:53]
	v_mfma_f32_16x16x32_bf16 v[54:57], v[150:153], v[194:197], v[54:57]
	v_mfma_f32_16x16x32_bf16 v[42:45], v[132:135], v[202:205], v[42:45]
	v_mfma_f32_16x16x32_bf16 v[46:49], v[150:153], v[202:205], v[46:49]
	v_mfma_f32_16x16x32_bf16 v[66:69], v[136:139], v[178:181], v[66:69]
	v_mfma_f32_16x16x32_bf16 v[70:73], v[154:157], v[178:181], v[70:73]
	v_mfma_f32_16x16x32_bf16 v[58:61], v[136:139], v[186:189], v[58:61]
	v_mfma_f32_16x16x32_bf16 v[62:65], v[154:157], v[186:189], v[62:65]
	v_mfma_f32_16x16x32_bf16 v[50:53], v[136:139], v[198:201], v[50:53]
	v_mfma_f32_16x16x32_bf16 v[54:57], v[154:157], v[198:201], v[54:57]
	v_mfma_f32_16x16x32_bf16 v[42:45], v[136:139], v[206:209], v[42:45]
	v_mfma_f32_16x16x32_bf16 v[46:49], v[154:157], v[206:209], v[46:49]
	s_setprio 0
	s_setprio 1
	v_mfma_f32_16x16x32_bf16 v[126:129], v[158:161], v[174:177], v[126:129]
	v_mfma_f32_16x16x32_bf16 v[122:125], v[166:169], v[174:177], v[122:125]
	v_mfma_f32_16x16x32_bf16 v[118:121], v[158:161], v[182:185], v[118:121]
	v_mfma_f32_16x16x32_bf16 v[114:117], v[166:169], v[182:185], v[114:117]
	v_mfma_f32_16x16x32_bf16 v[110:113], v[158:161], v[194:197], v[110:113]
	v_mfma_f32_16x16x32_bf16 v[106:109], v[166:169], v[194:197], v[106:109]
	v_mfma_f32_16x16x32_bf16 v[94:97], v[158:161], v[202:205], v[94:97]
	v_mfma_f32_16x16x32_bf16 v[90:93], v[166:169], v[202:205], v[90:93]
	v_mfma_f32_16x16x32_bf16 v[126:129], v[162:165], v[178:181], v[126:129]
	v_mfma_f32_16x16x32_bf16 v[122:125], v[170:173], v[178:181], v[122:125]
	v_mfma_f32_16x16x32_bf16 v[118:121], v[162:165], v[186:189], v[118:121]
	v_mfma_f32_16x16x32_bf16 v[114:117], v[170:173], v[186:189], v[114:117]
	v_mfma_f32_16x16x32_bf16 v[110:113], v[162:165], v[198:201], v[110:113]
	v_mfma_f32_16x16x32_bf16 v[106:109], v[170:173], v[198:201], v[106:109]
	v_mfma_f32_16x16x32_bf16 v[94:97], v[162:165], v[206:209], v[94:97]
	v_mfma_f32_16x16x32_bf16 v[90:93], v[170:173], v[206:209], v[90:93]
	s_barrier
	s_setprio 0
	s_add_i32 s14, s18, s70
	s_mov_b32 m0, s14
	ds_read_b128 v[174:177], v148 offset:49152
	ds_read_b128 v[178:181], v148 offset:50176
	ds_read_b128 v[182:185], v148 offset:51200
	ds_read_b128 v[186:189], v148 offset:52224
	ds_read_b128 v[194:197], v148 offset:53248
	ds_read_b128 v[198:201], v148 offset:54272
	ds_read_b128 v[202:205], v148 offset:55296
	ds_read_b128 v[206:209], v148 offset:56320
	s_nop 0
	global_load_lds_dwordx4 v143, s[38:39]
	s_add_i32 m0, s14, 0x2000
	s_add_u32 s14, s34, 0xc000
	s_addc_u32 s15, s35, 0
	s_add_i32 s18, s20, s70
	s_nop 0
	global_load_lds_dwordx4 v145, s[38:39]
	s_mov_b32 m0, s18
	s_nop 0
	global_load_lds_dwordx4 v143, s[14:15]
	s_add_i32 m0, s18, 0x2000
	s_nop 0
	global_load_lds_dwordx4 v145, s[14:15]
	s_mov_b32 m0, s81
	s_nop 0
	global_load_lds_dwordx4 v142, s[30:31]
	s_mov_b32 m0, s82
	s_nop 0
	global_load_lds_dwordx4 v144, s[30:31]
	s_waitcnt vmcnt(8)
	s_waitcnt lgkmcnt(0)
	s_setprio 1
	s_barrier
	v_mfma_f32_16x16x32_bf16 v[26:29], v[132:135], v[174:177], v[26:29]
	v_mfma_f32_16x16x32_bf16 v[30:33], v[150:153], v[174:177], v[30:33]
	v_mfma_f32_16x16x32_bf16 v[18:21], v[132:135], v[182:185], v[18:21]
	v_mfma_f32_16x16x32_bf16 v[22:25], v[150:153], v[182:185], v[22:25]
	v_mfma_f32_16x16x32_bf16 v[10:13], v[132:135], v[194:197], v[10:13]
	v_mfma_f32_16x16x32_bf16 v[14:17], v[150:153], v[194:197], v[14:17]
	v_mfma_f32_16x16x32_bf16 v[2:5], v[132:135], v[202:205], v[2:5]
	v_mfma_f32_16x16x32_bf16 v[6:9], v[150:153], v[202:205], v[6:9]
	v_mfma_f32_16x16x32_bf16 v[26:29], v[136:139], v[178:181], v[26:29]
	v_mfma_f32_16x16x32_bf16 v[30:33], v[154:157], v[178:181], v[30:33]
	v_mfma_f32_16x16x32_bf16 v[18:21], v[136:139], v[186:189], v[18:21]
	v_mfma_f32_16x16x32_bf16 v[22:25], v[154:157], v[186:189], v[22:25]
	v_mfma_f32_16x16x32_bf16 v[10:13], v[136:139], v[198:201], v[10:13]
	v_mfma_f32_16x16x32_bf16 v[14:17], v[154:157], v[198:201], v[14:17]
	v_mfma_f32_16x16x32_bf16 v[2:5], v[136:139], v[206:209], v[2:5]
	v_mfma_f32_16x16x32_bf16 v[6:9], v[154:157], v[206:209], v[6:9]
	s_setprio 0
	s_setprio 1
	v_mfma_f32_16x16x32_bf16 v[102:105], v[158:161], v[174:177], v[102:105]
	v_mfma_f32_16x16x32_bf16 v[98:101], v[166:169], v[174:177], v[98:101]
	v_mfma_f32_16x16x32_bf16 v[82:85], v[158:161], v[182:185], v[82:85]
	v_mfma_f32_16x16x32_bf16 v[86:89], v[166:169], v[182:185], v[86:89]
	v_mfma_f32_16x16x32_bf16 v[78:81], v[158:161], v[194:197], v[78:81]
	v_mfma_f32_16x16x32_bf16 v[74:77], v[166:169], v[194:197], v[74:77]
	v_mfma_f32_16x16x32_bf16 v[34:37], v[158:161], v[202:205], v[34:37]
	v_mfma_f32_16x16x32_bf16 v[38:41], v[166:169], v[202:205], v[38:41]
	v_mfma_f32_16x16x32_bf16 v[102:105], v[162:165], v[178:181], v[102:105]
	v_mfma_f32_16x16x32_bf16 v[98:101], v[170:173], v[178:181], v[98:101]
	v_mfma_f32_16x16x32_bf16 v[82:85], v[162:165], v[186:189], v[82:85]
	v_mfma_f32_16x16x32_bf16 v[86:89], v[170:173], v[186:189], v[86:89]
	v_mfma_f32_16x16x32_bf16 v[78:81], v[162:165], v[198:201], v[78:81]
	v_mfma_f32_16x16x32_bf16 v[74:77], v[170:173], v[198:201], v[74:77]
	v_mfma_f32_16x16x32_bf16 v[34:37], v[162:165], v[206:209], v[34:37]
	v_mfma_f32_16x16x32_bf16 v[38:41], v[170:173], v[206:209], v[38:41]
	s_barrier
	s_setprio 0
	s_add_u32 s1, s1, 0x10000
	s_addc_u32 s2, s2, 0
	s_add_u32 s28, s28, 0x10000
	s_addc_u32 s29, s29, 0
	s_cmp_ge_i32 s11, s78
	s_cbranch_scc1 .LBB0_457

.LBB0_498:
	s_add_i32 s83, s52, 2
	s_add_u32 s50, s48, 0x100
	s_addc_u32 s51, s49, 0
	s_add_i32 s84, 0, 0x10000
	s_cmp_eq_u32 s71, s52
	s_cselect_b32 s53, s43, s51
	s_cselect_b32 s52, s42, s50
	v_add_u32_e32 v131, s84, v137
	s_cselect_b32 s55, s47, s82
	s_cselect_b32 s54, s46, s81
	s_add_i32 s85, 0, 0x14000
	ds_read_b128 v[142:145], v131
	ds_read_b128 v[146:149], v131 offset:1024
	ds_read_b128 v[150:153], v131 offset:2048
	ds_read_b128 v[154:157], v131 offset:3072
	v_add_u32_e32 v131, s85, v137
	ds_read_b128 v[158:161], v131
	ds_read_b128 v[162:165], v131 offset:1024
	ds_read_b128 v[166:169], v131 offset:2048
	ds_read_b128 v[170:173], v131 offset:3072
	s_add_u32 s48, s48, s74
	s_addc_u32 s49, s49, s75
	s_add_i32 m0, s62, 0xc000
	ds_read_b128 v[174:177], v138
	ds_read_b128 v[178:181], v138 offset:1024
	ds_read_b128 v[182:185], v138 offset:2048
	ds_read_b128 v[186:189], v138 offset:3072
	ds_read_b128 v[194:197], v138 offset:4096
	ds_read_b128 v[198:201], v138 offset:5120
	ds_read_b128 v[202:205], v138 offset:6144
	ds_read_b128 v[206:209], v138 offset:7168
	s_nop 0
	global_load_lds_dwordx4 v130, s[48:49]
	s_add_i32 m0, s62, 0xe000
	s_nop 0
	global_load_lds_dwordx4 v132, s[48:49]
	s_waitcnt vmcnt(8)
	s_waitcnt lgkmcnt(0)
	s_setprio 1
	s_barrier
	v_mfma_f32_16x16x32_bf16 v[118:121], v[142:145], v[174:177], v[118:121]
	v_mfma_f32_16x16x32_bf16 v[114:117], v[150:153], v[174:177], v[114:117]
	v_mfma_f32_16x16x32_bf16 v[102:105], v[142:145], v[182:185], v[102:105]
	v_mfma_f32_16x16x32_bf16 v[98:101], v[150:153], v[182:185], v[98:101]
	v_mfma_f32_16x16x32_bf16 v[86:89], v[142:145], v[194:197], v[86:89]
	v_mfma_f32_16x16x32_bf16 v[82:85], v[150:153], v[194:197], v[82:85]
	v_mfma_f32_16x16x32_bf16 v[70:73], v[142:145], v[202:205], v[70:73]
	v_mfma_f32_16x16x32_bf16 v[66:69], v[150:153], v[202:205], v[66:69]
	v_mfma_f32_16x16x32_bf16 v[118:121], v[146:149], v[178:181], v[118:121]
	v_mfma_f32_16x16x32_bf16 v[114:117], v[154:157], v[178:181], v[114:117]
	v_mfma_f32_16x16x32_bf16 v[102:105], v[146:149], v[186:189], v[102:105]
	v_mfma_f32_16x16x32_bf16 v[98:101], v[154:157], v[186:189], v[98:101]
	v_mfma_f32_16x16x32_bf16 v[86:89], v[146:149], v[198:201], v[86:89]
	v_mfma_f32_16x16x32_bf16 v[82:85], v[154:157], v[198:201], v[82:85]
	v_mfma_f32_16x16x32_bf16 v[70:73], v[146:149], v[206:209], v[70:73]
	v_mfma_f32_16x16x32_bf16 v[66:69], v[154:157], v[206:209], v[66:69]
	s_setprio 0
	s_setprio 1
	v_mfma_f32_16x16x32_bf16 v[46:49], v[158:161], v[174:177], v[46:49]
	v_mfma_f32_16x16x32_bf16 v[42:45], v[166:169], v[174:177], v[42:45]
	v_mfma_f32_16x16x32_bf16 v[30:33], v[158:161], v[182:185], v[30:33]
	v_mfma_f32_16x16x32_bf16 v[26:29], v[166:169], v[182:185], v[26:29]
	v_mfma_f32_16x16x32_bf16 v[14:17], v[158:161], v[194:197], v[14:17]
	v_mfma_f32_16x16x32_bf16 v[10:13], v[166:169], v[194:197], v[10:13]
	v_mfma_f32_16x16x32_bf16 v[6:9], v[158:161], v[202:205], v[6:9]
	v_mfma_f32_16x16x32_bf16 v[2:5], v[166:169], v[202:205], v[2:5]
	v_mfma_f32_16x16x32_bf16 v[46:49], v[162:165], v[178:181], v[46:49]
	v_mfma_f32_16x16x32_bf16 v[42:45], v[170:173], v[178:181], v[42:45]
	v_mfma_f32_16x16x32_bf16 v[30:33], v[162:165], v[186:189], v[30:33]
	v_mfma_f32_16x16x32_bf16 v[26:29], v[170:173], v[186:189], v[26:29]
	v_mfma_f32_16x16x32_bf16 v[14:17], v[162:165], v[198:201], v[14:17]
	v_mfma_f32_16x16x32_bf16 v[10:13], v[170:173], v[198:201], v[10:13]
	v_mfma_f32_16x16x32_bf16 v[6:9], v[162:165], v[206:209], v[6:9]
	v_mfma_f32_16x16x32_bf16 v[2:5], v[170:173], v[206:209], v[2:5]
	s_barrier
	s_setprio 0
	s_add_i32 s48, s84, s61
	s_mov_b32 m0, s48
	ds_read_b128 v[174:177], v138 offset:16384
	ds_read_b128 v[178:181], v138 offset:17408
	ds_read_b128 v[182:185], v138 offset:18432
	ds_read_b128 v[186:189], v138 offset:19456
	ds_read_b128 v[194:197], v138 offset:20480
	ds_read_b128 v[198:201], v138 offset:21504
	ds_read_b128 v[202:205], v138 offset:22528
	ds_read_b128 v[206:209], v138 offset:23552
	s_nop 0
	global_load_lds_dwordx4 v0, s[54:55]
	s_add_i32 m0, s48, 0x2000
	s_add_u32 s48, s54, s28
	s_addc_u32 s49, s55, s29
	s_add_i32 s84, s85, s61
	s_nop 0
	global_load_lds_dwordx4 v134, s[54:55]
	s_mov_b32 m0, s84
	s_nop 0
	global_load_lds_dwordx4 v0, s[48:49]
	s_add_i32 m0, s84, 0x2000
	s_nop 0
	global_load_lds_dwordx4 v134, s[48:49]
	s_mov_b32 m0, s62
	s_nop 0
	global_load_lds_dwordx4 v130, s[52:53]
	s_mov_b32 m0, s63
	s_nop 0
	global_load_lds_dwordx4 v132, s[52:53]
	s_waitcnt vmcnt(8)
	s_waitcnt lgkmcnt(0)
	s_setprio 1
	s_barrier
	v_mfma_f32_16x16x32_bf16 v[126:129], v[142:145], v[174:177], v[126:129]
	v_mfma_f32_16x16x32_bf16 v[122:125], v[150:153], v[174:177], v[122:125]
	v_mfma_f32_16x16x32_bf16 v[110:113], v[142:145], v[182:185], v[110:113]
	v_mfma_f32_16x16x32_bf16 v[106:109], v[150:153], v[182:185], v[106:109]
	v_mfma_f32_16x16x32_bf16 v[94:97], v[142:145], v[194:197], v[94:97]
	v_mfma_f32_16x16x32_bf16 v[90:93], v[150:153], v[194:197], v[90:93]
	v_mfma_f32_16x16x32_bf16 v[78:81], v[142:145], v[202:205], v[78:81]
	v_mfma_f32_16x16x32_bf16 v[74:77], v[150:153], v[202:205], v[74:77]
	v_mfma_f32_16x16x32_bf16 v[126:129], v[146:149], v[178:181], v[126:129]
	v_mfma_f32_16x16x32_bf16 v[122:125], v[154:157], v[178:181], v[122:125]
	v_mfma_f32_16x16x32_bf16 v[110:113], v[146:149], v[186:189], v[110:113]
	v_mfma_f32_16x16x32_bf16 v[106:109], v[154:157], v[186:189], v[106:109]
	v_mfma_f32_16x16x32_bf16 v[94:97], v[146:149], v[198:201], v[94:97]
	v_mfma_f32_16x16x32_bf16 v[90:93], v[154:157], v[198:201], v[90:93]
	v_mfma_f32_16x16x32_bf16 v[78:81], v[146:149], v[206:209], v[78:81]
	v_mfma_f32_16x16x32_bf16 v[74:77], v[154:157], v[206:209], v[74:77]
	s_setprio 0
	s_setprio 1
	v_mfma_f32_16x16x32_bf16 v[54:57], v[158:161], v[174:177], v[54:57]
	v_mfma_f32_16x16x32_bf16 v[50:53], v[166:169], v[174:177], v[50:53]
	v_mfma_f32_16x16x32_bf16 v[38:41], v[158:161], v[182:185], v[38:41]
	v_mfma_f32_16x16x32_bf16 v[34:37], v[166:169], v[182:185], v[34:37]
	v_mfma_f32_16x16x32_bf16 v[22:25], v[158:161], v[194:197], v[22:25]
	v_mfma_f32_16x16x32_bf16 v[18:21], v[166:169], v[194:197], v[18:21]
	v_mfma_f32_16x16x32_bf16 v[58:61], v[158:161], v[202:205], v[58:61]
	v_mfma_f32_16x16x32_bf16 v[62:65], v[166:169], v[202:205], v[62:65]
	v_mfma_f32_16x16x32_bf16 v[54:57], v[162:165], v[178:181], v[54:57]
	v_mfma_f32_16x16x32_bf16 v[50:53], v[170:173], v[178:181], v[50:53]
	v_mfma_f32_16x16x32_bf16 v[38:41], v[162:165], v[186:189], v[38:41]
	v_mfma_f32_16x16x32_bf16 v[34:37], v[170:173], v[186:189], v[34:37]
	v_mfma_f32_16x16x32_bf16 v[22:25], v[162:165], v[198:201], v[22:25]
	v_mfma_f32_16x16x32_bf16 v[18:21], v[170:173], v[198:201], v[18:21]
	v_mfma_f32_16x16x32_bf16 v[58:61], v[162:165], v[206:209], v[58:61]
	v_mfma_f32_16x16x32_bf16 v[62:65], v[170:173], v[206:209], v[62:65]
	s_barrier
	s_setprio 0
	s_add_i32 s86, 0, 0x18000
	v_add_u32_e32 v131, s86, v137
	s_add_i32 s87, 0, 0x1c000
	ds_read_b128 v[142:145], v131
	ds_read_b128 v[146:149], v131 offset:1024
	ds_read_b128 v[150:153], v131 offset:2048
	ds_read_b128 v[154:157], v131 offset:3072
	v_add_u32_e32 v131, s87, v137
	ds_read_b128 v[158:161], v131
	ds_read_b128 v[162:165], v131 offset:1024
	ds_read_b128 v[166:169], v131 offset:2048
	ds_read_b128 v[170:173], v131 offset:3072
	s_add_u32 s84, s52, s28
	s_addc_u32 s85, s53, s29
	s_mov_b32 m0, s64
	ds_read_b128 v[174:177], v138 offset:32768
	ds_read_b128 v[178:181], v138 offset:33792
	ds_read_b128 v[182:185], v138 offset:34816
	ds_read_b128 v[186:189], v138 offset:35840
	ds_read_b128 v[194:197], v138 offset:36864
	ds_read_b128 v[198:201], v138 offset:37888
	ds_read_b128 v[202:205], v138 offset:38912
	ds_read_b128 v[206:209], v138 offset:39936
	s_nop 0
	global_load_lds_dwordx4 v130, s[84:85]
	s_mov_b32 m0, s65
	s_nop 0
	global_load_lds_dwordx4 v132, s[84:85]
	s_waitcnt vmcnt(8)
	s_waitcnt lgkmcnt(0)
	s_setprio 1
	s_barrier
	v_mfma_f32_16x16x32_bf16 v[118:121], v[142:145], v[174:177], v[118:121]
	v_mfma_f32_16x16x32_bf16 v[114:117], v[150:153], v[174:177], v[114:117]
	v_mfma_f32_16x16x32_bf16 v[102:105], v[142:145], v[182:185], v[102:105]
	v_mfma_f32_16x16x32_bf16 v[98:101], v[150:153], v[182:185], v[98:101]
	v_mfma_f32_16x16x32_bf16 v[86:89], v[142:145], v[194:197], v[86:89]
	v_mfma_f32_16x16x32_bf16 v[82:85], v[150:153], v[194:197], v[82:85]
	v_mfma_f32_16x16x32_bf16 v[70:73], v[142:145], v[202:205], v[70:73]
	v_mfma_f32_16x16x32_bf16 v[66:69], v[150:153], v[202:205], v[66:69]
	v_mfma_f32_16x16x32_bf16 v[118:121], v[146:149], v[178:181], v[118:121]
	v_mfma_f32_16x16x32_bf16 v[114:117], v[154:157], v[178:181], v[114:117]
	v_mfma_f32_16x16x32_bf16 v[102:105], v[146:149], v[186:189], v[102:105]
	v_mfma_f32_16x16x32_bf16 v[98:101], v[154:157], v[186:189], v[98:101]
	v_mfma_f32_16x16x32_bf16 v[86:89], v[146:149], v[198:201], v[86:89]
	v_mfma_f32_16x16x32_bf16 v[82:85], v[154:157], v[198:201], v[82:85]
	v_mfma_f32_16x16x32_bf16 v[70:73], v[146:149], v[206:209], v[70:73]
	v_mfma_f32_16x16x32_bf16 v[66:69], v[154:157], v[206:209], v[66:69]
	s_setprio 0
	s_setprio 1
	v_mfma_f32_16x16x32_bf16 v[46:49], v[158:161], v[174:177], v[46:49]
	v_mfma_f32_16x16x32_bf16 v[42:45], v[166:169], v[174:177], v[42:45]
	v_mfma_f32_16x16x32_bf16 v[30:33], v[158:161], v[182:185], v[30:33]
	v_mfma_f32_16x16x32_bf16 v[26:29], v[166:169], v[182:185], v[26:29]
	v_mfma_f32_16x16x32_bf16 v[14:17], v[158:161], v[194:197], v[14:17]
	v_mfma_f32_16x16x32_bf16 v[10:13], v[166:169], v[194:197], v[10:13]
	v_mfma_f32_16x16x32_bf16 v[6:9], v[158:161], v[202:205], v[6:9]
	v_mfma_f32_16x16x32_bf16 v[2:5], v[166:169], v[202:205], v[2:5]
	v_mfma_f32_16x16x32_bf16 v[46:49], v[162:165], v[178:181], v[46:49]
	v_mfma_f32_16x16x32_bf16 v[42:45], v[170:173], v[178:181], v[42:45]
	v_mfma_f32_16x16x32_bf16 v[30:33], v[162:165], v[186:189], v[30:33]
	v_mfma_f32_16x16x32_bf16 v[26:29], v[170:173], v[186:189], v[26:29]
	v_mfma_f32_16x16x32_bf16 v[14:17], v[162:165], v[198:201], v[14:17]
	v_mfma_f32_16x16x32_bf16 v[10:13], v[170:173], v[198:201], v[10:13]
	v_mfma_f32_16x16x32_bf16 v[6:9], v[162:165], v[206:209], v[6:9]
	v_mfma_f32_16x16x32_bf16 v[2:5], v[170:173], v[206:209], v[2:5]
	s_barrier
	s_setprio 0
	ds_read_b128 v[174:177], v138 offset:49152
	ds_read_b128 v[178:181], v138 offset:50176
	ds_read_b128 v[182:185], v138 offset:51200
	ds_read_b128 v[186:189], v138 offset:52224
	ds_read_b128 v[194:197], v138 offset:53248
	ds_read_b128 v[198:201], v138 offset:54272
	ds_read_b128 v[202:205], v138 offset:55296
	ds_read_b128 v[206:209], v138 offset:56320
	s_add_i32 s84, s86, s61
	v_lshl_add_u64 v[190:191], s[54:55], 0, v[0:1]
	v_lshl_add_u64 v[190:191], v[190:191], 0, s[16:17]
	s_mov_b32 m0, s84
	v_mov_b32_e32 v135, v1
	global_load_lds_dwordx4 v[190:191], off
	s_add_i32 m0, s84, 0x2000
	v_lshl_add_u64 v[190:191], s[54:55], 0, v[134:135]
	v_lshl_add_u64 v[190:191], v[190:191], 0, s[16:17]
	global_load_lds_dwordx4 v[190:191], off
	s_add_i32 s54, s87, s61
	v_lshl_add_u64 v[190:191], s[48:49], 0, v[0:1]
	v_lshl_add_u64 v[190:191], v[190:191], 0, s[16:17]
	s_mov_b32 m0, s54
	v_mov_b32_e32 v131, v1
	global_load_lds_dwordx4 v[190:191], off
	s_add_i32 m0, s54, 0x2000
	v_lshl_add_u64 v[190:191], s[48:49], 0, v[134:135]
	v_lshl_add_u64 v[190:191], v[190:191], 0, s[16:17]
	global_load_lds_dwordx4 v[190:191], off
	s_mov_b32 m0, s66
	v_lshl_add_u64 v[190:191], s[52:53], 0, v[130:131]
	v_lshl_add_u64 v[190:191], v[190:191], 0, s[16:17]
	v_mov_b32_e32 v133, v1
	global_load_lds_dwordx4 v[190:191], off
	s_mov_b32 m0, s67
	v_lshl_add_u64 v[190:191], s[52:53], 0, v[132:133]
	v_lshl_add_u64 v[190:191], v[190:191], 0, s[16:17]
	global_load_lds_dwordx4 v[190:191], off
	s_waitcnt vmcnt(8)
	s_waitcnt lgkmcnt(0)
	s_setprio 1
	s_barrier
	v_mfma_f32_16x16x32_bf16 v[126:129], v[142:145], v[174:177], v[126:129]
	v_mfma_f32_16x16x32_bf16 v[122:125], v[150:153], v[174:177], v[122:125]
	v_mfma_f32_16x16x32_bf16 v[110:113], v[142:145], v[182:185], v[110:113]
	v_mfma_f32_16x16x32_bf16 v[106:109], v[150:153], v[182:185], v[106:109]
	v_mfma_f32_16x16x32_bf16 v[94:97], v[142:145], v[194:197], v[94:97]
	v_mfma_f32_16x16x32_bf16 v[90:93], v[150:153], v[194:197], v[90:93]
	v_mfma_f32_16x16x32_bf16 v[78:81], v[142:145], v[202:205], v[78:81]
	v_mfma_f32_16x16x32_bf16 v[74:77], v[150:153], v[202:205], v[74:77]
	v_mfma_f32_16x16x32_bf16 v[126:129], v[146:149], v[178:181], v[126:129]
	v_mfma_f32_16x16x32_bf16 v[122:125], v[154:157], v[178:181], v[122:125]
	v_mfma_f32_16x16x32_bf16 v[110:113], v[146:149], v[186:189], v[110:113]
	v_mfma_f32_16x16x32_bf16 v[106:109], v[154:157], v[186:189], v[106:109]
	v_mfma_f32_16x16x32_bf16 v[94:97], v[146:149], v[198:201], v[94:97]
	v_mfma_f32_16x16x32_bf16 v[90:93], v[154:157], v[198:201], v[90:93]
	v_mfma_f32_16x16x32_bf16 v[78:81], v[146:149], v[206:209], v[78:81]
	v_mfma_f32_16x16x32_bf16 v[74:77], v[154:157], v[206:209], v[74:77]
	s_setprio 0
	s_setprio 1
	v_mfma_f32_16x16x32_bf16 v[54:57], v[158:161], v[174:177], v[54:57]
	v_mfma_f32_16x16x32_bf16 v[50:53], v[166:169], v[174:177], v[50:53]
	v_mfma_f32_16x16x32_bf16 v[38:41], v[158:161], v[182:185], v[38:41]
	v_mfma_f32_16x16x32_bf16 v[34:37], v[166:169], v[182:185], v[34:37]
	v_mfma_f32_16x16x32_bf16 v[22:25], v[158:161], v[194:197], v[22:25]
	v_mfma_f32_16x16x32_bf16 v[18:21], v[166:169], v[194:197], v[18:21]
	v_mfma_f32_16x16x32_bf16 v[58:61], v[158:161], v[202:205], v[58:61]
	v_mfma_f32_16x16x32_bf16 v[62:65], v[166:169], v[202:205], v[62:65]
	v_mfma_f32_16x16x32_bf16 v[54:57], v[162:165], v[178:181], v[54:57]
	v_mfma_f32_16x16x32_bf16 v[50:53], v[170:173], v[178:181], v[50:53]
	v_mfma_f32_16x16x32_bf16 v[38:41], v[162:165], v[186:189], v[38:41]
	v_mfma_f32_16x16x32_bf16 v[34:37], v[170:173], v[186:189], v[34:37]
	v_mfma_f32_16x16x32_bf16 v[22:25], v[162:165], v[198:201], v[22:25]
	v_mfma_f32_16x16x32_bf16 v[18:21], v[170:173], v[198:201], v[18:21]
	v_mfma_f32_16x16x32_bf16 v[58:61], v[162:165], v[206:209], v[58:61]
	v_mfma_f32_16x16x32_bf16 v[62:65], v[170:173], v[206:209], v[62:65]
	s_barrier
	s_setprio 0
	s_add_u32 s81, s81, 0x100
	s_addc_u32 s82, s82, 0
	s_cmp_ge_i32 s83, s68
	s_mov_b64 s[48:49], s[50:51]
	s_mov_b32 s52, s83
	s_cbranch_scc0 .LBB0_498

.LBB0_531:
	s_add_i32 s81, s52, 2
	s_add_u32 s50, s48, 0x100
	s_addc_u32 s51, s49, 0
	s_add_i32 s82, 0, 0x10000
	s_cmp_eq_u32 s71, s52
	s_cselect_b32 s53, s43, s51
	s_cselect_b32 s52, s42, s50
	v_add_u32_e32 v131, s82, v137
	s_cselect_b32 s55, s45, s80
	s_cselect_b32 s54, s44, s47
	s_add_i32 s83, 0, 0x14000
	ds_read_b128 v[142:145], v131
	ds_read_b128 v[146:149], v131 offset:1024
	ds_read_b128 v[150:153], v131 offset:2048
	ds_read_b128 v[154:157], v131 offset:3072
	v_add_u32_e32 v131, s83, v137
	ds_read_b128 v[158:161], v131
	ds_read_b128 v[162:165], v131 offset:1024
	ds_read_b128 v[166:169], v131 offset:2048
	ds_read_b128 v[170:173], v131 offset:3072
	s_add_u32 s48, s48, s74
	s_addc_u32 s49, s49, s75
	s_add_i32 m0, s62, 0xc000
	ds_read_b128 v[174:177], v138
	ds_read_b128 v[178:181], v138 offset:1024
	ds_read_b128 v[182:185], v138 offset:2048
	ds_read_b128 v[186:189], v138 offset:3072
	ds_read_b128 v[194:197], v138 offset:4096
	ds_read_b128 v[198:201], v138 offset:5120
	ds_read_b128 v[202:205], v138 offset:6144
	ds_read_b128 v[206:209], v138 offset:7168
	s_nop 0
	global_load_lds_dwordx4 v130, s[48:49]
	s_add_i32 m0, s62, 0xe000
	s_nop 0
	global_load_lds_dwordx4 v132, s[48:49]
	s_waitcnt vmcnt(8)
	s_waitcnt lgkmcnt(0)
	s_setprio 1
	s_barrier
	v_mfma_f32_16x16x32_bf16 v[118:121], v[142:145], v[174:177], v[118:121]
	v_mfma_f32_16x16x32_bf16 v[114:117], v[150:153], v[174:177], v[114:117]
	v_mfma_f32_16x16x32_bf16 v[102:105], v[142:145], v[182:185], v[102:105]
	v_mfma_f32_16x16x32_bf16 v[98:101], v[150:153], v[182:185], v[98:101]
	v_mfma_f32_16x16x32_bf16 v[86:89], v[142:145], v[194:197], v[86:89]
	v_mfma_f32_16x16x32_bf16 v[82:85], v[150:153], v[194:197], v[82:85]
	v_mfma_f32_16x16x32_bf16 v[70:73], v[142:145], v[202:205], v[70:73]
	v_mfma_f32_16x16x32_bf16 v[66:69], v[150:153], v[202:205], v[66:69]
	v_mfma_f32_16x16x32_bf16 v[118:121], v[146:149], v[178:181], v[118:121]
	v_mfma_f32_16x16x32_bf16 v[114:117], v[154:157], v[178:181], v[114:117]
	v_mfma_f32_16x16x32_bf16 v[102:105], v[146:149], v[186:189], v[102:105]
	v_mfma_f32_16x16x32_bf16 v[98:101], v[154:157], v[186:189], v[98:101]
	v_mfma_f32_16x16x32_bf16 v[86:89], v[146:149], v[198:201], v[86:89]
	v_mfma_f32_16x16x32_bf16 v[82:85], v[154:157], v[198:201], v[82:85]
	v_mfma_f32_16x16x32_bf16 v[70:73], v[146:149], v[206:209], v[70:73]
	v_mfma_f32_16x16x32_bf16 v[66:69], v[154:157], v[206:209], v[66:69]
	s_setprio 0
	s_setprio 1
	v_mfma_f32_16x16x32_bf16 v[46:49], v[158:161], v[174:177], v[46:49]
	v_mfma_f32_16x16x32_bf16 v[42:45], v[166:169], v[174:177], v[42:45]
	v_mfma_f32_16x16x32_bf16 v[30:33], v[158:161], v[182:185], v[30:33]
	v_mfma_f32_16x16x32_bf16 v[26:29], v[166:169], v[182:185], v[26:29]
	v_mfma_f32_16x16x32_bf16 v[14:17], v[158:161], v[194:197], v[14:17]
	v_mfma_f32_16x16x32_bf16 v[10:13], v[166:169], v[194:197], v[10:13]
	v_mfma_f32_16x16x32_bf16 v[6:9], v[158:161], v[202:205], v[6:9]
	v_mfma_f32_16x16x32_bf16 v[2:5], v[166:169], v[202:205], v[2:5]
	v_mfma_f32_16x16x32_bf16 v[46:49], v[162:165], v[178:181], v[46:49]
	v_mfma_f32_16x16x32_bf16 v[42:45], v[170:173], v[178:181], v[42:45]
	v_mfma_f32_16x16x32_bf16 v[30:33], v[162:165], v[186:189], v[30:33]
	v_mfma_f32_16x16x32_bf16 v[26:29], v[170:173], v[186:189], v[26:29]
	v_mfma_f32_16x16x32_bf16 v[14:17], v[162:165], v[198:201], v[14:17]
	v_mfma_f32_16x16x32_bf16 v[10:13], v[170:173], v[198:201], v[10:13]
	v_mfma_f32_16x16x32_bf16 v[6:9], v[162:165], v[206:209], v[6:9]
	v_mfma_f32_16x16x32_bf16 v[2:5], v[170:173], v[206:209], v[2:5]
	s_barrier
	s_setprio 0
	s_add_i32 s48, s82, s61
	s_mov_b32 m0, s48
	ds_read_b128 v[174:177], v138 offset:16384
	ds_read_b128 v[178:181], v138 offset:17408
	ds_read_b128 v[182:185], v138 offset:18432
	ds_read_b128 v[186:189], v138 offset:19456
	ds_read_b128 v[194:197], v138 offset:20480
	ds_read_b128 v[198:201], v138 offset:21504
	ds_read_b128 v[202:205], v138 offset:22528
	ds_read_b128 v[206:209], v138 offset:23552
	s_nop 0
	global_load_lds_dwordx4 v0, s[54:55]
	s_add_i32 m0, s48, 0x2000
	s_add_u32 s48, s54, s26
	s_addc_u32 s49, s55, s27
	s_add_i32 s82, s83, s61
	s_nop 0
	global_load_lds_dwordx4 v134, s[54:55]
	s_mov_b32 m0, s82
	s_nop 0
	global_load_lds_dwordx4 v0, s[48:49]
	s_add_i32 m0, s82, 0x2000
	s_nop 0
	global_load_lds_dwordx4 v134, s[48:49]
	s_mov_b32 m0, s62
	s_nop 0
	global_load_lds_dwordx4 v130, s[52:53]
	s_mov_b32 m0, s63
	s_nop 0
	global_load_lds_dwordx4 v132, s[52:53]
	s_waitcnt vmcnt(8)
	s_waitcnt lgkmcnt(0)
	s_setprio 1
	s_barrier
	v_mfma_f32_16x16x32_bf16 v[126:129], v[142:145], v[174:177], v[126:129]
	v_mfma_f32_16x16x32_bf16 v[122:125], v[150:153], v[174:177], v[122:125]
	v_mfma_f32_16x16x32_bf16 v[110:113], v[142:145], v[182:185], v[110:113]
	v_mfma_f32_16x16x32_bf16 v[106:109], v[150:153], v[182:185], v[106:109]
	v_mfma_f32_16x16x32_bf16 v[94:97], v[142:145], v[194:197], v[94:97]
	v_mfma_f32_16x16x32_bf16 v[90:93], v[150:153], v[194:197], v[90:93]
	v_mfma_f32_16x16x32_bf16 v[78:81], v[142:145], v[202:205], v[78:81]
	v_mfma_f32_16x16x32_bf16 v[74:77], v[150:153], v[202:205], v[74:77]
	v_mfma_f32_16x16x32_bf16 v[126:129], v[146:149], v[178:181], v[126:129]
	v_mfma_f32_16x16x32_bf16 v[122:125], v[154:157], v[178:181], v[122:125]
	v_mfma_f32_16x16x32_bf16 v[110:113], v[146:149], v[186:189], v[110:113]
	v_mfma_f32_16x16x32_bf16 v[106:109], v[154:157], v[186:189], v[106:109]
	v_mfma_f32_16x16x32_bf16 v[94:97], v[146:149], v[198:201], v[94:97]
	v_mfma_f32_16x16x32_bf16 v[90:93], v[154:157], v[198:201], v[90:93]
	v_mfma_f32_16x16x32_bf16 v[78:81], v[146:149], v[206:209], v[78:81]
	v_mfma_f32_16x16x32_bf16 v[74:77], v[154:157], v[206:209], v[74:77]
	s_setprio 0
	s_setprio 1
	v_mfma_f32_16x16x32_bf16 v[54:57], v[158:161], v[174:177], v[54:57]
	v_mfma_f32_16x16x32_bf16 v[50:53], v[166:169], v[174:177], v[50:53]
	v_mfma_f32_16x16x32_bf16 v[38:41], v[158:161], v[182:185], v[38:41]
	v_mfma_f32_16x16x32_bf16 v[34:37], v[166:169], v[182:185], v[34:37]
	v_mfma_f32_16x16x32_bf16 v[22:25], v[158:161], v[194:197], v[22:25]
	v_mfma_f32_16x16x32_bf16 v[18:21], v[166:169], v[194:197], v[18:21]
	v_mfma_f32_16x16x32_bf16 v[58:61], v[158:161], v[202:205], v[58:61]
	v_mfma_f32_16x16x32_bf16 v[62:65], v[166:169], v[202:205], v[62:65]
	v_mfma_f32_16x16x32_bf16 v[54:57], v[162:165], v[178:181], v[54:57]
	v_mfma_f32_16x16x32_bf16 v[50:53], v[170:173], v[178:181], v[50:53]
	v_mfma_f32_16x16x32_bf16 v[38:41], v[162:165], v[186:189], v[38:41]
	v_mfma_f32_16x16x32_bf16 v[34:37], v[170:173], v[186:189], v[34:37]
	v_mfma_f32_16x16x32_bf16 v[22:25], v[162:165], v[198:201], v[22:25]
	v_mfma_f32_16x16x32_bf16 v[18:21], v[170:173], v[198:201], v[18:21]
	v_mfma_f32_16x16x32_bf16 v[58:61], v[162:165], v[206:209], v[58:61]
	v_mfma_f32_16x16x32_bf16 v[62:65], v[170:173], v[206:209], v[62:65]
	s_barrier
	s_setprio 0
	s_add_i32 s84, 0, 0x18000
	v_add_u32_e32 v131, s84, v137
	s_add_i32 s85, 0, 0x1c000
	ds_read_b128 v[142:145], v131
	ds_read_b128 v[146:149], v131 offset:1024
	ds_read_b128 v[150:153], v131 offset:2048
	ds_read_b128 v[154:157], v131 offset:3072
	v_add_u32_e32 v131, s85, v137
	ds_read_b128 v[158:161], v131
	ds_read_b128 v[162:165], v131 offset:1024
	ds_read_b128 v[166:169], v131 offset:2048
	ds_read_b128 v[170:173], v131 offset:3072
	s_add_u32 s82, s52, s26
	s_addc_u32 s83, s53, s27
	s_mov_b32 m0, s64
	ds_read_b128 v[174:177], v138 offset:32768
	ds_read_b128 v[178:181], v138 offset:33792
	ds_read_b128 v[182:185], v138 offset:34816
	ds_read_b128 v[186:189], v138 offset:35840
	ds_read_b128 v[194:197], v138 offset:36864
	ds_read_b128 v[198:201], v138 offset:37888
	ds_read_b128 v[202:205], v138 offset:38912
	ds_read_b128 v[206:209], v138 offset:39936
	s_nop 0
	global_load_lds_dwordx4 v130, s[82:83]
	s_mov_b32 m0, s65
	s_nop 0
	global_load_lds_dwordx4 v132, s[82:83]
	s_waitcnt vmcnt(8)
	s_waitcnt lgkmcnt(0)
	s_setprio 1
	s_barrier
	v_mfma_f32_16x16x32_bf16 v[118:121], v[142:145], v[174:177], v[118:121]
	v_mfma_f32_16x16x32_bf16 v[114:117], v[150:153], v[174:177], v[114:117]
	v_mfma_f32_16x16x32_bf16 v[102:105], v[142:145], v[182:185], v[102:105]
	v_mfma_f32_16x16x32_bf16 v[98:101], v[150:153], v[182:185], v[98:101]
	v_mfma_f32_16x16x32_bf16 v[86:89], v[142:145], v[194:197], v[86:89]
	v_mfma_f32_16x16x32_bf16 v[82:85], v[150:153], v[194:197], v[82:85]
	v_mfma_f32_16x16x32_bf16 v[70:73], v[142:145], v[202:205], v[70:73]
	v_mfma_f32_16x16x32_bf16 v[66:69], v[150:153], v[202:205], v[66:69]
	v_mfma_f32_16x16x32_bf16 v[118:121], v[146:149], v[178:181], v[118:121]
	v_mfma_f32_16x16x32_bf16 v[114:117], v[154:157], v[178:181], v[114:117]
	v_mfma_f32_16x16x32_bf16 v[102:105], v[146:149], v[186:189], v[102:105]
	v_mfma_f32_16x16x32_bf16 v[98:101], v[154:157], v[186:189], v[98:101]
	v_mfma_f32_16x16x32_bf16 v[86:89], v[146:149], v[198:201], v[86:89]
	v_mfma_f32_16x16x32_bf16 v[82:85], v[154:157], v[198:201], v[82:85]
	v_mfma_f32_16x16x32_bf16 v[70:73], v[146:149], v[206:209], v[70:73]
	v_mfma_f32_16x16x32_bf16 v[66:69], v[154:157], v[206:209], v[66:69]
	s_setprio 0
	s_setprio 1
	v_mfma_f32_16x16x32_bf16 v[46:49], v[158:161], v[174:177], v[46:49]
	v_mfma_f32_16x16x32_bf16 v[42:45], v[166:169], v[174:177], v[42:45]
	v_mfma_f32_16x16x32_bf16 v[30:33], v[158:161], v[182:185], v[30:33]
	v_mfma_f32_16x16x32_bf16 v[26:29], v[166:169], v[182:185], v[26:29]
	v_mfma_f32_16x16x32_bf16 v[14:17], v[158:161], v[194:197], v[14:17]
	v_mfma_f32_16x16x32_bf16 v[10:13], v[166:169], v[194:197], v[10:13]
	v_mfma_f32_16x16x32_bf16 v[6:9], v[158:161], v[202:205], v[6:9]
	v_mfma_f32_16x16x32_bf16 v[2:5], v[166:169], v[202:205], v[2:5]
	v_mfma_f32_16x16x32_bf16 v[46:49], v[162:165], v[178:181], v[46:49]
	v_mfma_f32_16x16x32_bf16 v[42:45], v[170:173], v[178:181], v[42:45]
	v_mfma_f32_16x16x32_bf16 v[30:33], v[162:165], v[186:189], v[30:33]
	v_mfma_f32_16x16x32_bf16 v[26:29], v[170:173], v[186:189], v[26:29]
	v_mfma_f32_16x16x32_bf16 v[14:17], v[162:165], v[198:201], v[14:17]
	v_mfma_f32_16x16x32_bf16 v[10:13], v[170:173], v[198:201], v[10:13]
	v_mfma_f32_16x16x32_bf16 v[6:9], v[162:165], v[206:209], v[6:9]
	v_mfma_f32_16x16x32_bf16 v[2:5], v[170:173], v[206:209], v[2:5]
	s_barrier
	s_setprio 0
	ds_read_b128 v[174:177], v138 offset:49152
	ds_read_b128 v[178:181], v138 offset:50176
	ds_read_b128 v[182:185], v138 offset:51200
	ds_read_b128 v[186:189], v138 offset:52224
	ds_read_b128 v[194:197], v138 offset:53248
	ds_read_b128 v[198:201], v138 offset:54272
	ds_read_b128 v[202:205], v138 offset:55296
	ds_read_b128 v[206:209], v138 offset:56320
	s_add_i32 s82, s84, s61
	v_lshl_add_u64 v[190:191], s[54:55], 0, v[0:1]
	v_lshl_add_u64 v[190:191], v[190:191], 0, s[16:17]
	s_mov_b32 m0, s82
	v_mov_b32_e32 v135, v1
	global_load_lds_dwordx4 v[190:191], off
	s_add_i32 m0, s82, 0x2000
	v_lshl_add_u64 v[190:191], s[54:55], 0, v[134:135]
	v_lshl_add_u64 v[190:191], v[190:191], 0, s[16:17]
	global_load_lds_dwordx4 v[190:191], off
	s_add_i32 s54, s85, s61
	v_lshl_add_u64 v[190:191], s[48:49], 0, v[0:1]
	v_lshl_add_u64 v[190:191], v[190:191], 0, s[16:17]
	s_mov_b32 m0, s54
	v_mov_b32_e32 v131, v1
	global_load_lds_dwordx4 v[190:191], off
	s_add_i32 m0, s54, 0x2000
	v_lshl_add_u64 v[190:191], s[48:49], 0, v[134:135]
	v_lshl_add_u64 v[190:191], v[190:191], 0, s[16:17]
	global_load_lds_dwordx4 v[190:191], off
	s_mov_b32 m0, s66
	v_lshl_add_u64 v[190:191], s[52:53], 0, v[130:131]
	v_lshl_add_u64 v[190:191], v[190:191], 0, s[16:17]
	v_mov_b32_e32 v133, v1
	global_load_lds_dwordx4 v[190:191], off
	s_mov_b32 m0, s67
	v_lshl_add_u64 v[190:191], s[52:53], 0, v[132:133]
	v_lshl_add_u64 v[190:191], v[190:191], 0, s[16:17]
	global_load_lds_dwordx4 v[190:191], off
	s_waitcnt vmcnt(8)
	s_waitcnt lgkmcnt(0)
	s_setprio 1
	s_barrier
	v_mfma_f32_16x16x32_bf16 v[126:129], v[142:145], v[174:177], v[126:129]
	v_mfma_f32_16x16x32_bf16 v[122:125], v[150:153], v[174:177], v[122:125]
	v_mfma_f32_16x16x32_bf16 v[110:113], v[142:145], v[182:185], v[110:113]
	v_mfma_f32_16x16x32_bf16 v[106:109], v[150:153], v[182:185], v[106:109]
	v_mfma_f32_16x16x32_bf16 v[94:97], v[142:145], v[194:197], v[94:97]
	v_mfma_f32_16x16x32_bf16 v[90:93], v[150:153], v[194:197], v[90:93]
	v_mfma_f32_16x16x32_bf16 v[78:81], v[142:145], v[202:205], v[78:81]
	v_mfma_f32_16x16x32_bf16 v[74:77], v[150:153], v[202:205], v[74:77]
	v_mfma_f32_16x16x32_bf16 v[126:129], v[146:149], v[178:181], v[126:129]
	v_mfma_f32_16x16x32_bf16 v[122:125], v[154:157], v[178:181], v[122:125]
	v_mfma_f32_16x16x32_bf16 v[110:113], v[146:149], v[186:189], v[110:113]
	v_mfma_f32_16x16x32_bf16 v[106:109], v[154:157], v[186:189], v[106:109]
	v_mfma_f32_16x16x32_bf16 v[94:97], v[146:149], v[198:201], v[94:97]
	v_mfma_f32_16x16x32_bf16 v[90:93], v[154:157], v[198:201], v[90:93]
	v_mfma_f32_16x16x32_bf16 v[78:81], v[146:149], v[206:209], v[78:81]
	v_mfma_f32_16x16x32_bf16 v[74:77], v[154:157], v[206:209], v[74:77]
	s_setprio 0
	s_setprio 1
	v_mfma_f32_16x16x32_bf16 v[54:57], v[158:161], v[174:177], v[54:57]
	v_mfma_f32_16x16x32_bf16 v[50:53], v[166:169], v[174:177], v[50:53]
	v_mfma_f32_16x16x32_bf16 v[38:41], v[158:161], v[182:185], v[38:41]
	v_mfma_f32_16x16x32_bf16 v[34:37], v[166:169], v[182:185], v[34:37]
	v_mfma_f32_16x16x32_bf16 v[22:25], v[158:161], v[194:197], v[22:25]
	v_mfma_f32_16x16x32_bf16 v[18:21], v[166:169], v[194:197], v[18:21]
	v_mfma_f32_16x16x32_bf16 v[58:61], v[158:161], v[202:205], v[58:61]
	v_mfma_f32_16x16x32_bf16 v[62:65], v[166:169], v[202:205], v[62:65]
	v_mfma_f32_16x16x32_bf16 v[54:57], v[162:165], v[178:181], v[54:57]
	v_mfma_f32_16x16x32_bf16 v[50:53], v[170:173], v[178:181], v[50:53]
	v_mfma_f32_16x16x32_bf16 v[38:41], v[162:165], v[186:189], v[38:41]
	v_mfma_f32_16x16x32_bf16 v[34:37], v[170:173], v[186:189], v[34:37]
	v_mfma_f32_16x16x32_bf16 v[22:25], v[162:165], v[198:201], v[22:25]
	v_mfma_f32_16x16x32_bf16 v[18:21], v[170:173], v[198:201], v[18:21]
	v_mfma_f32_16x16x32_bf16 v[58:61], v[162:165], v[206:209], v[58:61]
	v_mfma_f32_16x16x32_bf16 v[62:65], v[170:173], v[206:209], v[62:65]
	s_barrier
	s_setprio 0
	s_add_u32 s47, s47, 0x100
	s_addc_u32 s80, s80, 0
	s_cmp_ge_i32 s81, s68
	s_mov_b64 s[48:49], s[50:51]
	s_mov_b32 s52, s81
	s_cbranch_scc0 .LBB0_531

.LBB0_707:
	s_add_i32 s74, s52, 2
	s_add_u32 s50, s48, 0x100
	s_addc_u32 s51, s49, 0
	s_add_i32 s75, 0, 0x10000
	s_cmp_eq_u32 s64, s52
	s_cselect_b32 s53, s41, s51
	s_cselect_b32 s52, s40, s50
	v_add_u32_e32 v139, s75, v148
	s_cselect_b32 s55, s47, s73
	s_cselect_b32 s54, s46, s72
	s_add_i32 s76, 0, 0x14000
	ds_read_b128 v[130:133], v139
	ds_read_b128 v[134:137], v139 offset:1024
	ds_read_b128 v[140:143], v139 offset:2048
	ds_read_b128 v[150:153], v139 offset:3072
	v_add_u32_e32 v139, s76, v148
	ds_read_b128 v[154:157], v139
	ds_read_b128 v[158:161], v139 offset:1024
	ds_read_b128 v[162:165], v139 offset:2048
	ds_read_b128 v[166:169], v139 offset:3072
	s_add_u32 s48, s48, s66
	s_addc_u32 s49, s49, s67
	s_add_i32 m0, s15, 0xc000
	ds_read_b128 v[170:173], v149
	ds_read_b128 v[174:177], v149 offset:1024
	ds_read_b128 v[178:181], v149 offset:2048
	ds_read_b128 v[182:185], v149 offset:3072
	ds_read_b128 v[186:189], v149 offset:4096
	ds_read_b128 v[194:197], v149 offset:5120
	ds_read_b128 v[198:201], v149 offset:6144
	ds_read_b128 v[202:205], v149 offset:7168
	s_nop 0
	global_load_lds_dwordx4 v0, s[48:49]
	s_add_i32 m0, s15, 0xe000
	s_nop 0
	global_load_lds_dwordx4 v138, s[48:49]
	s_waitcnt vmcnt(8)
	s_waitcnt lgkmcnt(0)
	s_setprio 1
	s_barrier
	v_mfma_f32_16x16x32_bf16 v[122:125], v[130:133], v[170:173], v[122:125]
	v_mfma_f32_16x16x32_bf16 v[126:129], v[140:143], v[170:173], v[126:129]
	v_mfma_f32_16x16x32_bf16 v[118:121], v[130:133], v[178:181], v[118:121]
	v_mfma_f32_16x16x32_bf16 v[114:117], v[140:143], v[178:181], v[114:117]
	v_mfma_f32_16x16x32_bf16 v[102:105], v[130:133], v[186:189], v[102:105]
	v_mfma_f32_16x16x32_bf16 v[98:101], v[140:143], v[186:189], v[98:101]
	v_mfma_f32_16x16x32_bf16 v[86:89], v[130:133], v[198:201], v[86:89]
	v_mfma_f32_16x16x32_bf16 v[82:85], v[140:143], v[198:201], v[82:85]
	v_mfma_f32_16x16x32_bf16 v[122:125], v[134:137], v[174:177], v[122:125]
	v_mfma_f32_16x16x32_bf16 v[126:129], v[150:153], v[174:177], v[126:129]
	v_mfma_f32_16x16x32_bf16 v[118:121], v[134:137], v[182:185], v[118:121]
	v_mfma_f32_16x16x32_bf16 v[114:117], v[150:153], v[182:185], v[114:117]
	v_mfma_f32_16x16x32_bf16 v[102:105], v[134:137], v[194:197], v[102:105]
	v_mfma_f32_16x16x32_bf16 v[98:101], v[150:153], v[194:197], v[98:101]
	v_mfma_f32_16x16x32_bf16 v[86:89], v[134:137], v[202:205], v[86:89]
	v_mfma_f32_16x16x32_bf16 v[82:85], v[150:153], v[202:205], v[82:85]
	s_setprio 0
	s_setprio 1
	v_mfma_f32_16x16x32_bf16 v[58:61], v[154:157], v[170:173], v[58:61]
	v_mfma_f32_16x16x32_bf16 v[62:65], v[162:165], v[170:173], v[62:65]
	v_mfma_f32_16x16x32_bf16 v[54:57], v[154:157], v[178:181], v[54:57]
	v_mfma_f32_16x16x32_bf16 v[50:53], v[162:165], v[178:181], v[50:53]
	v_mfma_f32_16x16x32_bf16 v[38:41], v[154:157], v[186:189], v[38:41]
	v_mfma_f32_16x16x32_bf16 v[34:37], v[162:165], v[186:189], v[34:37]
	v_mfma_f32_16x16x32_bf16 v[14:17], v[154:157], v[198:201], v[14:17]
	v_mfma_f32_16x16x32_bf16 v[10:13], v[162:165], v[198:201], v[10:13]
	v_mfma_f32_16x16x32_bf16 v[58:61], v[158:161], v[174:177], v[58:61]
	v_mfma_f32_16x16x32_bf16 v[62:65], v[166:169], v[174:177], v[62:65]
	v_mfma_f32_16x16x32_bf16 v[54:57], v[158:161], v[182:185], v[54:57]
	v_mfma_f32_16x16x32_bf16 v[50:53], v[166:169], v[182:185], v[50:53]
	v_mfma_f32_16x16x32_bf16 v[38:41], v[158:161], v[194:197], v[38:41]
	v_mfma_f32_16x16x32_bf16 v[34:37], v[166:169], v[194:197], v[34:37]
	v_mfma_f32_16x16x32_bf16 v[14:17], v[158:161], v[202:205], v[14:17]
	v_mfma_f32_16x16x32_bf16 v[10:13], v[166:169], v[202:205], v[10:13]
	s_barrier
	s_setprio 0
	s_add_i32 s48, s75, s14
	s_mov_b32 m0, s48
	ds_read_b128 v[170:173], v149 offset:16384
	ds_read_b128 v[174:177], v149 offset:17408
	ds_read_b128 v[178:181], v149 offset:18432
	ds_read_b128 v[182:185], v149 offset:19456
	ds_read_b128 v[186:189], v149 offset:20480
	ds_read_b128 v[194:197], v149 offset:21504
	ds_read_b128 v[198:201], v149 offset:22528
	ds_read_b128 v[202:205], v149 offset:23552
	s_nop 0
	global_load_lds_dwordx4 v147, s[54:55]
	s_add_i32 m0, s48, 0x2000
	s_add_u32 s48, s54, 0x4000
	s_addc_u32 s49, s55, 0
	s_add_i32 s75, s76, s14
	s_nop 0
	global_load_lds_dwordx4 v146, s[54:55]
	s_mov_b32 m0, s75
	s_nop 0
	global_load_lds_dwordx4 v147, s[48:49]
	s_add_i32 m0, s75, 0x2000
	s_nop 0
	global_load_lds_dwordx4 v146, s[48:49]
	s_mov_b32 m0, s15
	s_nop 0
	global_load_lds_dwordx4 v0, s[52:53]
	s_mov_b32 m0, s18
	s_nop 0
	global_load_lds_dwordx4 v138, s[52:53]
	s_waitcnt vmcnt(8)
	s_waitcnt lgkmcnt(0)
	s_setprio 1
	s_barrier
	v_mfma_f32_16x16x32_bf16 v[110:113], v[130:133], v[170:173], v[110:113]
	v_mfma_f32_16x16x32_bf16 v[106:109], v[140:143], v[170:173], v[106:109]
	v_mfma_f32_16x16x32_bf16 v[94:97], v[130:133], v[178:181], v[94:97]
	v_mfma_f32_16x16x32_bf16 v[90:93], v[140:143], v[178:181], v[90:93]
	v_mfma_f32_16x16x32_bf16 v[78:81], v[130:133], v[186:189], v[78:81]
	v_mfma_f32_16x16x32_bf16 v[74:77], v[140:143], v[186:189], v[74:77]
	v_mfma_f32_16x16x32_bf16 v[70:73], v[130:133], v[198:201], v[70:73]
	v_mfma_f32_16x16x32_bf16 v[66:69], v[140:143], v[198:201], v[66:69]
	v_mfma_f32_16x16x32_bf16 v[110:113], v[134:137], v[174:177], v[110:113]
	v_mfma_f32_16x16x32_bf16 v[106:109], v[150:153], v[174:177], v[106:109]
	v_mfma_f32_16x16x32_bf16 v[94:97], v[134:137], v[182:185], v[94:97]
	v_mfma_f32_16x16x32_bf16 v[90:93], v[150:153], v[182:185], v[90:93]
	v_mfma_f32_16x16x32_bf16 v[78:81], v[134:137], v[194:197], v[78:81]
	v_mfma_f32_16x16x32_bf16 v[74:77], v[150:153], v[194:197], v[74:77]
	v_mfma_f32_16x16x32_bf16 v[70:73], v[134:137], v[202:205], v[70:73]
	v_mfma_f32_16x16x32_bf16 v[66:69], v[150:153], v[202:205], v[66:69]
	s_setprio 0
	s_setprio 1
	v_mfma_f32_16x16x32_bf16 v[46:49], v[154:157], v[170:173], v[46:49]
	v_mfma_f32_16x16x32_bf16 v[42:45], v[162:165], v[170:173], v[42:45]
	v_mfma_f32_16x16x32_bf16 v[26:29], v[154:157], v[178:181], v[26:29]
	v_mfma_f32_16x16x32_bf16 v[22:25], v[162:165], v[178:181], v[22:25]
	v_mfma_f32_16x16x32_bf16 v[6:9], v[154:157], v[186:189], v[6:9]
	v_mfma_f32_16x16x32_bf16 v[2:5], v[162:165], v[186:189], v[2:5]
	v_mfma_f32_16x16x32_bf16 v[18:21], v[154:157], v[198:201], v[18:21]
	v_mfma_f32_16x16x32_bf16 v[30:33], v[162:165], v[198:201], v[30:33]
	v_mfma_f32_16x16x32_bf16 v[46:49], v[158:161], v[174:177], v[46:49]
	v_mfma_f32_16x16x32_bf16 v[42:45], v[166:169], v[174:177], v[42:45]
	v_mfma_f32_16x16x32_bf16 v[26:29], v[158:161], v[182:185], v[26:29]
	v_mfma_f32_16x16x32_bf16 v[22:25], v[166:169], v[182:185], v[22:25]
	v_mfma_f32_16x16x32_bf16 v[6:9], v[158:161], v[194:197], v[6:9]
	v_mfma_f32_16x16x32_bf16 v[2:5], v[166:169], v[194:197], v[2:5]
	v_mfma_f32_16x16x32_bf16 v[18:21], v[158:161], v[202:205], v[18:21]
	v_mfma_f32_16x16x32_bf16 v[30:33], v[166:169], v[202:205], v[30:33]
	s_barrier
	s_setprio 0
	s_add_i32 s75, 0, 0x18000
	v_add_u32_e32 v139, s75, v148
	s_add_i32 s76, 0, 0x1c000
	ds_read_b128 v[130:133], v139
	ds_read_b128 v[134:137], v139 offset:1024
	ds_read_b128 v[140:143], v139 offset:2048
	ds_read_b128 v[150:153], v139 offset:3072
	v_add_u32_e32 v139, s76, v148
	ds_read_b128 v[154:157], v139
	ds_read_b128 v[158:161], v139 offset:1024
	ds_read_b128 v[162:165], v139 offset:2048
	ds_read_b128 v[166:169], v139 offset:3072
	s_add_u32 s48, s52, s26
	s_addc_u32 s49, s53, s27
	s_mov_b32 m0, s20
	ds_read_b128 v[170:173], v149 offset:32768
	ds_read_b128 v[174:177], v149 offset:33792
	ds_read_b128 v[178:181], v149 offset:34816
	ds_read_b128 v[182:185], v149 offset:35840
	ds_read_b128 v[186:189], v149 offset:36864
	ds_read_b128 v[194:197], v149 offset:37888
	ds_read_b128 v[198:201], v149 offset:38912
	ds_read_b128 v[202:205], v149 offset:39936
	s_nop 0
	global_load_lds_dwordx4 v0, s[48:49]
	s_mov_b32 m0, s21
	s_nop 0
	global_load_lds_dwordx4 v138, s[48:49]
	s_waitcnt vmcnt(8)
	s_waitcnt lgkmcnt(0)
	s_setprio 1
	s_barrier
	v_mfma_f32_16x16x32_bf16 v[122:125], v[130:133], v[170:173], v[122:125]
	v_mfma_f32_16x16x32_bf16 v[126:129], v[140:143], v[170:173], v[126:129]
	v_mfma_f32_16x16x32_bf16 v[118:121], v[130:133], v[178:181], v[118:121]
	v_mfma_f32_16x16x32_bf16 v[114:117], v[140:143], v[178:181], v[114:117]
	v_mfma_f32_16x16x32_bf16 v[102:105], v[130:133], v[186:189], v[102:105]
	v_mfma_f32_16x16x32_bf16 v[98:101], v[140:143], v[186:189], v[98:101]
	v_mfma_f32_16x16x32_bf16 v[86:89], v[130:133], v[198:201], v[86:89]
	v_mfma_f32_16x16x32_bf16 v[82:85], v[140:143], v[198:201], v[82:85]
	v_mfma_f32_16x16x32_bf16 v[122:125], v[134:137], v[174:177], v[122:125]
	v_mfma_f32_16x16x32_bf16 v[126:129], v[150:153], v[174:177], v[126:129]
	v_mfma_f32_16x16x32_bf16 v[118:121], v[134:137], v[182:185], v[118:121]
	v_mfma_f32_16x16x32_bf16 v[114:117], v[150:153], v[182:185], v[114:117]
	v_mfma_f32_16x16x32_bf16 v[102:105], v[134:137], v[194:197], v[102:105]
	v_mfma_f32_16x16x32_bf16 v[98:101], v[150:153], v[194:197], v[98:101]
	v_mfma_f32_16x16x32_bf16 v[86:89], v[134:137], v[202:205], v[86:89]
	v_mfma_f32_16x16x32_bf16 v[82:85], v[150:153], v[202:205], v[82:85]
	s_setprio 0
	s_setprio 1
	v_mfma_f32_16x16x32_bf16 v[58:61], v[154:157], v[170:173], v[58:61]
	v_mfma_f32_16x16x32_bf16 v[62:65], v[162:165], v[170:173], v[62:65]
	v_mfma_f32_16x16x32_bf16 v[54:57], v[154:157], v[178:181], v[54:57]
	v_mfma_f32_16x16x32_bf16 v[50:53], v[162:165], v[178:181], v[50:53]
	v_mfma_f32_16x16x32_bf16 v[38:41], v[154:157], v[186:189], v[38:41]
	v_mfma_f32_16x16x32_bf16 v[34:37], v[162:165], v[186:189], v[34:37]
	v_mfma_f32_16x16x32_bf16 v[14:17], v[154:157], v[198:201], v[14:17]
	v_mfma_f32_16x16x32_bf16 v[10:13], v[162:165], v[198:201], v[10:13]
	v_mfma_f32_16x16x32_bf16 v[58:61], v[158:161], v[174:177], v[58:61]
	v_mfma_f32_16x16x32_bf16 v[62:65], v[166:169], v[174:177], v[62:65]
	v_mfma_f32_16x16x32_bf16 v[54:57], v[158:161], v[182:185], v[54:57]
	v_mfma_f32_16x16x32_bf16 v[50:53], v[166:169], v[182:185], v[50:53]
	v_mfma_f32_16x16x32_bf16 v[38:41], v[158:161], v[194:197], v[38:41]
	v_mfma_f32_16x16x32_bf16 v[34:37], v[166:169], v[194:197], v[34:37]
	v_mfma_f32_16x16x32_bf16 v[14:17], v[158:161], v[202:205], v[14:17]
	v_mfma_f32_16x16x32_bf16 v[10:13], v[166:169], v[202:205], v[10:13]
	s_barrier
	s_setprio 0
	s_add_u32 s48, s54, 0x8000
	s_addc_u32 s49, s55, 0
	s_add_i32 s75, s75, s14
	s_mov_b32 m0, s75
	ds_read_b128 v[170:173], v149 offset:49152
	ds_read_b128 v[174:177], v149 offset:50176
	ds_read_b128 v[178:181], v149 offset:51200
	ds_read_b128 v[182:185], v149 offset:52224
	ds_read_b128 v[186:189], v149 offset:53248
	ds_read_b128 v[194:197], v149 offset:54272
	ds_read_b128 v[198:201], v149 offset:55296
	ds_read_b128 v[202:205], v149 offset:56320
	v_mov_b32_e32 v139, v1
	global_load_lds_dwordx4 v147, s[48:49]
	s_add_i32 m0, s75, 0x2000
	s_nop 0
	global_load_lds_dwordx4 v146, s[48:49]
	s_add_u32 s48, s54, 0xc000
	s_addc_u32 s49, s55, 0
	s_add_i32 s54, s76, s14
	s_mov_b32 m0, s54
	s_nop 0
	global_load_lds_dwordx4 v147, s[48:49]
	s_add_i32 m0, s54, 0x2000
	s_nop 0
	global_load_lds_dwordx4 v146, s[48:49]
	s_mov_b32 m0, s62
	v_lshl_add_u64 v[190:191], s[52:53], 0, v[0:1]
	v_lshl_add_u64 v[190:191], v[190:191], 0, s[16:17]
	global_load_lds_dwordx4 v[190:191], off
	s_mov_b32 m0, s63
	v_lshl_add_u64 v[190:191], s[52:53], 0, v[138:139]
	v_lshl_add_u64 v[190:191], v[190:191], 0, s[16:17]
	global_load_lds_dwordx4 v[190:191], off
	s_waitcnt vmcnt(8)
	s_waitcnt lgkmcnt(0)
	s_setprio 1
	s_barrier
	v_mfma_f32_16x16x32_bf16 v[110:113], v[130:133], v[170:173], v[110:113]
	v_mfma_f32_16x16x32_bf16 v[106:109], v[140:143], v[170:173], v[106:109]
	v_mfma_f32_16x16x32_bf16 v[94:97], v[130:133], v[178:181], v[94:97]
	v_mfma_f32_16x16x32_bf16 v[90:93], v[140:143], v[178:181], v[90:93]
	v_mfma_f32_16x16x32_bf16 v[78:81], v[130:133], v[186:189], v[78:81]
	v_mfma_f32_16x16x32_bf16 v[74:77], v[140:143], v[186:189], v[74:77]
	v_mfma_f32_16x16x32_bf16 v[70:73], v[130:133], v[198:201], v[70:73]
	v_mfma_f32_16x16x32_bf16 v[66:69], v[140:143], v[198:201], v[66:69]
	v_mfma_f32_16x16x32_bf16 v[110:113], v[134:137], v[174:177], v[110:113]
	v_mfma_f32_16x16x32_bf16 v[106:109], v[150:153], v[174:177], v[106:109]
	v_mfma_f32_16x16x32_bf16 v[94:97], v[134:137], v[182:185], v[94:97]
	v_mfma_f32_16x16x32_bf16 v[90:93], v[150:153], v[182:185], v[90:93]
	v_mfma_f32_16x16x32_bf16 v[78:81], v[134:137], v[194:197], v[78:81]
	v_mfma_f32_16x16x32_bf16 v[74:77], v[150:153], v[194:197], v[74:77]
	v_mfma_f32_16x16x32_bf16 v[70:73], v[134:137], v[202:205], v[70:73]
	v_mfma_f32_16x16x32_bf16 v[66:69], v[150:153], v[202:205], v[66:69]
	s_setprio 0
	s_setprio 1
	v_mfma_f32_16x16x32_bf16 v[46:49], v[154:157], v[170:173], v[46:49]
	v_mfma_f32_16x16x32_bf16 v[42:45], v[162:165], v[170:173], v[42:45]
	v_mfma_f32_16x16x32_bf16 v[26:29], v[154:157], v[178:181], v[26:29]
	v_mfma_f32_16x16x32_bf16 v[22:25], v[162:165], v[178:181], v[22:25]
	v_mfma_f32_16x16x32_bf16 v[6:9], v[154:157], v[186:189], v[6:9]
	v_mfma_f32_16x16x32_bf16 v[2:5], v[162:165], v[186:189], v[2:5]
	v_mfma_f32_16x16x32_bf16 v[18:21], v[154:157], v[198:201], v[18:21]
	v_mfma_f32_16x16x32_bf16 v[30:33], v[162:165], v[198:201], v[30:33]
	v_mfma_f32_16x16x32_bf16 v[46:49], v[158:161], v[174:177], v[46:49]
	v_mfma_f32_16x16x32_bf16 v[42:45], v[166:169], v[174:177], v[42:45]
	v_mfma_f32_16x16x32_bf16 v[26:29], v[158:161], v[182:185], v[26:29]
	v_mfma_f32_16x16x32_bf16 v[22:25], v[166:169], v[182:185], v[22:25]
	v_mfma_f32_16x16x32_bf16 v[6:9], v[158:161], v[194:197], v[6:9]
	v_mfma_f32_16x16x32_bf16 v[2:5], v[166:169], v[194:197], v[2:5]
	v_mfma_f32_16x16x32_bf16 v[18:21], v[158:161], v[202:205], v[18:21]
	v_mfma_f32_16x16x32_bf16 v[30:33], v[166:169], v[202:205], v[30:33]
	s_barrier
	s_setprio 0
	s_add_u32 s72, s72, 0x10000
	s_addc_u32 s73, s73, 0
	s_cmp_ge_i32 s74, s59
	s_mov_b64 s[48:49], s[50:51]
	s_mov_b32 s52, s74
	s_cbranch_scc0 .LBB0_707

.LBB0_890:
	s_add_u32 s34, s26, 0x10000
	s_addc_u32 s35, s27, 0
	s_and_b64 s[30:31], s[48:49], exec
	s_cselect_b32 s47, s41, s35
	s_cselect_b32 s46, s40, s34
	s_add_u32 s65, s28, 0x10000
	s_addc_u32 s66, s29, 0
	s_add_u32 s30, s46, 0x8000
	s_addc_u32 s31, s47, 0
	s_add_i32 s67, 0, 0x10000
	s_and_b64 s[34:35], s[48:49], exec
	s_cselect_b32 s35, s45, s66
	s_cselect_b32 s34, s44, s65
	s_add_i32 s70, 0, 0x14000
	v_add_u32_e32 v114, s67, v236
	v_add_u32_e32 v115, s70, v236
	ds_read_b128 v[2:5], v114
	s_waitcnt lgkmcnt(0)
	ds_read_b128 v[6:9], v114 offset:1024
	ds_read_b128 v[10:13], v114 offset:2048
	ds_read_b128 v[14:17], v114 offset:3072
	ds_read_b128 v[18:21], v115
	ds_read_b128 v[22:25], v115 offset:1024
	ds_read_b128 v[26:29], v115 offset:2048
	ds_read_b128 v[30:33], v115 offset:3072
	s_add_u32 s68, s26, 0xc000
	s_addc_u32 s69, s27, 0
	s_add_i32 s65, s20, 0xc000
	s_mov_b32 m0, s65
	s_add_i32 s66, s20, 0xe000
	ds_read_b128 v[34:37], v237
	ds_read_b128 v[38:41], v237 offset:1024
	ds_read_b128 v[42:45], v237 offset:2048
	ds_read_b128 v[46:49], v237 offset:3072
	ds_read_b128 v[50:53], v237 offset:4096
	ds_read_b128 v[54:57], v237 offset:5120
	ds_read_b128 v[58:61], v237 offset:6144
	ds_read_b128 v[62:65], v237 offset:7168
	s_nop 0
	global_load_lds_dwordx4 v235, s[68:69]
	s_mov_b32 m0, s66
	s_nop 0
	global_load_lds_dwordx4 v226, s[68:69]
	s_waitcnt vmcnt(8)
	s_waitcnt lgkmcnt(0)
	s_setprio 1
	s_barrier
	v_mfma_f32_16x16x32_bf16 v[90:93], v[2:5], v[58:61], 0
	v_mfma_f32_16x16x32_bf16 v[66:69], v[2:5], v[34:37], 0
	v_mfma_f32_16x16x32_bf16 v[70:73], v[10:13], v[34:37], 0
	v_mfma_f32_16x16x32_bf16 v[74:77], v[2:5], v[42:45], 0
	v_mfma_f32_16x16x32_bf16 v[78:81], v[10:13], v[42:45], 0
	v_mfma_f32_16x16x32_bf16 v[82:85], v[2:5], v[50:53], 0
	v_mfma_f32_16x16x32_bf16 v[86:89], v[10:13], v[50:53], 0
	v_mfma_f32_16x16x32_bf16 v[98:101], v[6:9], v[62:65], v[90:93]
	v_mfma_f32_16x16x32_bf16 v[90:93], v[10:13], v[58:61], 0
	v_mfma_f32_16x16x32_bf16 v[66:69], v[6:9], v[38:41], v[66:69]
	v_mfma_f32_16x16x32_bf16 v[70:73], v[14:17], v[38:41], v[70:73]
	v_mfma_f32_16x16x32_bf16 v[74:77], v[6:9], v[46:49], v[74:77]
	v_mfma_f32_16x16x32_bf16 v[78:81], v[14:17], v[46:49], v[78:81]
	v_mfma_f32_16x16x32_bf16 v[82:85], v[6:9], v[54:57], v[82:85]
	v_mfma_f32_16x16x32_bf16 v[86:89], v[14:17], v[54:57], v[86:89]
	v_mfma_f32_16x16x32_bf16 v[102:105], v[14:17], v[62:65], v[90:93]
	s_setprio 0
	s_setprio 1
	v_mfma_f32_16x16x32_bf16 v[90:93], v[18:21], v[34:37], 0
	v_mfma_f32_16x16x32_bf16 v[34:37], v[26:29], v[34:37], 0
	v_mfma_f32_16x16x32_bf16 v[118:121], v[22:25], v[38:41], v[90:93]
	v_mfma_f32_16x16x32_bf16 v[34:37], v[30:33], v[38:41], v[34:37]
	v_mfma_f32_16x16x32_bf16 v[38:41], v[18:21], v[42:45], 0
	v_mfma_f32_16x16x32_bf16 v[42:45], v[26:29], v[42:45], 0
	v_mfma_f32_16x16x32_bf16 v[38:41], v[22:25], v[46:49], v[38:41]
	v_mfma_f32_16x16x32_bf16 v[42:45], v[30:33], v[46:49], v[42:45]
	v_mfma_f32_16x16x32_bf16 v[46:49], v[18:21], v[50:53], 0
	v_mfma_f32_16x16x32_bf16 v[50:53], v[26:29], v[50:53], 0
	v_mfma_f32_16x16x32_bf16 v[46:49], v[22:25], v[54:57], v[46:49]
	v_mfma_f32_16x16x32_bf16 v[50:53], v[30:33], v[54:57], v[50:53]
	v_mfma_f32_16x16x32_bf16 v[54:57], v[18:21], v[58:61], 0
	v_mfma_f32_16x16x32_bf16 v[58:61], v[26:29], v[58:61], 0
	v_mfma_f32_16x16x32_bf16 v[54:57], v[22:25], v[62:65], v[54:57]
	v_mfma_f32_16x16x32_bf16 v[58:61], v[30:33], v[62:65], v[58:61]
	s_barrier
	s_setprio 0
	s_add_i32 s67, s67, s18
	s_add_i32 s68, s67, 0x2000
	s_mov_b32 m0, s67
	s_add_u32 s72, s34, 0x4000
	ds_read_b128 v[62:65], v237 offset:16384
	ds_read_b128 v[90:93], v237 offset:17408
	ds_read_b128 v[94:97], v237 offset:18432
	ds_read_b128 v[106:109], v237 offset:19456
	ds_read_b128 v[110:113], v237 offset:20480
	ds_read_b128 v[122:125], v237 offset:21504
	ds_read_b128 v[126:129], v237 offset:22528
	ds_read_b128 v[130:133], v237 offset:23552
	s_addc_u32 s73, s35, 0
	global_load_lds_dwordx4 v227, s[34:35]
	s_mov_b32 m0, s68
	s_add_i32 s69, s70, s18
	s_add_i32 s70, s69, 0x2000
	global_load_lds_dwordx4 v0, s[34:35]
	s_mov_b32 m0, s69
	s_nop 0
	global_load_lds_dwordx4 v227, s[72:73]
	s_mov_b32 m0, s70
	s_nop 0
	global_load_lds_dwordx4 v0, s[72:73]
	s_mov_b32 m0, s20
	s_nop 0
	global_load_lds_dwordx4 v235, s[46:47]
	s_mov_b32 m0, s25
	s_nop 0
	global_load_lds_dwordx4 v226, s[46:47]
	s_waitcnt vmcnt(8)
	s_waitcnt lgkmcnt(0)
	s_setprio 1
	s_barrier
	v_mfma_f32_16x16x32_bf16 v[134:137], v[2:5], v[62:65], 0
	v_mfma_f32_16x16x32_bf16 v[142:145], v[2:5], v[94:97], 0
	v_mfma_f32_16x16x32_bf16 v[150:153], v[2:5], v[110:113], 0
	v_mfma_f32_16x16x32_bf16 v[2:5], v[2:5], v[126:129], 0
	v_mfma_f32_16x16x32_bf16 v[134:137], v[6:9], v[90:93], v[134:137]
	v_mfma_f32_16x16x32_bf16 v[142:145], v[6:9], v[106:109], v[142:145]
	v_mfma_f32_16x16x32_bf16 v[150:153], v[6:9], v[122:125], v[150:153]
	v_mfma_f32_16x16x32_bf16 v[2:5], v[6:9], v[130:133], v[2:5]
	v_mfma_f32_16x16x32_bf16 v[6:9], v[10:13], v[126:129], 0
	v_mfma_f32_16x16x32_bf16 v[138:141], v[10:13], v[62:65], 0
	v_mfma_f32_16x16x32_bf16 v[146:149], v[10:13], v[94:97], 0
	v_mfma_f32_16x16x32_bf16 v[154:157], v[10:13], v[110:113], 0
	v_mfma_f32_16x16x32_bf16 v[6:9], v[14:17], v[130:133], v[6:9]
	v_mfma_f32_16x16x32_bf16 v[138:141], v[14:17], v[90:93], v[138:141]
	v_mfma_f32_16x16x32_bf16 v[146:149], v[14:17], v[106:109], v[146:149]
	v_mfma_f32_16x16x32_bf16 v[154:157], v[14:17], v[122:125], v[154:157]
	s_setprio 0
	s_setprio 1
	v_mfma_f32_16x16x32_bf16 v[10:13], v[18:21], v[62:65], 0
	v_mfma_f32_16x16x32_bf16 v[158:161], v[22:25], v[90:93], v[10:13]
	v_mfma_f32_16x16x32_bf16 v[10:13], v[26:29], v[62:65], 0
	v_mfma_f32_16x16x32_bf16 v[162:165], v[30:33], v[90:93], v[10:13]
	v_mfma_f32_16x16x32_bf16 v[10:13], v[18:21], v[94:97], 0
	v_mfma_f32_16x16x32_bf16 v[174:177], v[22:25], v[106:109], v[10:13]
	v_mfma_f32_16x16x32_bf16 v[10:13], v[26:29], v[94:97], 0
	v_mfma_f32_16x16x32_bf16 v[178:181], v[30:33], v[106:109], v[10:13]
	v_mfma_f32_16x16x32_bf16 v[10:13], v[18:21], v[110:113], 0
	v_mfma_f32_16x16x32_bf16 v[182:185], v[22:25], v[122:125], v[10:13]
	v_mfma_f32_16x16x32_bf16 v[10:13], v[26:29], v[110:113], 0
	v_mfma_f32_16x16x32_bf16 v[122:125], v[30:33], v[122:125], v[10:13]
	v_mfma_f32_16x16x32_bf16 v[10:13], v[18:21], v[126:129], 0
	v_mfma_f32_16x16x32_bf16 v[186:189], v[22:25], v[130:133], v[10:13]
	v_mfma_f32_16x16x32_bf16 v[10:13], v[26:29], v[126:129], 0
	v_mfma_f32_16x16x32_bf16 v[130:133], v[30:33], v[130:133], v[10:13]
	s_barrier
	s_setprio 0
	s_add_i32 s71, 0, 0x18000
	s_add_i32 s74, 0, 0x1c000
	v_add_u32_e32 v116, s71, v236
	v_add_u32_e32 v117, s74, v236
	s_nop 0
	ds_read_b128 v[10:13], v116
	ds_read_b128 v[14:17], v116 offset:1024
	ds_read_b128 v[18:21], v116 offset:2048
	ds_read_b128 v[22:25], v116 offset:3072
	ds_read_b128 v[194:197], v117
	ds_read_b128 v[198:201], v117 offset:1024
	ds_read_b128 v[202:205], v117 offset:2048
	ds_read_b128 v[206:209], v117 offset:3072
	s_add_u32 s46, s46, 0x4000
	s_addc_u32 s47, s47, 0
	s_mov_b32 m0, s54
	ds_read_b128 v[26:29], v237 offset:32768
	ds_read_b128 v[30:33], v237 offset:33792
	ds_read_b128 v[62:65], v237 offset:34816
	ds_read_b128 v[210:213], v237 offset:35840
	ds_read_b128 v[214:217], v237 offset:36864
	ds_read_b128 v[218:221], v237 offset:37888
	ds_read_b128 v[222:225], v237 offset:38912
	ds_read_b128 v[238:241], v237 offset:39936
	s_nop 0
	global_load_lds_dwordx4 v235, s[46:47]
	s_mov_b32 m0, s55
	s_nop 0
	global_load_lds_dwordx4 v226, s[46:47]
	s_waitcnt vmcnt(8)
	s_waitcnt lgkmcnt(0)
	s_setprio 1
	s_barrier
	v_mfma_f32_16x16x32_bf16 v[66:69], v[10:13], v[26:29], v[66:69]
	v_mfma_f32_16x16x32_bf16 v[166:169], v[14:17], v[30:33], v[66:69]
	v_mfma_f32_16x16x32_bf16 v[66:69], v[18:21], v[26:29], v[70:73]
	v_mfma_f32_16x16x32_bf16 v[170:173], v[22:25], v[30:33], v[66:69]
	v_mfma_f32_16x16x32_bf16 v[66:69], v[10:13], v[62:65], v[74:77]
	v_mfma_f32_16x16x32_bf16 v[110:113], v[14:17], v[210:213], v[66:69]
	v_mfma_f32_16x16x32_bf16 v[66:69], v[18:21], v[62:65], v[78:81]
	v_mfma_f32_16x16x32_bf16 v[106:109], v[22:25], v[210:213], v[66:69]
	v_mfma_f32_16x16x32_bf16 v[66:69], v[10:13], v[214:217], v[82:85]
	v_mfma_f32_16x16x32_bf16 v[94:97], v[14:17], v[218:221], v[66:69]
	v_mfma_f32_16x16x32_bf16 v[66:69], v[18:21], v[214:217], v[86:89]
	v_mfma_f32_16x16x32_bf16 v[90:93], v[22:25], v[218:221], v[66:69]
	v_mfma_f32_16x16x32_bf16 v[66:69], v[10:13], v[222:225], v[98:101]
	v_mfma_f32_16x16x32_bf16 v[78:81], v[14:17], v[238:241], v[66:69]
	v_mfma_f32_16x16x32_bf16 v[66:69], v[18:21], v[222:225], v[102:105]
	v_mfma_f32_16x16x32_bf16 v[70:73], v[22:25], v[238:241], v[66:69]
	s_setprio 0
	s_setprio 1
	v_mfma_f32_16x16x32_bf16 v[66:69], v[194:197], v[26:29], v[118:121]
	v_mfma_f32_16x16x32_bf16 v[26:29], v[202:205], v[26:29], v[34:37]
	v_mfma_f32_16x16x32_bf16 v[118:121], v[206:209], v[30:33], v[26:29]
	v_mfma_f32_16x16x32_bf16 v[26:29], v[194:197], v[62:65], v[38:41]
	v_mfma_f32_16x16x32_bf16 v[102:105], v[198:201], v[210:213], v[26:29]
	v_mfma_f32_16x16x32_bf16 v[26:29], v[202:205], v[62:65], v[42:45]
	v_mfma_f32_16x16x32_bf16 v[98:101], v[206:209], v[210:213], v[26:29]
	v_mfma_f32_16x16x32_bf16 v[26:29], v[194:197], v[214:217], v[46:49]
	v_mfma_f32_16x16x32_bf16 v[86:89], v[198:201], v[218:221], v[26:29]
	v_mfma_f32_16x16x32_bf16 v[26:29], v[202:205], v[214:217], v[50:53]
	v_mfma_f32_16x16x32_bf16 v[82:85], v[206:209], v[218:221], v[26:29]
	v_mfma_f32_16x16x32_bf16 v[26:29], v[194:197], v[222:225], v[54:57]
	v_mfma_f32_16x16x32_bf16 v[62:65], v[198:201], v[238:241], v[26:29]
	v_mfma_f32_16x16x32_bf16 v[26:29], v[202:205], v[222:225], v[58:61]
	v_mfma_f32_16x16x32_bf16 v[126:129], v[198:201], v[30:33], v[66:69]
	v_mfma_f32_16x16x32_bf16 v[54:57], v[206:209], v[238:241], v[26:29]
	s_barrier
	s_setprio 0
	s_add_u32 s72, s34, 0x8000
	s_addc_u32 s73, s35, 0
	s_add_i32 s46, s71, s18
	s_add_i32 s47, s46, 0x2000
	s_mov_b32 m0, s46
	s_add_u32 s34, s34, 0xc000
	ds_read_b128 v[34:37], v237 offset:49152
	ds_read_b128 v[38:41], v237 offset:50176
	ds_read_b128 v[210:213], v237 offset:51200
	ds_read_b128 v[214:217], v237 offset:52224
	ds_read_b128 v[218:221], v237 offset:53248
	ds_read_b128 v[222:225], v237 offset:54272
	ds_read_b128 v[238:241], v237 offset:55296
	ds_read_b128 v[242:245], v237 offset:56320
	s_addc_u32 s35, s35, 0
	global_load_lds_dwordx4 v227, s[72:73]
	s_mov_b32 m0, s47
	s_add_i32 s71, s74, s18
	s_nop 0
	global_load_lds_dwordx4 v0, s[72:73]
	s_mov_b32 m0, s71
	s_add_i32 s72, s71, 0x2000
	s_nop 0
	global_load_lds_dwordx4 v227, s[34:35]
	s_mov_b32 m0, s72
	s_nop 0
	global_load_lds_dwordx4 v0, s[34:35]
	s_mov_b32 m0, s58
	s_nop 0
	global_load_lds_dwordx4 v235, s[30:31]
	s_mov_b32 m0, s59
	s_nop 0
	global_load_lds_dwordx4 v226, s[30:31]
	s_waitcnt vmcnt(8)
	s_waitcnt lgkmcnt(0)
	s_setprio 1
	s_barrier
	v_mfma_f32_16x16x32_bf16 v[26:29], v[10:13], v[34:37], v[134:137]
	v_mfma_f32_16x16x32_bf16 v[74:77], v[14:17], v[38:41], v[26:29]
	v_mfma_f32_16x16x32_bf16 v[26:29], v[18:21], v[34:37], v[138:141]
	v_mfma_f32_16x16x32_bf16 v[66:69], v[22:25], v[38:41], v[26:29]
	v_mfma_f32_16x16x32_bf16 v[26:29], v[10:13], v[210:213], v[142:145]
	v_mfma_f32_16x16x32_bf16 v[46:49], v[14:17], v[214:217], v[26:29]
	v_mfma_f32_16x16x32_bf16 v[26:29], v[18:21], v[210:213], v[146:149]
	v_mfma_f32_16x16x32_bf16 v[42:45], v[22:25], v[214:217], v[26:29]
	v_mfma_f32_16x16x32_bf16 v[26:29], v[10:13], v[218:221], v[150:153]
	v_mfma_f32_16x16x32_bf16 v[2:5], v[10:13], v[238:241], v[2:5]
	v_mfma_f32_16x16x32_bf16 v[30:33], v[14:17], v[222:225], v[26:29]
	v_mfma_f32_16x16x32_bf16 v[26:29], v[18:21], v[218:221], v[154:157]
	v_mfma_f32_16x16x32_bf16 v[14:17], v[14:17], v[242:245], v[2:5]
	v_mfma_f32_16x16x32_bf16 v[2:5], v[18:21], v[238:241], v[6:9]
	v_mfma_f32_16x16x32_bf16 v[26:29], v[22:25], v[222:225], v[26:29]
	v_mfma_f32_16x16x32_bf16 v[10:13], v[22:25], v[242:245], v[2:5]
	s_setprio 0
	s_setprio 1
	v_mfma_f32_16x16x32_bf16 v[2:5], v[194:197], v[34:37], v[158:161]
	v_mfma_f32_16x16x32_bf16 v[58:61], v[198:201], v[38:41], v[2:5]
	v_mfma_f32_16x16x32_bf16 v[2:5], v[202:205], v[34:37], v[162:165]
	v_mfma_f32_16x16x32_bf16 v[50:53], v[206:209], v[38:41], v[2:5]
	v_mfma_f32_16x16x32_bf16 v[2:5], v[194:197], v[210:213], v[174:177]
	v_mfma_f32_16x16x32_bf16 v[38:41], v[198:201], v[214:217], v[2:5]
	v_mfma_f32_16x16x32_bf16 v[2:5], v[202:205], v[210:213], v[178:181]
	v_mfma_f32_16x16x32_bf16 v[34:37], v[206:209], v[214:217], v[2:5]
	v_mfma_f32_16x16x32_bf16 v[2:5], v[194:197], v[218:221], v[182:185]
	v_mfma_f32_16x16x32_bf16 v[22:25], v[198:201], v[222:225], v[2:5]
	v_mfma_f32_16x16x32_bf16 v[2:5], v[202:205], v[218:221], v[122:125]
	v_mfma_f32_16x16x32_bf16 v[18:21], v[206:209], v[222:225], v[2:5]
	v_mfma_f32_16x16x32_bf16 v[2:5], v[194:197], v[238:241], v[186:189]
	v_mfma_f32_16x16x32_bf16 v[6:9], v[198:201], v[242:245], v[2:5]
	v_mfma_f32_16x16x32_bf16 v[2:5], v[202:205], v[238:241], v[130:133]
	v_mfma_f32_16x16x32_bf16 v[2:5], v[206:209], v[242:245], v[2:5]
	s_barrier
	s_setprio 0
	s_andn2_b64 vcc, exec, s[50:51]
	s_cbranch_vccnz .LBB0_893
	s_add_u32 s73, s28, 0x20000
	s_addc_u32 s74, s29, 0
	s_add_u32 s26, s26, 0x1c000
	s_addc_u32 s27, s27, 0
	s_mov_b32 s75, 4
.LBB0_892:
	ds_read_b128 v[122:125], v114
	ds_read_b128 v[130:133], v114 offset:1024
	ds_read_b128 v[134:137], v114 offset:2048
	ds_read_b128 v[138:141], v114 offset:3072
	ds_read_b128 v[142:145], v115
	ds_read_b128 v[146:149], v115 offset:1024
	ds_read_b128 v[150:153], v115 offset:2048
	ds_read_b128 v[154:157], v115 offset:3072
	s_add_u32 s28, s26, 0x4000
	s_addc_u32 s29, s27, 0
	s_cmp_eq_u32 s56, s75
	s_cselect_b32 s34, s40, s28
	s_cselect_b32 s35, s41, s29
	s_cselect_b32 s30, s44, s73
	s_cselect_b32 s31, s45, s74
	s_add_u32 s28, s34, 0x8000
	s_addc_u32 s29, s35, 0
	s_mov_b32 m0, s65
	ds_read_b128 v[158:161], v237
	ds_read_b128 v[162:165], v237 offset:1024
	ds_read_b128 v[174:177], v237 offset:2048
	ds_read_b128 v[178:181], v237 offset:3072
	ds_read_b128 v[182:185], v237 offset:4096
	ds_read_b128 v[186:189], v237 offset:5120
	ds_read_b128 v[194:197], v237 offset:6144
	ds_read_b128 v[198:201], v237 offset:7168
	s_nop 0
	global_load_lds_dwordx4 v235, s[26:27]
	s_mov_b32 m0, s66
	s_nop 0
	global_load_lds_dwordx4 v226, s[26:27]
	s_waitcnt vmcnt(8)
	s_waitcnt lgkmcnt(0)
	s_setprio 1
	s_barrier
	v_mfma_f32_16x16x32_bf16 v[166:169], v[122:125], v[158:161], v[166:169]
	v_mfma_f32_16x16x32_bf16 v[170:173], v[134:137], v[158:161], v[170:173]
	v_mfma_f32_16x16x32_bf16 v[110:113], v[122:125], v[174:177], v[110:113]
	v_mfma_f32_16x16x32_bf16 v[106:109], v[134:137], v[174:177], v[106:109]
	v_mfma_f32_16x16x32_bf16 v[94:97], v[122:125], v[182:185], v[94:97]
	v_mfma_f32_16x16x32_bf16 v[90:93], v[134:137], v[182:185], v[90:93]
	v_mfma_f32_16x16x32_bf16 v[78:81], v[122:125], v[194:197], v[78:81]
	v_mfma_f32_16x16x32_bf16 v[70:73], v[134:137], v[194:197], v[70:73]
	v_mfma_f32_16x16x32_bf16 v[166:169], v[130:133], v[162:165], v[166:169]
	v_mfma_f32_16x16x32_bf16 v[170:173], v[138:141], v[162:165], v[170:173]
	v_mfma_f32_16x16x32_bf16 v[110:113], v[130:133], v[178:181], v[110:113]
	v_mfma_f32_16x16x32_bf16 v[106:109], v[138:141], v[178:181], v[106:109]
	v_mfma_f32_16x16x32_bf16 v[94:97], v[130:133], v[186:189], v[94:97]
	v_mfma_f32_16x16x32_bf16 v[90:93], v[138:141], v[186:189], v[90:93]
	v_mfma_f32_16x16x32_bf16 v[78:81], v[130:133], v[198:201], v[78:81]
	v_mfma_f32_16x16x32_bf16 v[70:73], v[138:141], v[198:201], v[70:73]
	s_setprio 0
	s_setprio 1
	v_mfma_f32_16x16x32_bf16 v[126:129], v[142:145], v[158:161], v[126:129]
	v_mfma_f32_16x16x32_bf16 v[118:121], v[150:153], v[158:161], v[118:121]
	v_mfma_f32_16x16x32_bf16 v[102:105], v[142:145], v[174:177], v[102:105]
	v_mfma_f32_16x16x32_bf16 v[98:101], v[150:153], v[174:177], v[98:101]
	v_mfma_f32_16x16x32_bf16 v[86:89], v[142:145], v[182:185], v[86:89]
	v_mfma_f32_16x16x32_bf16 v[82:85], v[150:153], v[182:185], v[82:85]
	v_mfma_f32_16x16x32_bf16 v[62:65], v[142:145], v[194:197], v[62:65]
	v_mfma_f32_16x16x32_bf16 v[54:57], v[150:153], v[194:197], v[54:57]
	v_mfma_f32_16x16x32_bf16 v[126:129], v[146:149], v[162:165], v[126:129]
	v_mfma_f32_16x16x32_bf16 v[118:121], v[154:157], v[162:165], v[118:121]
	v_mfma_f32_16x16x32_bf16 v[102:105], v[146:149], v[178:181], v[102:105]
	v_mfma_f32_16x16x32_bf16 v[98:101], v[154:157], v[178:181], v[98:101]
	v_mfma_f32_16x16x32_bf16 v[86:89], v[146:149], v[186:189], v[86:89]
	v_mfma_f32_16x16x32_bf16 v[82:85], v[154:157], v[186:189], v[82:85]
	v_mfma_f32_16x16x32_bf16 v[62:65], v[146:149], v[198:201], v[62:65]
	v_mfma_f32_16x16x32_bf16 v[54:57], v[154:157], v[198:201], v[54:57]
	s_barrier
	s_setprio 0
	s_mov_b32 m0, s67
	ds_read_b128 v[158:161], v237 offset:16384
	ds_read_b128 v[162:165], v237 offset:17408
	ds_read_b128 v[174:177], v237 offset:18432
	ds_read_b128 v[178:181], v237 offset:19456
	ds_read_b128 v[182:185], v237 offset:20480
	ds_read_b128 v[186:189], v237 offset:21504
	ds_read_b128 v[194:197], v237 offset:22528
	ds_read_b128 v[198:201], v237 offset:23552
	s_add_u32 s76, s30, 0x4000
	global_load_lds_dwordx4 v227, s[30:31]
	s_mov_b32 m0, s68
	s_addc_u32 s77, s31, 0
	global_load_lds_dwordx4 v0, s[30:31]
	s_mov_b32 m0, s69
	s_nop 0
	global_load_lds_dwordx4 v227, s[76:77]
	s_mov_b32 m0, s70
	s_nop 0
	global_load_lds_dwordx4 v0, s[76:77]
	s_mov_b32 m0, s20
	s_nop 0
	global_load_lds_dwordx4 v235, s[34:35]
	s_mov_b32 m0, s25
	s_nop 0
	global_load_lds_dwordx4 v226, s[34:35]
	s_waitcnt vmcnt(8)
	s_waitcnt lgkmcnt(0)
	s_setprio 1
	s_barrier
	v_mfma_f32_16x16x32_bf16 v[74:77], v[122:125], v[158:161], v[74:77]
	v_mfma_f32_16x16x32_bf16 v[66:69], v[134:137], v[158:161], v[66:69]
	v_mfma_f32_16x16x32_bf16 v[46:49], v[122:125], v[174:177], v[46:49]
	v_mfma_f32_16x16x32_bf16 v[42:45], v[134:137], v[174:177], v[42:45]
	v_mfma_f32_16x16x32_bf16 v[30:33], v[122:125], v[182:185], v[30:33]
	v_mfma_f32_16x16x32_bf16 v[26:29], v[134:137], v[182:185], v[26:29]
	v_mfma_f32_16x16x32_bf16 v[14:17], v[122:125], v[194:197], v[14:17]
	v_mfma_f32_16x16x32_bf16 v[10:13], v[134:137], v[194:197], v[10:13]
	v_mfma_f32_16x16x32_bf16 v[74:77], v[130:133], v[162:165], v[74:77]
	v_mfma_f32_16x16x32_bf16 v[66:69], v[138:141], v[162:165], v[66:69]
	v_mfma_f32_16x16x32_bf16 v[46:49], v[130:133], v[178:181], v[46:49]
	v_mfma_f32_16x16x32_bf16 v[42:45], v[138:141], v[178:181], v[42:45]
	v_mfma_f32_16x16x32_bf16 v[30:33], v[130:133], v[186:189], v[30:33]
	v_mfma_f32_16x16x32_bf16 v[26:29], v[138:141], v[186:189], v[26:29]
	v_mfma_f32_16x16x32_bf16 v[14:17], v[130:133], v[198:201], v[14:17]
	v_mfma_f32_16x16x32_bf16 v[10:13], v[138:141], v[198:201], v[10:13]
	s_setprio 0
	s_setprio 1
	v_mfma_f32_16x16x32_bf16 v[58:61], v[142:145], v[158:161], v[58:61]
	v_mfma_f32_16x16x32_bf16 v[50:53], v[150:153], v[158:161], v[50:53]
	v_mfma_f32_16x16x32_bf16 v[38:41], v[142:145], v[174:177], v[38:41]
	v_mfma_f32_16x16x32_bf16 v[34:37], v[150:153], v[174:177], v[34:37]
	v_mfma_f32_16x16x32_bf16 v[22:25], v[142:145], v[182:185], v[22:25]
	v_mfma_f32_16x16x32_bf16 v[18:21], v[150:153], v[182:185], v[18:21]
	v_mfma_f32_16x16x32_bf16 v[6:9], v[142:145], v[194:197], v[6:9]
	v_mfma_f32_16x16x32_bf16 v[2:5], v[150:153], v[194:197], v[2:5]
	v_mfma_f32_16x16x32_bf16 v[58:61], v[146:149], v[162:165], v[58:61]
	v_mfma_f32_16x16x32_bf16 v[50:53], v[154:157], v[162:165], v[50:53]
	v_mfma_f32_16x16x32_bf16 v[38:41], v[146:149], v[178:181], v[38:41]
	v_mfma_f32_16x16x32_bf16 v[34:37], v[154:157], v[178:181], v[34:37]
	v_mfma_f32_16x16x32_bf16 v[22:25], v[146:149], v[186:189], v[22:25]
	v_mfma_f32_16x16x32_bf16 v[18:21], v[154:157], v[186:189], v[18:21]
	v_mfma_f32_16x16x32_bf16 v[6:9], v[146:149], v[198:201], v[6:9]
	v_mfma_f32_16x16x32_bf16 v[2:5], v[154:157], v[198:201], v[2:5]
	s_barrier
	s_setprio 0
	ds_read_b128 v[122:125], v116
	ds_read_b128 v[130:133], v116 offset:1024
	ds_read_b128 v[134:137], v116 offset:2048
	ds_read_b128 v[138:141], v116 offset:3072
	ds_read_b128 v[142:145], v117
	ds_read_b128 v[146:149], v117 offset:1024
	ds_read_b128 v[150:153], v117 offset:2048
	ds_read_b128 v[154:157], v117 offset:3072
	s_add_u32 s34, s34, 0x4000
	s_addc_u32 s35, s35, 0
	s_mov_b32 m0, s54
	ds_read_b128 v[158:161], v237 offset:32768
	ds_read_b128 v[162:165], v237 offset:33792
	ds_read_b128 v[174:177], v237 offset:34816
	ds_read_b128 v[178:181], v237 offset:35840
	ds_read_b128 v[182:185], v237 offset:36864
	ds_read_b128 v[186:189], v237 offset:37888
	ds_read_b128 v[194:197], v237 offset:38912
	ds_read_b128 v[198:201], v237 offset:39936
	s_nop 0
	global_load_lds_dwordx4 v235, s[34:35]
	s_mov_b32 m0, s55
	s_nop 0
	global_load_lds_dwordx4 v226, s[34:35]
	s_waitcnt vmcnt(8)
	s_waitcnt lgkmcnt(0)
	s_setprio 1
	s_barrier
	v_mfma_f32_16x16x32_bf16 v[166:169], v[122:125], v[158:161], v[166:169]
	v_mfma_f32_16x16x32_bf16 v[170:173], v[134:137], v[158:161], v[170:173]
	v_mfma_f32_16x16x32_bf16 v[110:113], v[122:125], v[174:177], v[110:113]
	v_mfma_f32_16x16x32_bf16 v[106:109], v[134:137], v[174:177], v[106:109]
	v_mfma_f32_16x16x32_bf16 v[94:97], v[122:125], v[182:185], v[94:97]
	v_mfma_f32_16x16x32_bf16 v[90:93], v[134:137], v[182:185], v[90:93]
	v_mfma_f32_16x16x32_bf16 v[78:81], v[122:125], v[194:197], v[78:81]
	v_mfma_f32_16x16x32_bf16 v[70:73], v[134:137], v[194:197], v[70:73]
	v_mfma_f32_16x16x32_bf16 v[166:169], v[130:133], v[162:165], v[166:169]
	v_mfma_f32_16x16x32_bf16 v[170:173], v[138:141], v[162:165], v[170:173]
	v_mfma_f32_16x16x32_bf16 v[110:113], v[130:133], v[178:181], v[110:113]
	v_mfma_f32_16x16x32_bf16 v[106:109], v[138:141], v[178:181], v[106:109]
	v_mfma_f32_16x16x32_bf16 v[94:97], v[130:133], v[186:189], v[94:97]
	v_mfma_f32_16x16x32_bf16 v[90:93], v[138:141], v[186:189], v[90:93]
	v_mfma_f32_16x16x32_bf16 v[78:81], v[130:133], v[198:201], v[78:81]
	v_mfma_f32_16x16x32_bf16 v[70:73], v[138:141], v[198:201], v[70:73]
	s_setprio 0
	s_setprio 1
	v_mfma_f32_16x16x32_bf16 v[126:129], v[142:145], v[158:161], v[126:129]
	v_mfma_f32_16x16x32_bf16 v[118:121], v[150:153], v[158:161], v[118:121]
	v_mfma_f32_16x16x32_bf16 v[102:105], v[142:145], v[174:177], v[102:105]
	v_mfma_f32_16x16x32_bf16 v[98:101], v[150:153], v[174:177], v[98:101]
	v_mfma_f32_16x16x32_bf16 v[86:89], v[142:145], v[182:185], v[86:89]
	v_mfma_f32_16x16x32_bf16 v[82:85], v[150:153], v[182:185], v[82:85]
	v_mfma_f32_16x16x32_bf16 v[62:65], v[142:145], v[194:197], v[62:65]
	v_mfma_f32_16x16x32_bf16 v[54:57], v[150:153], v[194:197], v[54:57]
	v_mfma_f32_16x16x32_bf16 v[126:129], v[146:149], v[162:165], v[126:129]
	v_mfma_f32_16x16x32_bf16 v[118:121], v[154:157], v[162:165], v[118:121]
	v_mfma_f32_16x16x32_bf16 v[102:105], v[146:149], v[178:181], v[102:105]
	v_mfma_f32_16x16x32_bf16 v[98:101], v[154:157], v[178:181], v[98:101]
	v_mfma_f32_16x16x32_bf16 v[86:89], v[146:149], v[186:189], v[86:89]
	v_mfma_f32_16x16x32_bf16 v[82:85], v[154:157], v[186:189], v[82:85]
	v_mfma_f32_16x16x32_bf16 v[62:65], v[146:149], v[198:201], v[62:65]
	v_mfma_f32_16x16x32_bf16 v[54:57], v[154:157], v[198:201], v[54:57]
	s_barrier
	s_setprio 0
	s_add_u32 s34, s30, 0x8000
	s_mov_b32 m0, s46
	s_addc_u32 s35, s31, 0
	ds_read_b128 v[158:161], v237 offset:49152
	ds_read_b128 v[162:165], v237 offset:50176
	ds_read_b128 v[174:177], v237 offset:51200
	ds_read_b128 v[178:181], v237 offset:52224
	ds_read_b128 v[182:185], v237 offset:53248
	ds_read_b128 v[186:189], v237 offset:54272
	ds_read_b128 v[194:197], v237 offset:55296
	ds_read_b128 v[198:201], v237 offset:56320
	s_add_u32 s30, s30, 0xc000
	global_load_lds_dwordx4 v227, s[34:35]
	s_mov_b32 m0, s47
	s_addc_u32 s31, s31, 0
	global_load_lds_dwordx4 v0, s[34:35]
	s_mov_b32 m0, s71
	s_nop 0
	global_load_lds_dwordx4 v227, s[30:31]
	s_mov_b32 m0, s72
	s_nop 0
	global_load_lds_dwordx4 v0, s[30:31]
	s_mov_b32 m0, s58
	s_nop 0
	global_load_lds_dwordx4 v235, s[28:29]
	s_mov_b32 m0, s59
	s_nop 0
	global_load_lds_dwordx4 v226, s[28:29]
	s_waitcnt vmcnt(8)
	s_waitcnt lgkmcnt(0)
	s_setprio 1
	s_barrier
	v_mfma_f32_16x16x32_bf16 v[74:77], v[122:125], v[158:161], v[74:77]
	v_mfma_f32_16x16x32_bf16 v[66:69], v[134:137], v[158:161], v[66:69]
	v_mfma_f32_16x16x32_bf16 v[46:49], v[122:125], v[174:177], v[46:49]
	v_mfma_f32_16x16x32_bf16 v[42:45], v[134:137], v[174:177], v[42:45]
	v_mfma_f32_16x16x32_bf16 v[30:33], v[122:125], v[182:185], v[30:33]
	v_mfma_f32_16x16x32_bf16 v[26:29], v[134:137], v[182:185], v[26:29]
	v_mfma_f32_16x16x32_bf16 v[14:17], v[122:125], v[194:197], v[14:17]
	v_mfma_f32_16x16x32_bf16 v[10:13], v[134:137], v[194:197], v[10:13]
	v_mfma_f32_16x16x32_bf16 v[74:77], v[130:133], v[162:165], v[74:77]
	v_mfma_f32_16x16x32_bf16 v[66:69], v[138:141], v[162:165], v[66:69]
	v_mfma_f32_16x16x32_bf16 v[46:49], v[130:133], v[178:181], v[46:49]
	v_mfma_f32_16x16x32_bf16 v[42:45], v[138:141], v[178:181], v[42:45]
	v_mfma_f32_16x16x32_bf16 v[30:33], v[130:133], v[186:189], v[30:33]
	v_mfma_f32_16x16x32_bf16 v[26:29], v[138:141], v[186:189], v[26:29]
	v_mfma_f32_16x16x32_bf16 v[14:17], v[130:133], v[198:201], v[14:17]
	v_mfma_f32_16x16x32_bf16 v[10:13], v[138:141], v[198:201], v[10:13]
	s_setprio 0
	s_setprio 1
	v_mfma_f32_16x16x32_bf16 v[58:61], v[142:145], v[158:161], v[58:61]
	v_mfma_f32_16x16x32_bf16 v[50:53], v[150:153], v[158:161], v[50:53]
	v_mfma_f32_16x16x32_bf16 v[38:41], v[142:145], v[174:177], v[38:41]
	v_mfma_f32_16x16x32_bf16 v[34:37], v[150:153], v[174:177], v[34:37]
	v_mfma_f32_16x16x32_bf16 v[22:25], v[142:145], v[182:185], v[22:25]
	v_mfma_f32_16x16x32_bf16 v[18:21], v[150:153], v[182:185], v[18:21]
	v_mfma_f32_16x16x32_bf16 v[6:9], v[142:145], v[194:197], v[6:9]
	v_mfma_f32_16x16x32_bf16 v[2:5], v[150:153], v[194:197], v[2:5]
	v_mfma_f32_16x16x32_bf16 v[58:61], v[146:149], v[162:165], v[58:61]
	v_mfma_f32_16x16x32_bf16 v[50:53], v[154:157], v[162:165], v[50:53]
	v_mfma_f32_16x16x32_bf16 v[38:41], v[146:149], v[178:181], v[38:41]
	v_mfma_f32_16x16x32_bf16 v[34:37], v[154:157], v[178:181], v[34:37]
	v_mfma_f32_16x16x32_bf16 v[22:25], v[146:149], v[186:189], v[22:25]
	v_mfma_f32_16x16x32_bf16 v[18:21], v[154:157], v[186:189], v[18:21]
	v_mfma_f32_16x16x32_bf16 v[6:9], v[146:149], v[198:201], v[6:9]
	v_mfma_f32_16x16x32_bf16 v[2:5], v[154:157], v[198:201], v[2:5]
	s_barrier
	s_setprio 0
	s_add_i32 s28, s75, 2
	s_add_u32 s73, s73, 0x10000
	s_addc_u32 s74, s74, 0
	s_add_u32 s26, s26, 0x10000
	s_addc_u32 s27, s27, 0
	s_cmp_lt_i32 s75, s56
	s_mov_b32 s75, s28
	s_cbranch_scc1 .LBB0_892

.LBB0_965:
	s_add_u32 s34, s28, 0x10000
	s_addc_u32 s35, s29, 0
	s_and_b64 s[30:31], s[48:49], exec
	s_cselect_b32 s57, s43, s35
	s_cselect_b32 s56, s42, s34
	s_add_u32 s58, s26, 0x100
	s_addc_u32 s59, s27, 0
	s_add_u32 s30, s56, 0x8000
	s_addc_u32 s31, s57, 0
	s_add_i32 s74, 0, 0x10000
	s_and_b64 s[34:35], s[48:49], exec
	s_cselect_b32 s35, s55, s59
	s_cselect_b32 s34, s54, s58
	s_add_i32 s76, 0, 0x14000
	v_add_u32_e32 v132, s74, v218
	v_add_u32_e32 v133, s76, v218
	ds_read_b128 v[2:5], v132
	ds_read_b128 v[6:9], v132 offset:1024
	ds_read_b128 v[10:13], v132 offset:2048
	ds_read_b128 v[14:17], v132 offset:3072
	ds_read_b128 v[18:21], v133
	ds_read_b128 v[22:25], v133 offset:1024
	ds_read_b128 v[26:29], v133 offset:2048
	ds_read_b128 v[30:33], v133 offset:3072
	s_add_u32 s58, s28, 0xc000
	s_addc_u32 s59, s29, 0
	s_add_i32 s72, s18, 0xc000
	s_mov_b32 m0, s72
	s_add_i32 s73, s18, 0xe000
	ds_read_b128 v[34:37], v219
	ds_read_b128 v[38:41], v219 offset:1024
	ds_read_b128 v[42:45], v219 offset:2048
	ds_read_b128 v[46:49], v219 offset:3072
	ds_read_b128 v[50:53], v219 offset:4096
	ds_read_b128 v[54:57], v219 offset:5120
	ds_read_b128 v[58:61], v219 offset:6144
	ds_read_b128 v[62:65], v219 offset:7168
	s_nop 0
	global_load_lds_dwordx4 v217, s[58:59]
	s_mov_b32 m0, s73
	s_nop 0
	global_load_lds_dwordx4 v216, s[58:59]
	s_waitcnt vmcnt(8)
	s_waitcnt lgkmcnt(0)
	s_setprio 1
	s_barrier
	v_mfma_f32_16x16x32_bf16 v[86:89], v[10:13], v[50:53], 0
	v_mfma_f32_16x16x32_bf16 v[90:93], v[14:17], v[54:57], v[86:89]
	v_mfma_f32_16x16x32_bf16 v[86:89], v[2:5], v[58:61], 0
	v_mfma_f32_16x16x32_bf16 v[66:69], v[2:5], v[34:37], 0
	v_mfma_f32_16x16x32_bf16 v[70:73], v[10:13], v[34:37], 0
	v_mfma_f32_16x16x32_bf16 v[74:77], v[2:5], v[42:45], 0
	v_mfma_f32_16x16x32_bf16 v[78:81], v[10:13], v[42:45], 0
	v_mfma_f32_16x16x32_bf16 v[82:85], v[2:5], v[50:53], 0
	v_mfma_f32_16x16x32_bf16 v[94:97], v[6:9], v[62:65], v[86:89]
	v_mfma_f32_16x16x32_bf16 v[86:89], v[10:13], v[58:61], 0
	v_mfma_f32_16x16x32_bf16 v[66:69], v[6:9], v[38:41], v[66:69]
	v_mfma_f32_16x16x32_bf16 v[70:73], v[14:17], v[38:41], v[70:73]
	v_mfma_f32_16x16x32_bf16 v[74:77], v[6:9], v[46:49], v[74:77]
	v_mfma_f32_16x16x32_bf16 v[78:81], v[14:17], v[46:49], v[78:81]
	v_mfma_f32_16x16x32_bf16 v[82:85], v[6:9], v[54:57], v[82:85]
	v_mfma_f32_16x16x32_bf16 v[106:109], v[14:17], v[62:65], v[86:89]
	s_setprio 0
	s_setprio 1
	v_mfma_f32_16x16x32_bf16 v[86:89], v[18:21], v[34:37], 0
	v_mfma_f32_16x16x32_bf16 v[34:37], v[26:29], v[34:37], 0
	v_mfma_f32_16x16x32_bf16 v[110:113], v[22:25], v[38:41], v[86:89]
	v_mfma_f32_16x16x32_bf16 v[34:37], v[30:33], v[38:41], v[34:37]
	v_mfma_f32_16x16x32_bf16 v[38:41], v[18:21], v[42:45], 0
	v_mfma_f32_16x16x32_bf16 v[42:45], v[26:29], v[42:45], 0
	v_mfma_f32_16x16x32_bf16 v[38:41], v[22:25], v[46:49], v[38:41]
	v_mfma_f32_16x16x32_bf16 v[42:45], v[30:33], v[46:49], v[42:45]
	v_mfma_f32_16x16x32_bf16 v[46:49], v[18:21], v[50:53], 0
	v_mfma_f32_16x16x32_bf16 v[50:53], v[26:29], v[50:53], 0
	v_mfma_f32_16x16x32_bf16 v[136:139], v[30:33], v[54:57], v[50:53]
	v_mfma_f32_16x16x32_bf16 v[50:53], v[18:21], v[58:61], 0
	v_mfma_f32_16x16x32_bf16 v[140:143], v[22:25], v[62:65], v[50:53]
	v_mfma_f32_16x16x32_bf16 v[50:53], v[26:29], v[58:61], 0
	v_mfma_f32_16x16x32_bf16 v[46:49], v[22:25], v[54:57], v[46:49]
	v_mfma_f32_16x16x32_bf16 v[58:61], v[30:33], v[62:65], v[50:53]
	s_barrier
	s_setprio 0
	s_add_i32 s74, s74, s15
	s_add_i32 s75, s74, 0x2000
	s_mov_b32 m0, s74
	s_add_u32 s58, s34, s36
	ds_read_b128 v[50:53], v219 offset:16384
	ds_read_b128 v[54:57], v219 offset:17408
	ds_read_b128 v[62:65], v219 offset:18432
	ds_read_b128 v[86:89], v219 offset:19456
	ds_read_b128 v[98:101], v219 offset:20480
	ds_read_b128 v[102:105], v219 offset:21504
	ds_read_b128 v[114:117], v219 offset:22528
	ds_read_b128 v[118:121], v219 offset:23552
	s_addc_u32 s59, s35, s37
	global_load_lds_dwordx4 v0, s[34:35]
	s_mov_b32 m0, s75
	s_add_i32 s76, s76, s15
	s_add_i32 s77, s76, 0x2000
	global_load_lds_dwordx4 v130, s[34:35]
	s_mov_b32 m0, s76
	s_nop 0
	global_load_lds_dwordx4 v0, s[58:59]
	s_mov_b32 m0, s77
	s_nop 0
	global_load_lds_dwordx4 v130, s[58:59]
	s_mov_b32 m0, s18
	s_nop 0
	global_load_lds_dwordx4 v217, s[56:57]
	s_mov_b32 m0, s20
	s_nop 0
	global_load_lds_dwordx4 v216, s[56:57]
	s_waitcnt vmcnt(8)
	s_waitcnt lgkmcnt(0)
	s_setprio 1
	s_barrier
	v_mfma_f32_16x16x32_bf16 v[122:125], v[2:5], v[50:53], 0
	v_mfma_f32_16x16x32_bf16 v[144:147], v[6:9], v[54:57], v[122:125]
	v_mfma_f32_16x16x32_bf16 v[122:125], v[10:13], v[50:53], 0
	v_mfma_f32_16x16x32_bf16 v[148:151], v[14:17], v[54:57], v[122:125]
	v_mfma_f32_16x16x32_bf16 v[122:125], v[2:5], v[62:65], 0
	v_mfma_f32_16x16x32_bf16 v[152:155], v[6:9], v[86:89], v[122:125]
	v_mfma_f32_16x16x32_bf16 v[122:125], v[10:13], v[62:65], 0
	v_mfma_f32_16x16x32_bf16 v[156:159], v[14:17], v[86:89], v[122:125]
	v_mfma_f32_16x16x32_bf16 v[122:125], v[2:5], v[98:101], 0
	v_mfma_f32_16x16x32_bf16 v[2:5], v[2:5], v[114:117], 0
	v_mfma_f32_16x16x32_bf16 v[160:163], v[6:9], v[102:105], v[122:125]
	v_mfma_f32_16x16x32_bf16 v[2:5], v[6:9], v[118:121], v[2:5]
	v_mfma_f32_16x16x32_bf16 v[6:9], v[10:13], v[114:117], 0
	v_mfma_f32_16x16x32_bf16 v[122:125], v[10:13], v[98:101], 0
	v_mfma_f32_16x16x32_bf16 v[10:13], v[14:17], v[118:121], v[6:9]
	v_mfma_f32_16x16x32_bf16 v[164:167], v[14:17], v[102:105], v[122:125]
	s_setprio 0
	s_setprio 1
	v_mfma_f32_16x16x32_bf16 v[6:9], v[18:21], v[50:53], 0
	v_mfma_f32_16x16x32_bf16 v[14:17], v[22:25], v[54:57], v[6:9]
	v_mfma_f32_16x16x32_bf16 v[6:9], v[26:29], v[50:53], 0
	v_mfma_f32_16x16x32_bf16 v[168:171], v[30:33], v[54:57], v[6:9]
	v_mfma_f32_16x16x32_bf16 v[6:9], v[18:21], v[62:65], 0
	v_mfma_f32_16x16x32_bf16 v[172:175], v[22:25], v[86:89], v[6:9]
	v_mfma_f32_16x16x32_bf16 v[6:9], v[26:29], v[62:65], 0
	v_mfma_f32_16x16x32_bf16 v[176:179], v[30:33], v[86:89], v[6:9]
	v_mfma_f32_16x16x32_bf16 v[6:9], v[18:21], v[98:101], 0
	v_mfma_f32_16x16x32_bf16 v[180:183], v[22:25], v[102:105], v[6:9]
	v_mfma_f32_16x16x32_bf16 v[6:9], v[26:29], v[98:101], 0
	v_mfma_f32_16x16x32_bf16 v[184:187], v[30:33], v[102:105], v[6:9]
	v_mfma_f32_16x16x32_bf16 v[6:9], v[18:21], v[114:117], 0
	v_mfma_f32_16x16x32_bf16 v[188:191], v[22:25], v[118:121], v[6:9]
	v_mfma_f32_16x16x32_bf16 v[6:9], v[26:29], v[114:117], 0
	v_mfma_f32_16x16x32_bf16 v[194:197], v[30:33], v[118:121], v[6:9]
	s_barrier
	s_setprio 0
	s_add_i32 s78, 0, 0x18000
	s_add_i32 s80, 0, 0x1c000
	v_add_u32_e32 v134, s78, v218
	v_add_u32_e32 v135, s80, v218
	s_nop 0
	ds_read_b128 v[6:9], v134
	ds_read_b128 v[26:29], v134 offset:1024
	ds_read_b128 v[30:33], v134 offset:2048
	ds_read_b128 v[198:201], v134 offset:3072
	ds_read_b128 v[202:205], v135
	ds_read_b128 v[206:209], v135 offset:1024
	ds_read_b128 v[210:213], v135 offset:2048
	ds_read_b128 v[220:223], v135 offset:3072
	s_add_u32 s56, s56, 0x4000
	s_addc_u32 s57, s57, 0
	s_mov_b32 m0, s25
	ds_read_b128 v[18:21], v219 offset:32768
	ds_read_b128 v[22:25], v219 offset:33792
	ds_read_b128 v[62:65], v219 offset:34816
	ds_read_b128 v[224:227], v219 offset:35840
	ds_read_b128 v[232:235], v219 offset:36864
	ds_read_b128 v[236:239], v219 offset:37888
	ds_read_b128 v[240:243], v219 offset:38912
	ds_read_b128 v[244:247], v219 offset:39936
	s_nop 0
	global_load_lds_dwordx4 v217, s[56:57]
	s_mov_b32 m0, s60
	s_nop 0
	global_load_lds_dwordx4 v216, s[56:57]
	s_waitcnt vmcnt(8)
	s_waitcnt lgkmcnt(0)
	s_setprio 1
	s_barrier
	v_mfma_f32_16x16x32_bf16 v[50:53], v[6:9], v[18:21], v[66:69]
	v_mfma_f32_16x16x32_bf16 v[126:129], v[26:29], v[22:25], v[50:53]
	v_mfma_f32_16x16x32_bf16 v[50:53], v[30:33], v[18:21], v[70:73]
	v_mfma_f32_16x16x32_bf16 v[122:125], v[198:201], v[22:25], v[50:53]
	v_mfma_f32_16x16x32_bf16 v[50:53], v[6:9], v[62:65], v[74:77]
	v_mfma_f32_16x16x32_bf16 v[102:105], v[26:29], v[224:227], v[50:53]
	v_mfma_f32_16x16x32_bf16 v[50:53], v[30:33], v[62:65], v[78:81]
	v_mfma_f32_16x16x32_bf16 v[98:101], v[198:201], v[224:227], v[50:53]
	v_mfma_f32_16x16x32_bf16 v[50:53], v[6:9], v[232:235], v[82:85]
	v_mfma_f32_16x16x32_bf16 v[86:89], v[26:29], v[236:239], v[50:53]
	v_mfma_f32_16x16x32_bf16 v[50:53], v[30:33], v[232:235], v[90:93]
	v_mfma_f32_16x16x32_bf16 v[82:85], v[198:201], v[236:239], v[50:53]
	v_mfma_f32_16x16x32_bf16 v[50:53], v[6:9], v[240:243], v[94:97]
	v_mfma_f32_16x16x32_bf16 v[54:57], v[26:29], v[244:247], v[50:53]
	v_mfma_f32_16x16x32_bf16 v[50:53], v[30:33], v[240:243], v[106:109]
	v_mfma_f32_16x16x32_bf16 v[50:53], v[198:201], v[244:247], v[50:53]
	s_setprio 0
	s_setprio 1
	v_mfma_f32_16x16x32_bf16 v[66:69], v[202:205], v[18:21], v[110:113]
	v_mfma_f32_16x16x32_bf16 v[18:21], v[210:213], v[18:21], v[34:37]
	v_mfma_f32_16x16x32_bf16 v[114:117], v[220:223], v[22:25], v[18:21]
	v_mfma_f32_16x16x32_bf16 v[18:21], v[202:205], v[62:65], v[38:41]
	v_mfma_f32_16x16x32_bf16 v[110:113], v[206:209], v[224:227], v[18:21]
	v_mfma_f32_16x16x32_bf16 v[18:21], v[210:213], v[62:65], v[42:45]
	v_mfma_f32_16x16x32_bf16 v[106:109], v[220:223], v[224:227], v[18:21]
	v_mfma_f32_16x16x32_bf16 v[18:21], v[202:205], v[232:235], v[46:49]
	v_mfma_f32_16x16x32_bf16 v[94:97], v[206:209], v[236:239], v[18:21]
	v_mfma_f32_16x16x32_bf16 v[18:21], v[210:213], v[232:235], v[136:139]
	v_mfma_f32_16x16x32_bf16 v[90:93], v[220:223], v[236:239], v[18:21]
	v_mfma_f32_16x16x32_bf16 v[18:21], v[202:205], v[240:243], v[140:143]
	v_mfma_f32_16x16x32_bf16 v[62:65], v[206:209], v[244:247], v[18:21]
	v_mfma_f32_16x16x32_bf16 v[18:21], v[210:213], v[240:243], v[58:61]
	v_mfma_f32_16x16x32_bf16 v[118:121], v[206:209], v[22:25], v[66:69]
	v_mfma_f32_16x16x32_bf16 v[58:61], v[220:223], v[244:247], v[18:21]
	s_barrier
	s_setprio 0
	ds_read_b128 v[42:45], v219 offset:49152
	ds_read_b128 v[46:49], v219 offset:50176
	ds_read_b128 v[136:139], v219 offset:51200
	ds_read_b128 v[140:143], v219 offset:52224
	ds_read_b128 v[224:227], v219 offset:53248
	ds_read_b128 v[232:235], v219 offset:54272
	ds_read_b128 v[236:239], v219 offset:55296
	ds_read_b128 v[240:243], v219 offset:56320
	s_add_i32 s78, s78, s15
	v_lshl_add_u64 v[18:19], s[34:35], 0, v[0:1]
	v_lshl_add_u64 v[18:19], v[18:19], 0, s[16:17]
	s_mov_b32 m0, s78
	v_mov_b32_e32 v131, v1
	global_load_lds_dwordx4 v[18:19], off
	s_add_i32 s79, s78, 0x2000
	v_lshl_add_u64 v[18:19], s[34:35], 0, v[130:131]
	v_lshl_add_u64 v[18:19], v[18:19], 0, s[16:17]
	s_mov_b32 m0, s79
	s_add_i32 s80, s80, s15
	global_load_lds_dwordx4 v[18:19], off
	s_mov_b32 m0, s80
	v_lshl_add_u64 v[18:19], s[58:59], 0, v[0:1]
	v_lshl_add_u64 v[18:19], v[18:19], 0, s[16:17]
	global_load_lds_dwordx4 v[18:19], off
	s_nop 0
	v_lshl_add_u64 v[18:19], s[58:59], 0, v[130:131]
	s_add_i32 s58, s80, 0x2000
	v_lshl_add_u64 v[18:19], v[18:19], 0, s[16:17]
	s_mov_b32 m0, s58
	s_nop 0
	global_load_lds_dwordx4 v[18:19], off
	s_mov_b32 m0, s65
	s_nop 0
	global_load_lds_dwordx4 v217, s[30:31]
	s_mov_b32 m0, s66
	s_nop 0
	global_load_lds_dwordx4 v216, s[30:31]
	s_waitcnt vmcnt(8)
	s_waitcnt lgkmcnt(0)
	s_setprio 1
	s_barrier
	v_mfma_f32_16x16x32_bf16 v[18:21], v[6:9], v[42:45], v[144:147]
	v_mfma_f32_16x16x32_bf16 v[70:73], v[26:29], v[46:49], v[18:21]
	v_mfma_f32_16x16x32_bf16 v[18:21], v[30:33], v[42:45], v[148:151]
	v_mfma_f32_16x16x32_bf16 v[66:69], v[198:201], v[46:49], v[18:21]
	v_mfma_f32_16x16x32_bf16 v[18:21], v[6:9], v[136:139], v[152:155]
	v_mfma_f32_16x16x32_bf16 v[38:41], v[26:29], v[140:143], v[18:21]
	v_mfma_f32_16x16x32_bf16 v[18:21], v[30:33], v[136:139], v[156:159]
	v_mfma_f32_16x16x32_bf16 v[34:37], v[198:201], v[140:143], v[18:21]
	v_mfma_f32_16x16x32_bf16 v[18:21], v[6:9], v[224:227], v[160:163]
	v_mfma_f32_16x16x32_bf16 v[2:5], v[6:9], v[236:239], v[2:5]
	v_mfma_f32_16x16x32_bf16 v[22:25], v[26:29], v[232:235], v[18:21]
	v_mfma_f32_16x16x32_bf16 v[18:21], v[30:33], v[224:227], v[164:167]
	v_mfma_f32_16x16x32_bf16 v[6:9], v[26:29], v[240:243], v[2:5]
	v_mfma_f32_16x16x32_bf16 v[2:5], v[30:33], v[236:239], v[10:13]
	v_mfma_f32_16x16x32_bf16 v[18:21], v[198:201], v[232:235], v[18:21]
	v_mfma_f32_16x16x32_bf16 v[2:5], v[198:201], v[240:243], v[2:5]
	s_setprio 0
	s_setprio 1
	v_mfma_f32_16x16x32_bf16 v[10:13], v[202:205], v[42:45], v[14:17]
	v_mfma_f32_16x16x32_bf16 v[78:81], v[206:209], v[46:49], v[10:13]
	v_mfma_f32_16x16x32_bf16 v[10:13], v[210:213], v[42:45], v[168:171]
	v_mfma_f32_16x16x32_bf16 v[74:77], v[220:223], v[46:49], v[10:13]
	v_mfma_f32_16x16x32_bf16 v[10:13], v[202:205], v[136:139], v[172:175]
	v_mfma_f32_16x16x32_bf16 v[46:49], v[206:209], v[140:143], v[10:13]
	v_mfma_f32_16x16x32_bf16 v[10:13], v[210:213], v[136:139], v[176:179]
	v_mfma_f32_16x16x32_bf16 v[42:45], v[220:223], v[140:143], v[10:13]
	v_mfma_f32_16x16x32_bf16 v[10:13], v[202:205], v[224:227], v[180:183]
	v_mfma_f32_16x16x32_bf16 v[30:33], v[206:209], v[232:235], v[10:13]
	v_mfma_f32_16x16x32_bf16 v[10:13], v[210:213], v[224:227], v[184:187]
	v_mfma_f32_16x16x32_bf16 v[26:29], v[220:223], v[232:235], v[10:13]
	v_mfma_f32_16x16x32_bf16 v[10:13], v[202:205], v[236:239], v[188:191]
	v_mfma_f32_16x16x32_bf16 v[14:17], v[206:209], v[240:243], v[10:13]
	v_mfma_f32_16x16x32_bf16 v[10:13], v[210:213], v[236:239], v[194:197]
	v_mfma_f32_16x16x32_bf16 v[10:13], v[220:223], v[240:243], v[10:13]
	s_barrier
	s_setprio 0
	s_andn2_b64 vcc, exec, s[50:51]
	s_cbranch_vccnz .LBB0_968
	s_add_u32 s59, s26, 0x200
	s_addc_u32 s81, s27, 0
	s_add_u32 s26, s28, 0x1c000
	s_addc_u32 s27, s29, 0
	s_mov_b32 s82, 4
.LBB0_967:
	ds_read_b128 v[136:139], v132
	ds_read_b128 v[140:143], v132 offset:1024
	ds_read_b128 v[144:147], v132 offset:2048
	ds_read_b128 v[148:151], v132 offset:3072
	ds_read_b128 v[152:155], v133
	ds_read_b128 v[156:159], v133 offset:1024
	ds_read_b128 v[160:163], v133 offset:2048
	ds_read_b128 v[164:167], v133 offset:3072
	s_add_u32 s28, s26, 0x4000
	s_addc_u32 s29, s27, 0
	s_cmp_eq_u32 s63, s82
	s_cselect_b32 s34, s42, s28
	s_cselect_b32 s35, s43, s29
	s_cselect_b32 s30, s54, s59
	s_cselect_b32 s31, s55, s81
	s_add_u32 s28, s34, 0x8000
	s_addc_u32 s29, s35, 0
	s_mov_b32 m0, s72
	ds_read_b128 v[168:171], v219
	ds_read_b128 v[172:175], v219 offset:1024
	ds_read_b128 v[176:179], v219 offset:2048
	ds_read_b128 v[180:183], v219 offset:3072
	ds_read_b128 v[184:187], v219 offset:4096
	ds_read_b128 v[188:191], v219 offset:5120
	ds_read_b128 v[194:197], v219 offset:6144
	ds_read_b128 v[198:201], v219 offset:7168
	s_nop 0
	global_load_lds_dwordx4 v217, s[26:27]
	s_mov_b32 m0, s73
	s_nop 0
	global_load_lds_dwordx4 v216, s[26:27]
	s_waitcnt vmcnt(8)
	s_waitcnt lgkmcnt(0)
	s_setprio 1
	s_barrier
	v_mfma_f32_16x16x32_bf16 v[126:129], v[136:139], v[168:171], v[126:129]
	v_mfma_f32_16x16x32_bf16 v[122:125], v[144:147], v[168:171], v[122:125]
	v_mfma_f32_16x16x32_bf16 v[102:105], v[136:139], v[176:179], v[102:105]
	v_mfma_f32_16x16x32_bf16 v[98:101], v[144:147], v[176:179], v[98:101]
	v_mfma_f32_16x16x32_bf16 v[86:89], v[136:139], v[184:187], v[86:89]
	v_mfma_f32_16x16x32_bf16 v[82:85], v[144:147], v[184:187], v[82:85]
	v_mfma_f32_16x16x32_bf16 v[54:57], v[136:139], v[194:197], v[54:57]
	v_mfma_f32_16x16x32_bf16 v[50:53], v[144:147], v[194:197], v[50:53]
	v_mfma_f32_16x16x32_bf16 v[126:129], v[140:143], v[172:175], v[126:129]
	v_mfma_f32_16x16x32_bf16 v[122:125], v[148:151], v[172:175], v[122:125]
	v_mfma_f32_16x16x32_bf16 v[102:105], v[140:143], v[180:183], v[102:105]
	v_mfma_f32_16x16x32_bf16 v[98:101], v[148:151], v[180:183], v[98:101]
	v_mfma_f32_16x16x32_bf16 v[86:89], v[140:143], v[188:191], v[86:89]
	v_mfma_f32_16x16x32_bf16 v[82:85], v[148:151], v[188:191], v[82:85]
	v_mfma_f32_16x16x32_bf16 v[54:57], v[140:143], v[198:201], v[54:57]
	v_mfma_f32_16x16x32_bf16 v[50:53], v[148:151], v[198:201], v[50:53]
	s_setprio 0
	s_setprio 1
	v_mfma_f32_16x16x32_bf16 v[118:121], v[152:155], v[168:171], v[118:121]
	v_mfma_f32_16x16x32_bf16 v[114:117], v[160:163], v[168:171], v[114:117]
	v_mfma_f32_16x16x32_bf16 v[110:113], v[152:155], v[176:179], v[110:113]
	v_mfma_f32_16x16x32_bf16 v[106:109], v[160:163], v[176:179], v[106:109]
	v_mfma_f32_16x16x32_bf16 v[94:97], v[152:155], v[184:187], v[94:97]
	v_mfma_f32_16x16x32_bf16 v[90:93], v[160:163], v[184:187], v[90:93]
	v_mfma_f32_16x16x32_bf16 v[62:65], v[152:155], v[194:197], v[62:65]
	v_mfma_f32_16x16x32_bf16 v[58:61], v[160:163], v[194:197], v[58:61]
	v_mfma_f32_16x16x32_bf16 v[118:121], v[156:159], v[172:175], v[118:121]
	v_mfma_f32_16x16x32_bf16 v[114:117], v[164:167], v[172:175], v[114:117]
	v_mfma_f32_16x16x32_bf16 v[110:113], v[156:159], v[180:183], v[110:113]
	v_mfma_f32_16x16x32_bf16 v[106:109], v[164:167], v[180:183], v[106:109]
	v_mfma_f32_16x16x32_bf16 v[94:97], v[156:159], v[188:191], v[94:97]
	v_mfma_f32_16x16x32_bf16 v[90:93], v[164:167], v[188:191], v[90:93]
	v_mfma_f32_16x16x32_bf16 v[62:65], v[156:159], v[198:201], v[62:65]
	v_mfma_f32_16x16x32_bf16 v[58:61], v[164:167], v[198:201], v[58:61]
	s_barrier
	s_setprio 0
	s_mov_b32 m0, s74
	ds_read_b128 v[168:171], v219 offset:16384
	ds_read_b128 v[172:175], v219 offset:17408
	ds_read_b128 v[176:179], v219 offset:18432
	ds_read_b128 v[180:183], v219 offset:19456
	ds_read_b128 v[184:187], v219 offset:20480
	ds_read_b128 v[188:191], v219 offset:21504
	ds_read_b128 v[194:197], v219 offset:22528
	ds_read_b128 v[198:201], v219 offset:23552
	s_add_u32 s56, s30, s36
	global_load_lds_dwordx4 v0, s[30:31]
	s_mov_b32 m0, s75
	s_addc_u32 s57, s31, s37
	global_load_lds_dwordx4 v130, s[30:31]
	s_mov_b32 m0, s76
	s_nop 0
	global_load_lds_dwordx4 v0, s[56:57]
	s_mov_b32 m0, s77
	s_nop 0
	global_load_lds_dwordx4 v130, s[56:57]
	s_mov_b32 m0, s18
	s_nop 0
	global_load_lds_dwordx4 v217, s[34:35]
	s_mov_b32 m0, s20
	s_nop 0
	global_load_lds_dwordx4 v216, s[34:35]
	s_waitcnt vmcnt(8)
	s_waitcnt lgkmcnt(0)
	s_setprio 1
	s_barrier
	v_mfma_f32_16x16x32_bf16 v[70:73], v[136:139], v[168:171], v[70:73]
	v_mfma_f32_16x16x32_bf16 v[66:69], v[144:147], v[168:171], v[66:69]
	v_mfma_f32_16x16x32_bf16 v[38:41], v[136:139], v[176:179], v[38:41]
	v_mfma_f32_16x16x32_bf16 v[34:37], v[144:147], v[176:179], v[34:37]
	v_mfma_f32_16x16x32_bf16 v[22:25], v[136:139], v[184:187], v[22:25]
	v_mfma_f32_16x16x32_bf16 v[18:21], v[144:147], v[184:187], v[18:21]
	v_mfma_f32_16x16x32_bf16 v[6:9], v[136:139], v[194:197], v[6:9]
	v_mfma_f32_16x16x32_bf16 v[2:5], v[144:147], v[194:197], v[2:5]
	v_mfma_f32_16x16x32_bf16 v[70:73], v[140:143], v[172:175], v[70:73]
	v_mfma_f32_16x16x32_bf16 v[66:69], v[148:151], v[172:175], v[66:69]
	v_mfma_f32_16x16x32_bf16 v[38:41], v[140:143], v[180:183], v[38:41]
	v_mfma_f32_16x16x32_bf16 v[34:37], v[148:151], v[180:183], v[34:37]
	v_mfma_f32_16x16x32_bf16 v[22:25], v[140:143], v[188:191], v[22:25]
	v_mfma_f32_16x16x32_bf16 v[18:21], v[148:151], v[188:191], v[18:21]
	v_mfma_f32_16x16x32_bf16 v[6:9], v[140:143], v[198:201], v[6:9]
	v_mfma_f32_16x16x32_bf16 v[2:5], v[148:151], v[198:201], v[2:5]
	s_setprio 0
	s_setprio 1
	v_mfma_f32_16x16x32_bf16 v[78:81], v[152:155], v[168:171], v[78:81]
	v_mfma_f32_16x16x32_bf16 v[74:77], v[160:163], v[168:171], v[74:77]
	v_mfma_f32_16x16x32_bf16 v[46:49], v[152:155], v[176:179], v[46:49]
	v_mfma_f32_16x16x32_bf16 v[42:45], v[160:163], v[176:179], v[42:45]
	v_mfma_f32_16x16x32_bf16 v[30:33], v[152:155], v[184:187], v[30:33]
	v_mfma_f32_16x16x32_bf16 v[26:29], v[160:163], v[184:187], v[26:29]
	v_mfma_f32_16x16x32_bf16 v[14:17], v[152:155], v[194:197], v[14:17]
	v_mfma_f32_16x16x32_bf16 v[10:13], v[160:163], v[194:197], v[10:13]
	v_mfma_f32_16x16x32_bf16 v[78:81], v[156:159], v[172:175], v[78:81]
	v_mfma_f32_16x16x32_bf16 v[74:77], v[164:167], v[172:175], v[74:77]
	v_mfma_f32_16x16x32_bf16 v[46:49], v[156:159], v[180:183], v[46:49]
	v_mfma_f32_16x16x32_bf16 v[42:45], v[164:167], v[180:183], v[42:45]
	v_mfma_f32_16x16x32_bf16 v[30:33], v[156:159], v[188:191], v[30:33]
	v_mfma_f32_16x16x32_bf16 v[26:29], v[164:167], v[188:191], v[26:29]
	v_mfma_f32_16x16x32_bf16 v[14:17], v[156:159], v[198:201], v[14:17]
	v_mfma_f32_16x16x32_bf16 v[10:13], v[164:167], v[198:201], v[10:13]
	s_barrier
	s_setprio 0
	ds_read_b128 v[136:139], v134
	ds_read_b128 v[140:143], v134 offset:1024
	ds_read_b128 v[144:147], v134 offset:2048
	ds_read_b128 v[148:151], v134 offset:3072
	ds_read_b128 v[152:155], v135
	ds_read_b128 v[156:159], v135 offset:1024
	ds_read_b128 v[160:163], v135 offset:2048
	ds_read_b128 v[164:167], v135 offset:3072
	s_add_u32 s34, s34, 0x4000
	s_addc_u32 s35, s35, 0
	s_mov_b32 m0, s25
	ds_read_b128 v[168:171], v219 offset:32768
	ds_read_b128 v[172:175], v219 offset:33792
	ds_read_b128 v[176:179], v219 offset:34816
	ds_read_b128 v[180:183], v219 offset:35840
	ds_read_b128 v[184:187], v219 offset:36864
	ds_read_b128 v[188:191], v219 offset:37888
	ds_read_b128 v[194:197], v219 offset:38912
	ds_read_b128 v[198:201], v219 offset:39936
	s_nop 0
	global_load_lds_dwordx4 v217, s[34:35]
	s_mov_b32 m0, s60
	s_nop 0
	global_load_lds_dwordx4 v216, s[34:35]
	s_waitcnt vmcnt(8)
	s_waitcnt lgkmcnt(0)
	s_setprio 1
	s_barrier
	v_mfma_f32_16x16x32_bf16 v[126:129], v[136:139], v[168:171], v[126:129]
	v_mfma_f32_16x16x32_bf16 v[122:125], v[144:147], v[168:171], v[122:125]
	v_mfma_f32_16x16x32_bf16 v[102:105], v[136:139], v[176:179], v[102:105]
	v_mfma_f32_16x16x32_bf16 v[98:101], v[144:147], v[176:179], v[98:101]
	v_mfma_f32_16x16x32_bf16 v[86:89], v[136:139], v[184:187], v[86:89]
	v_mfma_f32_16x16x32_bf16 v[82:85], v[144:147], v[184:187], v[82:85]
	v_mfma_f32_16x16x32_bf16 v[54:57], v[136:139], v[194:197], v[54:57]
	v_mfma_f32_16x16x32_bf16 v[50:53], v[144:147], v[194:197], v[50:53]
	v_mfma_f32_16x16x32_bf16 v[126:129], v[140:143], v[172:175], v[126:129]
	v_mfma_f32_16x16x32_bf16 v[122:125], v[148:151], v[172:175], v[122:125]
	v_mfma_f32_16x16x32_bf16 v[102:105], v[140:143], v[180:183], v[102:105]
	v_mfma_f32_16x16x32_bf16 v[98:101], v[148:151], v[180:183], v[98:101]
	v_mfma_f32_16x16x32_bf16 v[86:89], v[140:143], v[188:191], v[86:89]
	v_mfma_f32_16x16x32_bf16 v[82:85], v[148:151], v[188:191], v[82:85]
	v_mfma_f32_16x16x32_bf16 v[54:57], v[140:143], v[198:201], v[54:57]
	v_mfma_f32_16x16x32_bf16 v[50:53], v[148:151], v[198:201], v[50:53]
	s_setprio 0
	s_setprio 1
	v_mfma_f32_16x16x32_bf16 v[118:121], v[152:155], v[168:171], v[118:121]
	v_mfma_f32_16x16x32_bf16 v[114:117], v[160:163], v[168:171], v[114:117]
	v_mfma_f32_16x16x32_bf16 v[110:113], v[152:155], v[176:179], v[110:113]
	v_mfma_f32_16x16x32_bf16 v[106:109], v[160:163], v[176:179], v[106:109]
	v_mfma_f32_16x16x32_bf16 v[94:97], v[152:155], v[184:187], v[94:97]
	v_mfma_f32_16x16x32_bf16 v[90:93], v[160:163], v[184:187], v[90:93]
	v_mfma_f32_16x16x32_bf16 v[62:65], v[152:155], v[194:197], v[62:65]
	v_mfma_f32_16x16x32_bf16 v[58:61], v[160:163], v[194:197], v[58:61]
	v_mfma_f32_16x16x32_bf16 v[118:121], v[156:159], v[172:175], v[118:121]
	v_mfma_f32_16x16x32_bf16 v[114:117], v[164:167], v[172:175], v[114:117]
	v_mfma_f32_16x16x32_bf16 v[110:113], v[156:159], v[180:183], v[110:113]
	v_mfma_f32_16x16x32_bf16 v[106:109], v[164:167], v[180:183], v[106:109]
	v_mfma_f32_16x16x32_bf16 v[94:97], v[156:159], v[188:191], v[94:97]
	v_mfma_f32_16x16x32_bf16 v[90:93], v[164:167], v[188:191], v[90:93]
	v_mfma_f32_16x16x32_bf16 v[62:65], v[156:159], v[198:201], v[62:65]
	v_mfma_f32_16x16x32_bf16 v[58:61], v[164:167], v[198:201], v[58:61]
	s_barrier
	s_setprio 0
	ds_read_b128 v[168:171], v219 offset:49152
	ds_read_b128 v[172:175], v219 offset:50176
	ds_read_b128 v[176:179], v219 offset:51200
	ds_read_b128 v[180:183], v219 offset:52224
	ds_read_b128 v[184:187], v219 offset:53248
	ds_read_b128 v[188:191], v219 offset:54272
	ds_read_b128 v[194:197], v219 offset:55296
	ds_read_b128 v[198:201], v219 offset:56320
	s_mov_b32 m0, s78
	v_lshl_add_u64 v[202:203], s[30:31], 0, v[0:1]
	v_lshl_add_u64 v[202:203], v[202:203], 0, s[16:17]
	v_mov_b32_e32 v131, v1
	global_load_lds_dwordx4 v[202:203], off
	s_mov_b32 m0, s79
	v_lshl_add_u64 v[202:203], s[30:31], 0, v[130:131]
	v_lshl_add_u64 v[202:203], v[202:203], 0, s[16:17]
	global_load_lds_dwordx4 v[202:203], off
	s_mov_b32 m0, s80
	v_lshl_add_u64 v[202:203], s[56:57], 0, v[0:1]
	v_lshl_add_u64 v[202:203], v[202:203], 0, s[16:17]
	global_load_lds_dwordx4 v[202:203], off
	s_mov_b32 m0, s58
	v_lshl_add_u64 v[202:203], s[56:57], 0, v[130:131]
	v_lshl_add_u64 v[202:203], v[202:203], 0, s[16:17]
	global_load_lds_dwordx4 v[202:203], off
	s_mov_b32 m0, s65
	s_nop 0
	global_load_lds_dwordx4 v217, s[28:29]
	s_mov_b32 m0, s66
	s_nop 0
	global_load_lds_dwordx4 v216, s[28:29]
	s_waitcnt vmcnt(8)
	s_waitcnt lgkmcnt(0)
	s_setprio 1
	s_barrier
	v_mfma_f32_16x16x32_bf16 v[70:73], v[136:139], v[168:171], v[70:73]
	v_mfma_f32_16x16x32_bf16 v[66:69], v[144:147], v[168:171], v[66:69]
	v_mfma_f32_16x16x32_bf16 v[38:41], v[136:139], v[176:179], v[38:41]
	v_mfma_f32_16x16x32_bf16 v[34:37], v[144:147], v[176:179], v[34:37]
	v_mfma_f32_16x16x32_bf16 v[22:25], v[136:139], v[184:187], v[22:25]
	v_mfma_f32_16x16x32_bf16 v[18:21], v[144:147], v[184:187], v[18:21]
	v_mfma_f32_16x16x32_bf16 v[6:9], v[136:139], v[194:197], v[6:9]
	v_mfma_f32_16x16x32_bf16 v[2:5], v[144:147], v[194:197], v[2:5]
	v_mfma_f32_16x16x32_bf16 v[70:73], v[140:143], v[172:175], v[70:73]
	v_mfma_f32_16x16x32_bf16 v[66:69], v[148:151], v[172:175], v[66:69]
	v_mfma_f32_16x16x32_bf16 v[38:41], v[140:143], v[180:183], v[38:41]
	v_mfma_f32_16x16x32_bf16 v[34:37], v[148:151], v[180:183], v[34:37]
	v_mfma_f32_16x16x32_bf16 v[22:25], v[140:143], v[188:191], v[22:25]
	v_mfma_f32_16x16x32_bf16 v[18:21], v[148:151], v[188:191], v[18:21]
	v_mfma_f32_16x16x32_bf16 v[6:9], v[140:143], v[198:201], v[6:9]
	v_mfma_f32_16x16x32_bf16 v[2:5], v[148:151], v[198:201], v[2:5]
	s_setprio 0
	s_setprio 1
	v_mfma_f32_16x16x32_bf16 v[78:81], v[152:155], v[168:171], v[78:81]
	v_mfma_f32_16x16x32_bf16 v[74:77], v[160:163], v[168:171], v[74:77]
	v_mfma_f32_16x16x32_bf16 v[46:49], v[152:155], v[176:179], v[46:49]
	v_mfma_f32_16x16x32_bf16 v[42:45], v[160:163], v[176:179], v[42:45]
	v_mfma_f32_16x16x32_bf16 v[30:33], v[152:155], v[184:187], v[30:33]
	v_mfma_f32_16x16x32_bf16 v[26:29], v[160:163], v[184:187], v[26:29]
	v_mfma_f32_16x16x32_bf16 v[14:17], v[152:155], v[194:197], v[14:17]
	v_mfma_f32_16x16x32_bf16 v[10:13], v[160:163], v[194:197], v[10:13]
	v_mfma_f32_16x16x32_bf16 v[78:81], v[156:159], v[172:175], v[78:81]
	v_mfma_f32_16x16x32_bf16 v[74:77], v[164:167], v[172:175], v[74:77]
	v_mfma_f32_16x16x32_bf16 v[46:49], v[156:159], v[180:183], v[46:49]
	v_mfma_f32_16x16x32_bf16 v[42:45], v[164:167], v[180:183], v[42:45]
	v_mfma_f32_16x16x32_bf16 v[30:33], v[156:159], v[188:191], v[30:33]
	v_mfma_f32_16x16x32_bf16 v[26:29], v[164:167], v[188:191], v[26:29]
	v_mfma_f32_16x16x32_bf16 v[14:17], v[156:159], v[198:201], v[14:17]
	v_mfma_f32_16x16x32_bf16 v[10:13], v[164:167], v[198:201], v[10:13]
	s_barrier
	s_setprio 0
	s_add_i32 s28, s82, 2
	s_add_u32 s59, s59, 0x100
	s_addc_u32 s81, s81, 0
	s_add_u32 s26, s26, 0x10000
	s_addc_u32 s27, s27, 0
	s_cmp_lt_i32 s82, s63
	s_mov_b32 s82, s28
	s_cbranch_scc1 .LBB0_967

.LBB0_1072:
	s_add_u32 s21, s26, 0x10000
	s_addc_u32 s34, s27, 0
	s_and_b64 s[30:31], s[48:49], exec
	s_cselect_b32 s55, s43, s34
	s_cselect_b32 s54, s42, s21
	s_add_u32 s21, s28, 0x100
	s_addc_u32 s56, s29, 0
	s_add_u32 s30, s54, 0x8000
	s_addc_u32 s31, s55, 0
	s_add_i32 s71, 0, 0x10000
	s_and_b64 s[34:35], s[48:49], exec
	s_cselect_b32 s35, s45, s56
	s_cselect_b32 s34, s44, s21
	s_add_i32 s73, 0, 0x14000
	v_add_u32_e32 v114, s71, v237
	v_add_u32_e32 v115, s73, v237
	ds_read_b128 v[2:5], v114
	s_waitcnt lgkmcnt(0)
	ds_read_b128 v[6:9], v114 offset:1024
	ds_read_b128 v[10:13], v114 offset:2048
	ds_read_b128 v[14:17], v114 offset:3072
	ds_read_b128 v[18:21], v115
	ds_read_b128 v[22:25], v115 offset:1024
	ds_read_b128 v[26:29], v115 offset:2048
	ds_read_b128 v[30:33], v115 offset:3072
	s_add_u32 s56, s26, 0xc000
	s_addc_u32 s57, s27, 0
	s_add_i32 s21, s20, 0xc000
	s_mov_b32 m0, s21
	s_add_i32 s70, s20, 0xe000
	ds_read_b128 v[34:37], v238
	ds_read_b128 v[38:41], v238 offset:1024
	ds_read_b128 v[42:45], v238 offset:2048
	ds_read_b128 v[46:49], v238 offset:3072
	ds_read_b128 v[50:53], v238 offset:4096
	ds_read_b128 v[54:57], v238 offset:5120
	ds_read_b128 v[58:61], v238 offset:6144
	ds_read_b128 v[62:65], v238 offset:7168
	s_nop 0
	global_load_lds_dwordx4 v236, s[56:57]
	s_mov_b32 m0, s70
	s_nop 0
	global_load_lds_dwordx4 v235, s[56:57]
	s_waitcnt vmcnt(8)
	s_waitcnt lgkmcnt(0)
	s_setprio 1
	s_barrier
	v_mfma_f32_16x16x32_bf16 v[90:93], v[2:5], v[58:61], 0
	v_mfma_f32_16x16x32_bf16 v[66:69], v[2:5], v[34:37], 0
	v_mfma_f32_16x16x32_bf16 v[70:73], v[10:13], v[34:37], 0
	v_mfma_f32_16x16x32_bf16 v[74:77], v[2:5], v[42:45], 0
	v_mfma_f32_16x16x32_bf16 v[78:81], v[10:13], v[42:45], 0
	v_mfma_f32_16x16x32_bf16 v[82:85], v[2:5], v[50:53], 0
	v_mfma_f32_16x16x32_bf16 v[86:89], v[10:13], v[50:53], 0
	v_mfma_f32_16x16x32_bf16 v[98:101], v[6:9], v[62:65], v[90:93]
	v_mfma_f32_16x16x32_bf16 v[90:93], v[10:13], v[58:61], 0
	v_mfma_f32_16x16x32_bf16 v[66:69], v[6:9], v[38:41], v[66:69]
	v_mfma_f32_16x16x32_bf16 v[70:73], v[14:17], v[38:41], v[70:73]
	v_mfma_f32_16x16x32_bf16 v[74:77], v[6:9], v[46:49], v[74:77]
	v_mfma_f32_16x16x32_bf16 v[78:81], v[14:17], v[46:49], v[78:81]
	v_mfma_f32_16x16x32_bf16 v[82:85], v[6:9], v[54:57], v[82:85]
	v_mfma_f32_16x16x32_bf16 v[86:89], v[14:17], v[54:57], v[86:89]
	v_mfma_f32_16x16x32_bf16 v[102:105], v[14:17], v[62:65], v[90:93]
	s_setprio 0
	s_setprio 1
	v_mfma_f32_16x16x32_bf16 v[90:93], v[18:21], v[34:37], 0
	v_mfma_f32_16x16x32_bf16 v[34:37], v[26:29], v[34:37], 0
	v_mfma_f32_16x16x32_bf16 v[118:121], v[22:25], v[38:41], v[90:93]
	v_mfma_f32_16x16x32_bf16 v[34:37], v[30:33], v[38:41], v[34:37]
	v_mfma_f32_16x16x32_bf16 v[38:41], v[18:21], v[42:45], 0
	v_mfma_f32_16x16x32_bf16 v[42:45], v[26:29], v[42:45], 0
	v_mfma_f32_16x16x32_bf16 v[38:41], v[22:25], v[46:49], v[38:41]
	v_mfma_f32_16x16x32_bf16 v[42:45], v[30:33], v[46:49], v[42:45]
	v_mfma_f32_16x16x32_bf16 v[46:49], v[18:21], v[50:53], 0
	v_mfma_f32_16x16x32_bf16 v[50:53], v[26:29], v[50:53], 0
	v_mfma_f32_16x16x32_bf16 v[46:49], v[22:25], v[54:57], v[46:49]
	v_mfma_f32_16x16x32_bf16 v[50:53], v[30:33], v[54:57], v[50:53]
	v_mfma_f32_16x16x32_bf16 v[54:57], v[18:21], v[58:61], 0
	v_mfma_f32_16x16x32_bf16 v[58:61], v[26:29], v[58:61], 0
	v_mfma_f32_16x16x32_bf16 v[54:57], v[22:25], v[62:65], v[54:57]
	v_mfma_f32_16x16x32_bf16 v[58:61], v[30:33], v[62:65], v[58:61]
	s_barrier
	s_setprio 0
	s_add_i32 s71, s71, s18
	s_add_i32 s72, s71, 0x2000
	s_mov_b32 m0, s71
	s_add_u32 s56, s34, s36
	ds_read_b128 v[62:65], v238 offset:16384
	ds_read_b128 v[90:93], v238 offset:17408
	ds_read_b128 v[94:97], v238 offset:18432
	ds_read_b128 v[106:109], v238 offset:19456
	ds_read_b128 v[110:113], v238 offset:20480
	ds_read_b128 v[122:125], v238 offset:21504
	ds_read_b128 v[126:129], v238 offset:22528
	ds_read_b128 v[130:133], v238 offset:23552
	s_addc_u32 s57, s35, s37
	global_load_lds_dwordx4 v0, s[34:35]
	s_mov_b32 m0, s72
	s_add_i32 s73, s73, s18
	s_add_i32 s74, s73, 0x2000
	global_load_lds_dwordx4 v210, s[34:35]
	s_mov_b32 m0, s73
	s_nop 0
	global_load_lds_dwordx4 v0, s[56:57]
	s_mov_b32 m0, s74
	s_nop 0
	global_load_lds_dwordx4 v210, s[56:57]
	s_mov_b32 m0, s20
	s_nop 0
	global_load_lds_dwordx4 v236, s[54:55]
	s_mov_b32 m0, s25
	s_nop 0
	global_load_lds_dwordx4 v235, s[54:55]
	s_waitcnt vmcnt(8)
	s_waitcnt lgkmcnt(0)
	s_setprio 1
	s_barrier
	v_mfma_f32_16x16x32_bf16 v[134:137], v[2:5], v[62:65], 0
	v_mfma_f32_16x16x32_bf16 v[142:145], v[2:5], v[94:97], 0
	v_mfma_f32_16x16x32_bf16 v[150:153], v[2:5], v[110:113], 0
	v_mfma_f32_16x16x32_bf16 v[2:5], v[2:5], v[126:129], 0
	v_mfma_f32_16x16x32_bf16 v[134:137], v[6:9], v[90:93], v[134:137]
	v_mfma_f32_16x16x32_bf16 v[142:145], v[6:9], v[106:109], v[142:145]
	v_mfma_f32_16x16x32_bf16 v[150:153], v[6:9], v[122:125], v[150:153]
	v_mfma_f32_16x16x32_bf16 v[2:5], v[6:9], v[130:133], v[2:5]
	v_mfma_f32_16x16x32_bf16 v[6:9], v[10:13], v[126:129], 0
	v_mfma_f32_16x16x32_bf16 v[138:141], v[10:13], v[62:65], 0
	v_mfma_f32_16x16x32_bf16 v[146:149], v[10:13], v[94:97], 0
	v_mfma_f32_16x16x32_bf16 v[154:157], v[10:13], v[110:113], 0
	v_mfma_f32_16x16x32_bf16 v[6:9], v[14:17], v[130:133], v[6:9]
	v_mfma_f32_16x16x32_bf16 v[138:141], v[14:17], v[90:93], v[138:141]
	v_mfma_f32_16x16x32_bf16 v[146:149], v[14:17], v[106:109], v[146:149]
	v_mfma_f32_16x16x32_bf16 v[154:157], v[14:17], v[122:125], v[154:157]
	s_setprio 0
	s_setprio 1
	v_mfma_f32_16x16x32_bf16 v[10:13], v[18:21], v[62:65], 0
	v_mfma_f32_16x16x32_bf16 v[158:161], v[22:25], v[90:93], v[10:13]
	v_mfma_f32_16x16x32_bf16 v[10:13], v[26:29], v[62:65], 0
	v_mfma_f32_16x16x32_bf16 v[170:173], v[30:33], v[90:93], v[10:13]
	v_mfma_f32_16x16x32_bf16 v[10:13], v[18:21], v[94:97], 0
	v_mfma_f32_16x16x32_bf16 v[174:177], v[22:25], v[106:109], v[10:13]
	v_mfma_f32_16x16x32_bf16 v[10:13], v[26:29], v[94:97], 0
	v_mfma_f32_16x16x32_bf16 v[178:181], v[30:33], v[106:109], v[10:13]
	v_mfma_f32_16x16x32_bf16 v[10:13], v[18:21], v[110:113], 0
	v_mfma_f32_16x16x32_bf16 v[182:185], v[22:25], v[122:125], v[10:13]
	v_mfma_f32_16x16x32_bf16 v[10:13], v[26:29], v[110:113], 0
	v_mfma_f32_16x16x32_bf16 v[186:189], v[30:33], v[122:125], v[10:13]
	v_mfma_f32_16x16x32_bf16 v[10:13], v[18:21], v[126:129], 0
	v_mfma_f32_16x16x32_bf16 v[194:197], v[22:25], v[130:133], v[10:13]
	v_mfma_f32_16x16x32_bf16 v[10:13], v[26:29], v[126:129], 0
	v_mfma_f32_16x16x32_bf16 v[126:129], v[30:33], v[130:133], v[10:13]
	s_barrier
	s_setprio 0
	s_add_i32 s75, 0, 0x18000
	s_add_i32 s77, 0, 0x1c000
	v_add_u32_e32 v116, s75, v237
	v_add_u32_e32 v117, s77, v237
	s_nop 0
	ds_read_b128 v[10:13], v116
	ds_read_b128 v[14:17], v116 offset:1024
	ds_read_b128 v[18:21], v116 offset:2048
	ds_read_b128 v[22:25], v116 offset:3072
	ds_read_b128 v[130:133], v117
	ds_read_b128 v[198:201], v117 offset:1024
	ds_read_b128 v[202:205], v117 offset:2048
	ds_read_b128 v[206:209], v117 offset:3072
	s_add_u32 s54, s54, 0x4000
	s_addc_u32 s55, s55, 0
	s_mov_b32 m0, s58
	ds_read_b128 v[26:29], v238 offset:32768
	ds_read_b128 v[30:33], v238 offset:33792
	ds_read_b128 v[62:65], v238 offset:34816
	ds_read_b128 v[212:215], v238 offset:35840
	ds_read_b128 v[216:219], v238 offset:36864
	ds_read_b128 v[220:223], v238 offset:37888
	ds_read_b128 v[224:227], v238 offset:38912
	ds_read_b128 v[240:243], v238 offset:39936
	s_nop 0
	global_load_lds_dwordx4 v236, s[54:55]
	s_mov_b32 m0, s59
	s_nop 0
	global_load_lds_dwordx4 v235, s[54:55]
	s_waitcnt vmcnt(8)
	s_waitcnt lgkmcnt(0)
	s_setprio 1
	s_barrier
	v_mfma_f32_16x16x32_bf16 v[66:69], v[10:13], v[26:29], v[66:69]
	v_mfma_f32_16x16x32_bf16 v[162:165], v[14:17], v[30:33], v[66:69]
	v_mfma_f32_16x16x32_bf16 v[66:69], v[18:21], v[26:29], v[70:73]
	v_mfma_f32_16x16x32_bf16 v[166:169], v[22:25], v[30:33], v[66:69]
	v_mfma_f32_16x16x32_bf16 v[66:69], v[10:13], v[62:65], v[74:77]
	v_mfma_f32_16x16x32_bf16 v[110:113], v[14:17], v[212:215], v[66:69]
	v_mfma_f32_16x16x32_bf16 v[66:69], v[18:21], v[62:65], v[78:81]
	v_mfma_f32_16x16x32_bf16 v[106:109], v[22:25], v[212:215], v[66:69]
	v_mfma_f32_16x16x32_bf16 v[66:69], v[10:13], v[216:219], v[82:85]
	v_mfma_f32_16x16x32_bf16 v[94:97], v[14:17], v[220:223], v[66:69]
	v_mfma_f32_16x16x32_bf16 v[66:69], v[18:21], v[216:219], v[86:89]
	v_mfma_f32_16x16x32_bf16 v[90:93], v[22:25], v[220:223], v[66:69]
	v_mfma_f32_16x16x32_bf16 v[66:69], v[10:13], v[224:227], v[98:101]
	v_mfma_f32_16x16x32_bf16 v[70:73], v[14:17], v[240:243], v[66:69]
	v_mfma_f32_16x16x32_bf16 v[66:69], v[18:21], v[224:227], v[102:105]
	v_mfma_f32_16x16x32_bf16 v[66:69], v[22:25], v[240:243], v[66:69]
	s_setprio 0
	s_setprio 1
	v_mfma_f32_16x16x32_bf16 v[74:77], v[130:133], v[26:29], v[118:121]
	v_mfma_f32_16x16x32_bf16 v[26:29], v[202:205], v[26:29], v[34:37]
	v_mfma_f32_16x16x32_bf16 v[118:121], v[206:209], v[30:33], v[26:29]
	v_mfma_f32_16x16x32_bf16 v[26:29], v[130:133], v[62:65], v[38:41]
	v_mfma_f32_16x16x32_bf16 v[102:105], v[198:201], v[212:215], v[26:29]
	v_mfma_f32_16x16x32_bf16 v[26:29], v[202:205], v[62:65], v[42:45]
	v_mfma_f32_16x16x32_bf16 v[98:101], v[206:209], v[212:215], v[26:29]
	v_mfma_f32_16x16x32_bf16 v[26:29], v[130:133], v[216:219], v[46:49]
	v_mfma_f32_16x16x32_bf16 v[86:89], v[198:201], v[220:223], v[26:29]
	v_mfma_f32_16x16x32_bf16 v[26:29], v[202:205], v[216:219], v[50:53]
	v_mfma_f32_16x16x32_bf16 v[82:85], v[206:209], v[220:223], v[26:29]
	v_mfma_f32_16x16x32_bf16 v[26:29], v[130:133], v[224:227], v[54:57]
	v_mfma_f32_16x16x32_bf16 v[54:57], v[198:201], v[240:243], v[26:29]
	v_mfma_f32_16x16x32_bf16 v[26:29], v[202:205], v[224:227], v[58:61]
	v_mfma_f32_16x16x32_bf16 v[122:125], v[198:201], v[30:33], v[74:77]
	v_mfma_f32_16x16x32_bf16 v[50:53], v[206:209], v[240:243], v[26:29]
	s_barrier
	s_setprio 0
	ds_read_b128 v[34:37], v238 offset:49152
	ds_read_b128 v[38:41], v238 offset:50176
	ds_read_b128 v[212:215], v238 offset:51200
	ds_read_b128 v[216:219], v238 offset:52224
	ds_read_b128 v[220:223], v238 offset:53248
	ds_read_b128 v[224:227], v238 offset:54272
	ds_read_b128 v[240:243], v238 offset:55296
	ds_read_b128 v[244:247], v238 offset:56320
	s_add_i32 s75, s75, s18
	v_lshl_add_u64 v[26:27], s[34:35], 0, v[0:1]
	v_lshl_add_u64 v[26:27], v[26:27], 0, s[16:17]
	s_mov_b32 m0, s75
	v_mov_b32_e32 v211, v1
	global_load_lds_dwordx4 v[26:27], off
	s_add_i32 s76, s75, 0x2000
	v_lshl_add_u64 v[26:27], s[34:35], 0, v[210:211]
	v_lshl_add_u64 v[26:27], v[26:27], 0, s[16:17]
	s_mov_b32 m0, s76
	s_add_i32 s77, s77, s18
	global_load_lds_dwordx4 v[26:27], off
	s_mov_b32 m0, s77
	v_lshl_add_u64 v[26:27], s[56:57], 0, v[0:1]
	v_lshl_add_u64 v[26:27], v[26:27], 0, s[16:17]
	global_load_lds_dwordx4 v[26:27], off
	s_nop 0
	v_lshl_add_u64 v[26:27], s[56:57], 0, v[210:211]
	s_add_i32 s56, s77, 0x2000
	v_lshl_add_u64 v[26:27], v[26:27], 0, s[16:17]
	s_mov_b32 m0, s56
	s_nop 0
	global_load_lds_dwordx4 v[26:27], off
	s_mov_b32 m0, s62
	s_nop 0
	global_load_lds_dwordx4 v236, s[30:31]
	s_mov_b32 m0, s63
	s_nop 0
	global_load_lds_dwordx4 v235, s[30:31]
	s_waitcnt vmcnt(8)
	s_waitcnt lgkmcnt(0)
	s_setprio 1
	s_barrier
	v_mfma_f32_16x16x32_bf16 v[26:29], v[10:13], v[34:37], v[134:137]
	v_mfma_f32_16x16x32_bf16 v[78:81], v[14:17], v[38:41], v[26:29]
	v_mfma_f32_16x16x32_bf16 v[26:29], v[18:21], v[34:37], v[138:141]
	v_mfma_f32_16x16x32_bf16 v[74:77], v[22:25], v[38:41], v[26:29]
	v_mfma_f32_16x16x32_bf16 v[26:29], v[10:13], v[212:215], v[142:145]
	v_mfma_f32_16x16x32_bf16 v[46:49], v[14:17], v[216:219], v[26:29]
	v_mfma_f32_16x16x32_bf16 v[26:29], v[18:21], v[212:215], v[146:149]
	v_mfma_f32_16x16x32_bf16 v[42:45], v[22:25], v[216:219], v[26:29]
	v_mfma_f32_16x16x32_bf16 v[26:29], v[10:13], v[220:223], v[150:153]
	v_mfma_f32_16x16x32_bf16 v[2:5], v[10:13], v[240:243], v[2:5]
	v_mfma_f32_16x16x32_bf16 v[30:33], v[14:17], v[224:227], v[26:29]
	v_mfma_f32_16x16x32_bf16 v[26:29], v[18:21], v[220:223], v[154:157]
	v_mfma_f32_16x16x32_bf16 v[14:17], v[14:17], v[244:247], v[2:5]
	v_mfma_f32_16x16x32_bf16 v[2:5], v[18:21], v[240:243], v[6:9]
	v_mfma_f32_16x16x32_bf16 v[26:29], v[22:25], v[224:227], v[26:29]
	v_mfma_f32_16x16x32_bf16 v[10:13], v[22:25], v[244:247], v[2:5]
	s_setprio 0
	s_setprio 1
	v_mfma_f32_16x16x32_bf16 v[2:5], v[130:133], v[34:37], v[158:161]
	v_mfma_f32_16x16x32_bf16 v[62:65], v[198:201], v[38:41], v[2:5]
	v_mfma_f32_16x16x32_bf16 v[2:5], v[202:205], v[34:37], v[170:173]
	v_mfma_f32_16x16x32_bf16 v[58:61], v[206:209], v[38:41], v[2:5]
	v_mfma_f32_16x16x32_bf16 v[2:5], v[130:133], v[212:215], v[174:177]
	v_mfma_f32_16x16x32_bf16 v[38:41], v[198:201], v[216:219], v[2:5]
	v_mfma_f32_16x16x32_bf16 v[2:5], v[202:205], v[212:215], v[178:181]
	v_mfma_f32_16x16x32_bf16 v[34:37], v[206:209], v[216:219], v[2:5]
	v_mfma_f32_16x16x32_bf16 v[2:5], v[130:133], v[220:223], v[182:185]
	v_mfma_f32_16x16x32_bf16 v[22:25], v[198:201], v[224:227], v[2:5]
	v_mfma_f32_16x16x32_bf16 v[2:5], v[202:205], v[220:223], v[186:189]
	v_mfma_f32_16x16x32_bf16 v[18:21], v[206:209], v[224:227], v[2:5]
	v_mfma_f32_16x16x32_bf16 v[2:5], v[130:133], v[240:243], v[194:197]
	v_mfma_f32_16x16x32_bf16 v[6:9], v[198:201], v[244:247], v[2:5]
	v_mfma_f32_16x16x32_bf16 v[2:5], v[202:205], v[240:243], v[126:129]
	v_mfma_f32_16x16x32_bf16 v[2:5], v[206:209], v[244:247], v[2:5]
	s_barrier
	s_setprio 0
	s_andn2_b64 vcc, exec, s[50:51]
	s_cbranch_vccnz .LBB0_1075
	s_add_u32 s57, s28, 0x200
	s_addc_u32 s78, s29, 0
	s_add_u32 s26, s26, 0x1c000
	s_addc_u32 s27, s27, 0
	s_mov_b32 s79, 4
.LBB0_1074:
	ds_read_b128 v[126:129], v114
	ds_read_b128 v[130:133], v114 offset:1024
	ds_read_b128 v[134:137], v114 offset:2048
	ds_read_b128 v[138:141], v114 offset:3072
	ds_read_b128 v[142:145], v115
	ds_read_b128 v[146:149], v115 offset:1024
	ds_read_b128 v[150:153], v115 offset:2048
	ds_read_b128 v[154:157], v115 offset:3072
	s_add_u32 s28, s26, 0x4000
	s_addc_u32 s29, s27, 0
	s_cmp_eq_u32 s60, s79
	s_cselect_b32 s34, s42, s28
	s_cselect_b32 s35, s43, s29
	s_cselect_b32 s30, s44, s57
	s_cselect_b32 s31, s45, s78
	s_add_u32 s28, s34, 0x8000
	s_addc_u32 s29, s35, 0
	s_mov_b32 m0, s21
	ds_read_b128 v[158:161], v238
	ds_read_b128 v[170:173], v238 offset:1024
	ds_read_b128 v[174:177], v238 offset:2048
	ds_read_b128 v[178:181], v238 offset:3072
	ds_read_b128 v[182:185], v238 offset:4096
	ds_read_b128 v[186:189], v238 offset:5120
	ds_read_b128 v[194:197], v238 offset:6144
	ds_read_b128 v[198:201], v238 offset:7168
	s_nop 0
	global_load_lds_dwordx4 v236, s[26:27]
	s_mov_b32 m0, s70
	s_nop 0
	global_load_lds_dwordx4 v235, s[26:27]
	s_waitcnt vmcnt(8)
	s_waitcnt lgkmcnt(0)
	s_setprio 1
	s_barrier
	v_mfma_f32_16x16x32_bf16 v[162:165], v[126:129], v[158:161], v[162:165]
	v_mfma_f32_16x16x32_bf16 v[166:169], v[134:137], v[158:161], v[166:169]
	v_mfma_f32_16x16x32_bf16 v[110:113], v[126:129], v[174:177], v[110:113]
	v_mfma_f32_16x16x32_bf16 v[106:109], v[134:137], v[174:177], v[106:109]
	v_mfma_f32_16x16x32_bf16 v[94:97], v[126:129], v[182:185], v[94:97]
	v_mfma_f32_16x16x32_bf16 v[90:93], v[134:137], v[182:185], v[90:93]
	v_mfma_f32_16x16x32_bf16 v[70:73], v[126:129], v[194:197], v[70:73]
	v_mfma_f32_16x16x32_bf16 v[66:69], v[134:137], v[194:197], v[66:69]
	v_mfma_f32_16x16x32_bf16 v[162:165], v[130:133], v[170:173], v[162:165]
	v_mfma_f32_16x16x32_bf16 v[166:169], v[138:141], v[170:173], v[166:169]
	v_mfma_f32_16x16x32_bf16 v[110:113], v[130:133], v[178:181], v[110:113]
	v_mfma_f32_16x16x32_bf16 v[106:109], v[138:141], v[178:181], v[106:109]
	v_mfma_f32_16x16x32_bf16 v[94:97], v[130:133], v[186:189], v[94:97]
	v_mfma_f32_16x16x32_bf16 v[90:93], v[138:141], v[186:189], v[90:93]
	v_mfma_f32_16x16x32_bf16 v[70:73], v[130:133], v[198:201], v[70:73]
	v_mfma_f32_16x16x32_bf16 v[66:69], v[138:141], v[198:201], v[66:69]
	s_setprio 0
	s_setprio 1
	v_mfma_f32_16x16x32_bf16 v[122:125], v[142:145], v[158:161], v[122:125]
	v_mfma_f32_16x16x32_bf16 v[118:121], v[150:153], v[158:161], v[118:121]
	v_mfma_f32_16x16x32_bf16 v[102:105], v[142:145], v[174:177], v[102:105]
	v_mfma_f32_16x16x32_bf16 v[98:101], v[150:153], v[174:177], v[98:101]
	v_mfma_f32_16x16x32_bf16 v[86:89], v[142:145], v[182:185], v[86:89]
	v_mfma_f32_16x16x32_bf16 v[82:85], v[150:153], v[182:185], v[82:85]
	v_mfma_f32_16x16x32_bf16 v[54:57], v[142:145], v[194:197], v[54:57]
	v_mfma_f32_16x16x32_bf16 v[50:53], v[150:153], v[194:197], v[50:53]
	v_mfma_f32_16x16x32_bf16 v[122:125], v[146:149], v[170:173], v[122:125]
	v_mfma_f32_16x16x32_bf16 v[118:121], v[154:157], v[170:173], v[118:121]
	v_mfma_f32_16x16x32_bf16 v[102:105], v[146:149], v[178:181], v[102:105]
	v_mfma_f32_16x16x32_bf16 v[98:101], v[154:157], v[178:181], v[98:101]
	v_mfma_f32_16x16x32_bf16 v[86:89], v[146:149], v[186:189], v[86:89]
	v_mfma_f32_16x16x32_bf16 v[82:85], v[154:157], v[186:189], v[82:85]
	v_mfma_f32_16x16x32_bf16 v[54:57], v[146:149], v[198:201], v[54:57]
	v_mfma_f32_16x16x32_bf16 v[50:53], v[154:157], v[198:201], v[50:53]
	s_barrier
	s_setprio 0
	s_mov_b32 m0, s71
	ds_read_b128 v[158:161], v238 offset:16384
	ds_read_b128 v[170:173], v238 offset:17408
	ds_read_b128 v[174:177], v238 offset:18432
	ds_read_b128 v[178:181], v238 offset:19456
	ds_read_b128 v[182:185], v238 offset:20480
	ds_read_b128 v[186:189], v238 offset:21504
	ds_read_b128 v[194:197], v238 offset:22528
	ds_read_b128 v[198:201], v238 offset:23552
	s_add_u32 s54, s30, s36
	global_load_lds_dwordx4 v0, s[30:31]
	s_mov_b32 m0, s72
	s_addc_u32 s55, s31, s37
	global_load_lds_dwordx4 v210, s[30:31]
	s_mov_b32 m0, s73
	s_nop 0
	global_load_lds_dwordx4 v0, s[54:55]
	s_mov_b32 m0, s74
	s_nop 0
	global_load_lds_dwordx4 v210, s[54:55]
	s_mov_b32 m0, s20
	s_nop 0
	global_load_lds_dwordx4 v236, s[34:35]
	s_mov_b32 m0, s25
	s_nop 0
	global_load_lds_dwordx4 v235, s[34:35]
	s_waitcnt vmcnt(8)
	s_waitcnt lgkmcnt(0)
	s_setprio 1
	s_barrier
	v_mfma_f32_16x16x32_bf16 v[78:81], v[126:129], v[158:161], v[78:81]
	v_mfma_f32_16x16x32_bf16 v[74:77], v[134:137], v[158:161], v[74:77]
	v_mfma_f32_16x16x32_bf16 v[46:49], v[126:129], v[174:177], v[46:49]
	v_mfma_f32_16x16x32_bf16 v[42:45], v[134:137], v[174:177], v[42:45]
	v_mfma_f32_16x16x32_bf16 v[30:33], v[126:129], v[182:185], v[30:33]
	v_mfma_f32_16x16x32_bf16 v[26:29], v[134:137], v[182:185], v[26:29]
	v_mfma_f32_16x16x32_bf16 v[14:17], v[126:129], v[194:197], v[14:17]
	v_mfma_f32_16x16x32_bf16 v[10:13], v[134:137], v[194:197], v[10:13]
	v_mfma_f32_16x16x32_bf16 v[78:81], v[130:133], v[170:173], v[78:81]
	v_mfma_f32_16x16x32_bf16 v[74:77], v[138:141], v[170:173], v[74:77]
	v_mfma_f32_16x16x32_bf16 v[46:49], v[130:133], v[178:181], v[46:49]
	v_mfma_f32_16x16x32_bf16 v[42:45], v[138:141], v[178:181], v[42:45]
	v_mfma_f32_16x16x32_bf16 v[30:33], v[130:133], v[186:189], v[30:33]
	v_mfma_f32_16x16x32_bf16 v[26:29], v[138:141], v[186:189], v[26:29]
	v_mfma_f32_16x16x32_bf16 v[14:17], v[130:133], v[198:201], v[14:17]
	v_mfma_f32_16x16x32_bf16 v[10:13], v[138:141], v[198:201], v[10:13]
	s_setprio 0
	s_setprio 1
	v_mfma_f32_16x16x32_bf16 v[62:65], v[142:145], v[158:161], v[62:65]
	v_mfma_f32_16x16x32_bf16 v[58:61], v[150:153], v[158:161], v[58:61]
	v_mfma_f32_16x16x32_bf16 v[38:41], v[142:145], v[174:177], v[38:41]
	v_mfma_f32_16x16x32_bf16 v[34:37], v[150:153], v[174:177], v[34:37]
	v_mfma_f32_16x16x32_bf16 v[22:25], v[142:145], v[182:185], v[22:25]
	v_mfma_f32_16x16x32_bf16 v[18:21], v[150:153], v[182:185], v[18:21]
	v_mfma_f32_16x16x32_bf16 v[6:9], v[142:145], v[194:197], v[6:9]
	v_mfma_f32_16x16x32_bf16 v[2:5], v[150:153], v[194:197], v[2:5]
	v_mfma_f32_16x16x32_bf16 v[62:65], v[146:149], v[170:173], v[62:65]
	v_mfma_f32_16x16x32_bf16 v[58:61], v[154:157], v[170:173], v[58:61]
	v_mfma_f32_16x16x32_bf16 v[38:41], v[146:149], v[178:181], v[38:41]
	v_mfma_f32_16x16x32_bf16 v[34:37], v[154:157], v[178:181], v[34:37]
	v_mfma_f32_16x16x32_bf16 v[22:25], v[146:149], v[186:189], v[22:25]
	v_mfma_f32_16x16x32_bf16 v[18:21], v[154:157], v[186:189], v[18:21]
	v_mfma_f32_16x16x32_bf16 v[6:9], v[146:149], v[198:201], v[6:9]
	v_mfma_f32_16x16x32_bf16 v[2:5], v[154:157], v[198:201], v[2:5]
	s_barrier
	s_setprio 0
	ds_read_b128 v[126:129], v116
	ds_read_b128 v[130:133], v116 offset:1024
	ds_read_b128 v[134:137], v116 offset:2048
	ds_read_b128 v[138:141], v116 offset:3072
	ds_read_b128 v[142:145], v117
	ds_read_b128 v[146:149], v117 offset:1024
	ds_read_b128 v[150:153], v117 offset:2048
	ds_read_b128 v[154:157], v117 offset:3072
	s_add_u32 s34, s34, 0x4000
	s_addc_u32 s35, s35, 0
	s_mov_b32 m0, s58
	ds_read_b128 v[158:161], v238 offset:32768
	ds_read_b128 v[170:173], v238 offset:33792
	ds_read_b128 v[174:177], v238 offset:34816
	ds_read_b128 v[178:181], v238 offset:35840
	ds_read_b128 v[182:185], v238 offset:36864
	ds_read_b128 v[186:189], v238 offset:37888
	ds_read_b128 v[194:197], v238 offset:38912
	ds_read_b128 v[198:201], v238 offset:39936
	s_nop 0
	global_load_lds_dwordx4 v236, s[34:35]
	s_mov_b32 m0, s59
	s_nop 0
	global_load_lds_dwordx4 v235, s[34:35]
	s_waitcnt vmcnt(8)
	s_waitcnt lgkmcnt(0)
	s_setprio 1
	s_barrier
	v_mfma_f32_16x16x32_bf16 v[162:165], v[126:129], v[158:161], v[162:165]
	v_mfma_f32_16x16x32_bf16 v[166:169], v[134:137], v[158:161], v[166:169]
	v_mfma_f32_16x16x32_bf16 v[110:113], v[126:129], v[174:177], v[110:113]
	v_mfma_f32_16x16x32_bf16 v[106:109], v[134:137], v[174:177], v[106:109]
	v_mfma_f32_16x16x32_bf16 v[94:97], v[126:129], v[182:185], v[94:97]
	v_mfma_f32_16x16x32_bf16 v[90:93], v[134:137], v[182:185], v[90:93]
	v_mfma_f32_16x16x32_bf16 v[70:73], v[126:129], v[194:197], v[70:73]
	v_mfma_f32_16x16x32_bf16 v[66:69], v[134:137], v[194:197], v[66:69]
	v_mfma_f32_16x16x32_bf16 v[162:165], v[130:133], v[170:173], v[162:165]
	v_mfma_f32_16x16x32_bf16 v[166:169], v[138:141], v[170:173], v[166:169]
	v_mfma_f32_16x16x32_bf16 v[110:113], v[130:133], v[178:181], v[110:113]
	v_mfma_f32_16x16x32_bf16 v[106:109], v[138:141], v[178:181], v[106:109]
	v_mfma_f32_16x16x32_bf16 v[94:97], v[130:133], v[186:189], v[94:97]
	v_mfma_f32_16x16x32_bf16 v[90:93], v[138:141], v[186:189], v[90:93]
	v_mfma_f32_16x16x32_bf16 v[70:73], v[130:133], v[198:201], v[70:73]
	v_mfma_f32_16x16x32_bf16 v[66:69], v[138:141], v[198:201], v[66:69]
	s_setprio 0
	s_setprio 1
	v_mfma_f32_16x16x32_bf16 v[122:125], v[142:145], v[158:161], v[122:125]
	v_mfma_f32_16x16x32_bf16 v[118:121], v[150:153], v[158:161], v[118:121]
	v_mfma_f32_16x16x32_bf16 v[102:105], v[142:145], v[174:177], v[102:105]
	v_mfma_f32_16x16x32_bf16 v[98:101], v[150:153], v[174:177], v[98:101]
	v_mfma_f32_16x16x32_bf16 v[86:89], v[142:145], v[182:185], v[86:89]
	v_mfma_f32_16x16x32_bf16 v[82:85], v[150:153], v[182:185], v[82:85]
	v_mfma_f32_16x16x32_bf16 v[54:57], v[142:145], v[194:197], v[54:57]
	v_mfma_f32_16x16x32_bf16 v[50:53], v[150:153], v[194:197], v[50:53]
	v_mfma_f32_16x16x32_bf16 v[122:125], v[146:149], v[170:173], v[122:125]
	v_mfma_f32_16x16x32_bf16 v[118:121], v[154:157], v[170:173], v[118:121]
	v_mfma_f32_16x16x32_bf16 v[102:105], v[146:149], v[178:181], v[102:105]
	v_mfma_f32_16x16x32_bf16 v[98:101], v[154:157], v[178:181], v[98:101]
	v_mfma_f32_16x16x32_bf16 v[86:89], v[146:149], v[186:189], v[86:89]
	v_mfma_f32_16x16x32_bf16 v[82:85], v[154:157], v[186:189], v[82:85]
	v_mfma_f32_16x16x32_bf16 v[54:57], v[146:149], v[198:201], v[54:57]
	v_mfma_f32_16x16x32_bf16 v[50:53], v[154:157], v[198:201], v[50:53]
	s_barrier
	s_setprio 0
	ds_read_b128 v[158:161], v238 offset:49152
	ds_read_b128 v[170:173], v238 offset:50176
	ds_read_b128 v[174:177], v238 offset:51200
	ds_read_b128 v[178:181], v238 offset:52224
	ds_read_b128 v[182:185], v238 offset:53248
	ds_read_b128 v[186:189], v238 offset:54272
	ds_read_b128 v[194:197], v238 offset:55296
	ds_read_b128 v[198:201], v238 offset:56320
	s_mov_b32 m0, s75
	v_lshl_add_u64 v[190:191], s[30:31], 0, v[0:1]
	v_lshl_add_u64 v[190:191], v[190:191], 0, s[16:17]
	v_mov_b32_e32 v211, v1
	global_load_lds_dwordx4 v[190:191], off
	s_mov_b32 m0, s76
	v_lshl_add_u64 v[190:191], s[30:31], 0, v[210:211]
	v_lshl_add_u64 v[190:191], v[190:191], 0, s[16:17]
	global_load_lds_dwordx4 v[190:191], off
	s_mov_b32 m0, s77
	v_lshl_add_u64 v[190:191], s[54:55], 0, v[0:1]
	v_lshl_add_u64 v[190:191], v[190:191], 0, s[16:17]
	global_load_lds_dwordx4 v[190:191], off
	s_mov_b32 m0, s56
	v_lshl_add_u64 v[190:191], s[54:55], 0, v[210:211]
	v_lshl_add_u64 v[190:191], v[190:191], 0, s[16:17]
	global_load_lds_dwordx4 v[190:191], off
	s_mov_b32 m0, s62
	s_nop 0
	global_load_lds_dwordx4 v236, s[28:29]
	s_mov_b32 m0, s63
	s_nop 0
	global_load_lds_dwordx4 v235, s[28:29]
	s_waitcnt vmcnt(8)
	s_waitcnt lgkmcnt(0)
	s_setprio 1
	s_barrier
	v_mfma_f32_16x16x32_bf16 v[78:81], v[126:129], v[158:161], v[78:81]
	v_mfma_f32_16x16x32_bf16 v[74:77], v[134:137], v[158:161], v[74:77]
	v_mfma_f32_16x16x32_bf16 v[46:49], v[126:129], v[174:177], v[46:49]
	v_mfma_f32_16x16x32_bf16 v[42:45], v[134:137], v[174:177], v[42:45]
	v_mfma_f32_16x16x32_bf16 v[30:33], v[126:129], v[182:185], v[30:33]
	v_mfma_f32_16x16x32_bf16 v[26:29], v[134:137], v[182:185], v[26:29]
	v_mfma_f32_16x16x32_bf16 v[14:17], v[126:129], v[194:197], v[14:17]
	v_mfma_f32_16x16x32_bf16 v[10:13], v[134:137], v[194:197], v[10:13]
	v_mfma_f32_16x16x32_bf16 v[78:81], v[130:133], v[170:173], v[78:81]
	v_mfma_f32_16x16x32_bf16 v[74:77], v[138:141], v[170:173], v[74:77]
	v_mfma_f32_16x16x32_bf16 v[46:49], v[130:133], v[178:181], v[46:49]
	v_mfma_f32_16x16x32_bf16 v[42:45], v[138:141], v[178:181], v[42:45]
	v_mfma_f32_16x16x32_bf16 v[30:33], v[130:133], v[186:189], v[30:33]
	v_mfma_f32_16x16x32_bf16 v[26:29], v[138:141], v[186:189], v[26:29]
	v_mfma_f32_16x16x32_bf16 v[14:17], v[130:133], v[198:201], v[14:17]
	v_mfma_f32_16x16x32_bf16 v[10:13], v[138:141], v[198:201], v[10:13]
	s_setprio 0
	s_setprio 1
	v_mfma_f32_16x16x32_bf16 v[62:65], v[142:145], v[158:161], v[62:65]
	v_mfma_f32_16x16x32_bf16 v[58:61], v[150:153], v[158:161], v[58:61]
	v_mfma_f32_16x16x32_bf16 v[38:41], v[142:145], v[174:177], v[38:41]
	v_mfma_f32_16x16x32_bf16 v[34:37], v[150:153], v[174:177], v[34:37]
	v_mfma_f32_16x16x32_bf16 v[22:25], v[142:145], v[182:185], v[22:25]
	v_mfma_f32_16x16x32_bf16 v[18:21], v[150:153], v[182:185], v[18:21]
	v_mfma_f32_16x16x32_bf16 v[6:9], v[142:145], v[194:197], v[6:9]
	v_mfma_f32_16x16x32_bf16 v[2:5], v[150:153], v[194:197], v[2:5]
	v_mfma_f32_16x16x32_bf16 v[62:65], v[146:149], v[170:173], v[62:65]
	v_mfma_f32_16x16x32_bf16 v[58:61], v[154:157], v[170:173], v[58:61]
	v_mfma_f32_16x16x32_bf16 v[38:41], v[146:149], v[178:181], v[38:41]
	v_mfma_f32_16x16x32_bf16 v[34:37], v[154:157], v[178:181], v[34:37]
	v_mfma_f32_16x16x32_bf16 v[22:25], v[146:149], v[186:189], v[22:25]
	v_mfma_f32_16x16x32_bf16 v[18:21], v[154:157], v[186:189], v[18:21]
	v_mfma_f32_16x16x32_bf16 v[6:9], v[146:149], v[198:201], v[6:9]
	v_mfma_f32_16x16x32_bf16 v[2:5], v[154:157], v[198:201], v[2:5]
	s_barrier
	s_setprio 0
	s_add_i32 s28, s79, 2
	s_add_u32 s57, s57, 0x100
	s_addc_u32 s78, s78, 0
	s_add_u32 s26, s26, 0x10000
	s_addc_u32 s27, s27, 0
	s_cmp_lt_i32 s79, s60
	s_mov_b32 s79, s28
	s_cbranch_scc1 .LBB0_1074

.LBB0_1147:
	s_or_b64 exec, exec, s[58:59]
	s_add_u32 s60, s54, 0x10000
	s_addc_u32 s61, s55, 0
	s_and_b64 s[58:59], s[34:35], exec
	s_cselect_b32 s65, s49, s61
	s_cselect_b32 s64, s48, s60
	s_add_u32 s60, s56, 0x10000
	s_addc_u32 s61, s57, 0
	s_and_b64 s[58:59], s[34:35], exec
	s_cselect_b32 s61, s51, s61
	s_cselect_b32 s60, s50, s60
	s_add_u32 s58, s64, 0x8000
	s_addc_u32 s59, s65, 0
	s_add_u32 s62, s60, 0x8000
	s_addc_u32 s63, s61, 0
	s_add_i32 s82, 0, 0x10000
	s_add_i32 s83, 0, 0x14000
	v_add_u32_e32 v132, s82, v140
	v_add_u32_e32 v133, s83, v140
	ds_read_b128 v[2:5], v132
	ds_read_b128 v[6:9], v132 offset:1024
	ds_read_b128 v[10:13], v132 offset:2048
	ds_read_b128 v[14:17], v132 offset:3072
	ds_read_b128 v[18:21], v133
	ds_read_b128 v[22:25], v133 offset:1024
	ds_read_b128 v[26:29], v133 offset:2048
	ds_read_b128 v[30:33], v133 offset:3072
	s_add_u32 s80, s54, 0xc000
	s_addc_u32 s81, s55, 0
	s_add_i32 s78, s15, 0xc000
	s_mov_b32 m0, s78
	s_add_i32 s79, s15, 0xe000
	ds_read_b128 v[34:37], v142
	ds_read_b128 v[38:41], v142 offset:1024
	ds_read_b128 v[42:45], v142 offset:2048
	ds_read_b128 v[46:49], v142 offset:3072
	ds_read_b128 v[50:53], v142 offset:4096
	ds_read_b128 v[54:57], v142 offset:5120
	ds_read_b128 v[58:61], v142 offset:6144
	ds_read_b128 v[62:65], v142 offset:7168
	s_nop 0
	global_load_lds_dwordx4 v136, s[80:81]
	s_mov_b32 m0, s79
	s_nop 0
	global_load_lds_dwordx4 v138, s[80:81]
	s_waitcnt vmcnt(8)
	s_waitcnt lgkmcnt(0)
	s_setprio 1
	s_barrier
	v_mfma_f32_16x16x32_bf16 v[86:89], v[10:13], v[50:53], 0
	v_mfma_f32_16x16x32_bf16 v[90:93], v[14:17], v[54:57], v[86:89]
	v_mfma_f32_16x16x32_bf16 v[86:89], v[2:5], v[58:61], 0
	v_mfma_f32_16x16x32_bf16 v[66:69], v[2:5], v[34:37], 0
	v_mfma_f32_16x16x32_bf16 v[70:73], v[10:13], v[34:37], 0
	v_mfma_f32_16x16x32_bf16 v[74:77], v[2:5], v[42:45], 0
	v_mfma_f32_16x16x32_bf16 v[78:81], v[10:13], v[42:45], 0
	v_mfma_f32_16x16x32_bf16 v[82:85], v[2:5], v[50:53], 0
	v_mfma_f32_16x16x32_bf16 v[94:97], v[6:9], v[62:65], v[86:89]
	v_mfma_f32_16x16x32_bf16 v[86:89], v[10:13], v[58:61], 0
	v_mfma_f32_16x16x32_bf16 v[66:69], v[6:9], v[38:41], v[66:69]
	v_mfma_f32_16x16x32_bf16 v[70:73], v[14:17], v[38:41], v[70:73]
	v_mfma_f32_16x16x32_bf16 v[74:77], v[6:9], v[46:49], v[74:77]
	v_mfma_f32_16x16x32_bf16 v[78:81], v[14:17], v[46:49], v[78:81]
	v_mfma_f32_16x16x32_bf16 v[82:85], v[6:9], v[54:57], v[82:85]
	v_mfma_f32_16x16x32_bf16 v[106:109], v[14:17], v[62:65], v[86:89]
	s_setprio 0
	s_setprio 1
	v_mfma_f32_16x16x32_bf16 v[86:89], v[18:21], v[34:37], 0
	v_mfma_f32_16x16x32_bf16 v[34:37], v[26:29], v[34:37], 0
	v_mfma_f32_16x16x32_bf16 v[110:113], v[22:25], v[38:41], v[86:89]
	v_mfma_f32_16x16x32_bf16 v[34:37], v[30:33], v[38:41], v[34:37]
	v_mfma_f32_16x16x32_bf16 v[38:41], v[18:21], v[42:45], 0
	v_mfma_f32_16x16x32_bf16 v[42:45], v[26:29], v[42:45], 0
	v_mfma_f32_16x16x32_bf16 v[38:41], v[22:25], v[46:49], v[38:41]
	v_mfma_f32_16x16x32_bf16 v[42:45], v[30:33], v[46:49], v[42:45]
	v_mfma_f32_16x16x32_bf16 v[46:49], v[18:21], v[50:53], 0
	v_mfma_f32_16x16x32_bf16 v[50:53], v[26:29], v[50:53], 0
	v_mfma_f32_16x16x32_bf16 v[46:49], v[22:25], v[54:57], v[46:49]
	v_mfma_f32_16x16x32_bf16 v[50:53], v[30:33], v[54:57], v[50:53]
	v_mfma_f32_16x16x32_bf16 v[54:57], v[18:21], v[58:61], 0
	v_mfma_f32_16x16x32_bf16 v[144:147], v[22:25], v[62:65], v[54:57]
	v_mfma_f32_16x16x32_bf16 v[54:57], v[26:29], v[58:61], 0
	v_mfma_f32_16x16x32_bf16 v[58:61], v[30:33], v[62:65], v[54:57]
	s_barrier
	s_setprio 0
	s_add_i32 s80, s82, s14
	s_add_i32 s81, s80, 0x2000
	s_mov_b32 m0, s80
	s_add_u32 s84, s60, 0x4000
	s_nop 0
	ds_read_b128 v[54:57], v142 offset:16384
	ds_read_b128 v[62:65], v142 offset:17408
	ds_read_b128 v[86:89], v142 offset:18432
	ds_read_b128 v[98:101], v142 offset:19456
	ds_read_b128 v[102:105], v142 offset:20480
	ds_read_b128 v[114:117], v142 offset:21504
	ds_read_b128 v[118:121], v142 offset:22528
	ds_read_b128 v[122:125], v142 offset:23552
	s_addc_u32 s85, s61, 0
	global_load_lds_dwordx4 v137, s[60:61]
	s_mov_b32 m0, s81
	s_add_i32 s82, s83, s14
	s_add_i32 s83, s82, 0x2000
	global_load_lds_dwordx4 v139, s[60:61]
	s_mov_b32 m0, s82
	s_nop 0
	global_load_lds_dwordx4 v137, s[84:85]
	s_mov_b32 m0, s83
	s_nop 0
	global_load_lds_dwordx4 v139, s[84:85]
	s_mov_b32 m0, s15
	s_nop 0
	global_load_lds_dwordx4 v136, s[64:65]
	s_mov_b32 m0, s18
	s_nop 0
	global_load_lds_dwordx4 v138, s[64:65]
	s_waitcnt vmcnt(8)
	s_waitcnt lgkmcnt(0)
	s_setprio 1
	s_barrier
	v_mfma_f32_16x16x32_bf16 v[126:129], v[2:5], v[54:57], 0
	v_mfma_f32_16x16x32_bf16 v[148:151], v[6:9], v[62:65], v[126:129]
	v_mfma_f32_16x16x32_bf16 v[126:129], v[10:13], v[54:57], 0
	v_mfma_f32_16x16x32_bf16 v[152:155], v[14:17], v[62:65], v[126:129]
	v_mfma_f32_16x16x32_bf16 v[126:129], v[2:5], v[86:89], 0
	v_mfma_f32_16x16x32_bf16 v[156:159], v[6:9], v[98:101], v[126:129]
	v_mfma_f32_16x16x32_bf16 v[126:129], v[10:13], v[86:89], 0
	v_mfma_f32_16x16x32_bf16 v[160:163], v[14:17], v[98:101], v[126:129]
	v_mfma_f32_16x16x32_bf16 v[126:129], v[2:5], v[102:105], 0
	v_mfma_f32_16x16x32_bf16 v[2:5], v[2:5], v[118:121], 0
	v_mfma_f32_16x16x32_bf16 v[164:167], v[6:9], v[114:117], v[126:129]
	v_mfma_f32_16x16x32_bf16 v[2:5], v[6:9], v[122:125], v[2:5]
	v_mfma_f32_16x16x32_bf16 v[6:9], v[10:13], v[118:121], 0
	v_mfma_f32_16x16x32_bf16 v[126:129], v[10:13], v[102:105], 0
	v_mfma_f32_16x16x32_bf16 v[10:13], v[14:17], v[122:125], v[6:9]
	v_mfma_f32_16x16x32_bf16 v[168:171], v[14:17], v[114:117], v[126:129]
	s_setprio 0
	s_setprio 1
	v_mfma_f32_16x16x32_bf16 v[6:9], v[18:21], v[54:57], 0
	v_mfma_f32_16x16x32_bf16 v[14:17], v[22:25], v[62:65], v[6:9]
	v_mfma_f32_16x16x32_bf16 v[6:9], v[26:29], v[54:57], 0
	v_mfma_f32_16x16x32_bf16 v[172:175], v[30:33], v[62:65], v[6:9]
	v_mfma_f32_16x16x32_bf16 v[6:9], v[18:21], v[86:89], 0
	v_mfma_f32_16x16x32_bf16 v[176:179], v[22:25], v[98:101], v[6:9]
	v_mfma_f32_16x16x32_bf16 v[6:9], v[26:29], v[86:89], 0
	v_mfma_f32_16x16x32_bf16 v[180:183], v[30:33], v[98:101], v[6:9]
	v_mfma_f32_16x16x32_bf16 v[6:9], v[18:21], v[102:105], 0
	v_mfma_f32_16x16x32_bf16 v[184:187], v[22:25], v[114:117], v[6:9]
	v_mfma_f32_16x16x32_bf16 v[6:9], v[26:29], v[102:105], 0
	v_mfma_f32_16x16x32_bf16 v[188:191], v[30:33], v[114:117], v[6:9]
	v_mfma_f32_16x16x32_bf16 v[6:9], v[18:21], v[118:121], 0
	v_mfma_f32_16x16x32_bf16 v[194:197], v[22:25], v[122:125], v[6:9]
	v_mfma_f32_16x16x32_bf16 v[6:9], v[26:29], v[118:121], 0
	v_mfma_f32_16x16x32_bf16 v[198:201], v[30:33], v[122:125], v[6:9]
	s_barrier
	s_setprio 0
	s_add_i32 s84, 0, 0x18000
	s_add_i32 s85, 0, 0x1c000
	v_add_u32_e32 v134, s84, v140
	v_add_u32_e32 v135, s85, v140
	s_nop 0
	ds_read_b128 v[6:9], v134
	ds_read_b128 v[26:29], v134 offset:1024
	ds_read_b128 v[30:33], v134 offset:2048
	ds_read_b128 v[202:205], v134 offset:3072
	ds_read_b128 v[206:209], v135
	ds_read_b128 v[210:213], v135 offset:1024
	ds_read_b128 v[214:217], v135 offset:2048
	ds_read_b128 v[218:221], v135 offset:3072
	s_add_u32 s64, s64, 0x4000
	s_addc_u32 s65, s65, 0
	s_mov_b32 m0, s20
	ds_read_b128 v[18:21], v142 offset:32768
	ds_read_b128 v[22:25], v142 offset:33792
	ds_read_b128 v[222:225], v142 offset:34816
	ds_read_b128 v[226:229], v142 offset:35840
	ds_read_b128 v[232:235], v142 offset:36864
	ds_read_b128 v[236:239], v142 offset:37888
	ds_read_b128 v[240:243], v142 offset:38912
	ds_read_b128 v[244:247], v142 offset:39936
	s_nop 0
	global_load_lds_dwordx4 v136, s[64:65]
	s_mov_b32 m0, s21
	s_nop 0
	global_load_lds_dwordx4 v138, s[64:65]
	s_waitcnt vmcnt(8)
	s_waitcnt lgkmcnt(0)
	s_setprio 1
	s_barrier
	v_mfma_f32_16x16x32_bf16 v[54:57], v[6:9], v[18:21], v[66:69]
	v_mfma_f32_16x16x32_bf16 v[118:121], v[26:29], v[22:25], v[54:57]
	v_mfma_f32_16x16x32_bf16 v[54:57], v[30:33], v[18:21], v[70:73]
	v_mfma_f32_16x16x32_bf16 v[114:117], v[202:205], v[22:25], v[54:57]
	v_mfma_f32_16x16x32_bf16 v[54:57], v[6:9], v[222:225], v[74:77]
	v_mfma_f32_16x16x32_bf16 v[102:105], v[26:29], v[226:229], v[54:57]
	v_mfma_f32_16x16x32_bf16 v[54:57], v[30:33], v[222:225], v[78:81]
	v_mfma_f32_16x16x32_bf16 v[98:101], v[202:205], v[226:229], v[54:57]
	v_mfma_f32_16x16x32_bf16 v[54:57], v[6:9], v[232:235], v[82:85]
	v_mfma_f32_16x16x32_bf16 v[86:89], v[26:29], v[236:239], v[54:57]
	v_mfma_f32_16x16x32_bf16 v[54:57], v[30:33], v[232:235], v[90:93]
	v_mfma_f32_16x16x32_bf16 v[82:85], v[202:205], v[236:239], v[54:57]
	v_mfma_f32_16x16x32_bf16 v[54:57], v[6:9], v[240:243], v[94:97]
	v_mfma_f32_16x16x32_bf16 v[62:65], v[26:29], v[244:247], v[54:57]
	v_mfma_f32_16x16x32_bf16 v[54:57], v[30:33], v[240:243], v[106:109]
	v_mfma_f32_16x16x32_bf16 v[54:57], v[202:205], v[244:247], v[54:57]
	s_setprio 0
	s_setprio 1
	v_mfma_f32_16x16x32_bf16 v[66:69], v[206:209], v[18:21], v[110:113]
	v_mfma_f32_16x16x32_bf16 v[18:21], v[214:217], v[18:21], v[34:37]
	v_mfma_f32_16x16x32_bf16 v[122:125], v[218:221], v[22:25], v[18:21]
	v_mfma_f32_16x16x32_bf16 v[18:21], v[206:209], v[222:225], v[38:41]
	v_mfma_f32_16x16x32_bf16 v[110:113], v[210:213], v[226:229], v[18:21]
	v_mfma_f32_16x16x32_bf16 v[18:21], v[214:217], v[222:225], v[42:45]
	v_mfma_f32_16x16x32_bf16 v[106:109], v[218:221], v[226:229], v[18:21]
	v_mfma_f32_16x16x32_bf16 v[18:21], v[206:209], v[232:235], v[46:49]
	v_mfma_f32_16x16x32_bf16 v[94:97], v[210:213], v[236:239], v[18:21]
	v_mfma_f32_16x16x32_bf16 v[18:21], v[214:217], v[232:235], v[50:53]
	v_mfma_f32_16x16x32_bf16 v[90:93], v[218:221], v[236:239], v[18:21]
	v_mfma_f32_16x16x32_bf16 v[18:21], v[206:209], v[240:243], v[144:147]
	v_mfma_f32_16x16x32_bf16 v[78:81], v[210:213], v[244:247], v[18:21]
	v_mfma_f32_16x16x32_bf16 v[18:21], v[214:217], v[240:243], v[58:61]
	v_mfma_f32_16x16x32_bf16 v[126:129], v[210:213], v[22:25], v[66:69]
	v_mfma_f32_16x16x32_bf16 v[70:73], v[218:221], v[244:247], v[18:21]
	s_barrier
	s_setprio 0
	s_add_i32 s64, s84, s14
	s_add_i32 s65, s64, 0x2000
	s_mov_b32 m0, s64
	s_add_u32 s60, s60, 0xc000
	ds_read_b128 v[42:45], v142 offset:49152
	ds_read_b128 v[46:49], v142 offset:50176
	ds_read_b128 v[144:147], v142 offset:51200
	ds_read_b128 v[222:225], v142 offset:52224
	ds_read_b128 v[226:229], v142 offset:53248
	ds_read_b128 v[232:235], v142 offset:54272
	ds_read_b128 v[236:239], v142 offset:55296
	ds_read_b128 v[240:243], v142 offset:56320
	s_addc_u32 s61, s61, 0
	global_load_lds_dwordx4 v137, s[62:63]
	s_mov_b32 m0, s65
	s_add_i32 s84, s85, s14
	s_add_i32 s85, s84, 0x2000
	global_load_lds_dwordx4 v139, s[62:63]
	s_mov_b32 m0, s84
	s_nop 0
	global_load_lds_dwordx4 v137, s[60:61]
	s_mov_b32 m0, s85
	s_nop 0
	global_load_lds_dwordx4 v139, s[60:61]
	s_mov_b32 m0, s67
	s_nop 0
	global_load_lds_dwordx4 v136, s[58:59]
	s_mov_b32 m0, s68
	s_nop 0
	global_load_lds_dwordx4 v138, s[58:59]
	s_waitcnt vmcnt(8)
	s_waitcnt lgkmcnt(0)
	s_setprio 1
	s_barrier
	v_mfma_f32_16x16x32_bf16 v[18:21], v[6:9], v[42:45], v[148:151]
	v_mfma_f32_16x16x32_bf16 v[58:61], v[26:29], v[46:49], v[18:21]
	v_mfma_f32_16x16x32_bf16 v[18:21], v[30:33], v[42:45], v[152:155]
	v_mfma_f32_16x16x32_bf16 v[50:53], v[202:205], v[46:49], v[18:21]
	v_mfma_f32_16x16x32_bf16 v[18:21], v[6:9], v[144:147], v[156:159]
	v_mfma_f32_16x16x32_bf16 v[38:41], v[26:29], v[222:225], v[18:21]
	v_mfma_f32_16x16x32_bf16 v[18:21], v[30:33], v[144:147], v[160:163]
	v_mfma_f32_16x16x32_bf16 v[34:37], v[202:205], v[222:225], v[18:21]
	v_mfma_f32_16x16x32_bf16 v[18:21], v[6:9], v[226:229], v[164:167]
	v_mfma_f32_16x16x32_bf16 v[2:5], v[6:9], v[236:239], v[2:5]
	v_mfma_f32_16x16x32_bf16 v[22:25], v[26:29], v[232:235], v[18:21]
	v_mfma_f32_16x16x32_bf16 v[18:21], v[30:33], v[226:229], v[168:171]
	v_mfma_f32_16x16x32_bf16 v[6:9], v[26:29], v[240:243], v[2:5]
	v_mfma_f32_16x16x32_bf16 v[2:5], v[30:33], v[236:239], v[10:13]
	v_mfma_f32_16x16x32_bf16 v[18:21], v[202:205], v[232:235], v[18:21]
	v_mfma_f32_16x16x32_bf16 v[2:5], v[202:205], v[240:243], v[2:5]
	s_setprio 0
	s_setprio 1
	v_mfma_f32_16x16x32_bf16 v[10:13], v[206:209], v[42:45], v[14:17]
	v_mfma_f32_16x16x32_bf16 v[74:77], v[210:213], v[46:49], v[10:13]
	v_mfma_f32_16x16x32_bf16 v[10:13], v[214:217], v[42:45], v[172:175]
	v_mfma_f32_16x16x32_bf16 v[66:69], v[218:221], v[46:49], v[10:13]
	v_mfma_f32_16x16x32_bf16 v[10:13], v[206:209], v[144:147], v[176:179]
	v_mfma_f32_16x16x32_bf16 v[46:49], v[210:213], v[222:225], v[10:13]
	v_mfma_f32_16x16x32_bf16 v[10:13], v[214:217], v[144:147], v[180:183]
	v_mfma_f32_16x16x32_bf16 v[42:45], v[218:221], v[222:225], v[10:13]
	v_mfma_f32_16x16x32_bf16 v[10:13], v[206:209], v[226:229], v[184:187]
	v_mfma_f32_16x16x32_bf16 v[30:33], v[210:213], v[232:235], v[10:13]
	v_mfma_f32_16x16x32_bf16 v[10:13], v[214:217], v[226:229], v[188:191]
	v_mfma_f32_16x16x32_bf16 v[26:29], v[218:221], v[232:235], v[10:13]
	v_mfma_f32_16x16x32_bf16 v[10:13], v[206:209], v[236:239], v[194:197]
	v_mfma_f32_16x16x32_bf16 v[14:17], v[210:213], v[240:243], v[10:13]
	v_mfma_f32_16x16x32_bf16 v[10:13], v[214:217], v[236:239], v[198:201]
	v_mfma_f32_16x16x32_bf16 v[10:13], v[218:221], v[240:243], v[10:13]
	s_barrier
	s_setprio 0
	s_andn2_b64 vcc, exec, s[38:39]
	s_cbranch_vccnz .LBB0_1153
	s_lshl_b32 s58, s72, 10
	s_xor_b32 s86, s58, 0x400
	s_add_u32 s87, s56, 0x20000
	s_addc_u32 s88, s57, 0
	v_ashrrev_i32_e32 v131, 31, v130
	s_add_u32 s54, s54, 0x1c000
	v_lshl_add_u64 v[130:131], v[130:131], 3, s[26:27]
	s_addc_u32 s55, s55, 0
	s_mov_b32 s89, 4

.LBB0_1151:
	s_or_b64 exec, exec, s[58:59]
	ds_read_b128 v[144:147], v132
	ds_read_b128 v[148:151], v132 offset:1024
	ds_read_b128 v[152:155], v132 offset:2048
	ds_read_b128 v[156:159], v132 offset:3072
	ds_read_b128 v[160:163], v133
	ds_read_b128 v[164:167], v133 offset:1024
	ds_read_b128 v[168:171], v133 offset:2048
	ds_read_b128 v[172:175], v133 offset:3072
	s_add_u32 s58, s54, 0x4000
	s_addc_u32 s59, s55, 0
	s_and_b64 s[56:57], s[56:57], exec
	s_cselect_b32 s62, s48, s58
	s_cselect_b32 s63, s49, s59
	s_cselect_b32 s59, s51, s88
	s_cselect_b32 s58, s50, s87
	s_add_u32 s56, s62, 0x8000
	s_addc_u32 s57, s63, 0
	s_add_u32 s60, s58, 0x8000
	s_addc_u32 s61, s59, 0
	s_mov_b32 m0, s78
	ds_read_b128 v[176:179], v142
	ds_read_b128 v[180:183], v142 offset:1024
	ds_read_b128 v[184:187], v142 offset:2048
	ds_read_b128 v[188:191], v142 offset:3072
	ds_read_b128 v[194:197], v142 offset:4096
	ds_read_b128 v[198:201], v142 offset:5120
	ds_read_b128 v[202:205], v142 offset:6144
	ds_read_b128 v[206:209], v142 offset:7168
	s_nop 0
	global_load_lds_dwordx4 v136, s[54:55]
	s_mov_b32 m0, s79
	s_nop 0
	global_load_lds_dwordx4 v138, s[54:55]
	s_waitcnt vmcnt(8)
	s_waitcnt lgkmcnt(0)
	s_setprio 1
	s_barrier
	v_mfma_f32_16x16x32_bf16 v[118:121], v[144:147], v[176:179], v[118:121]
	v_mfma_f32_16x16x32_bf16 v[114:117], v[152:155], v[176:179], v[114:117]
	v_mfma_f32_16x16x32_bf16 v[102:105], v[144:147], v[184:187], v[102:105]
	v_mfma_f32_16x16x32_bf16 v[98:101], v[152:155], v[184:187], v[98:101]
	v_mfma_f32_16x16x32_bf16 v[86:89], v[144:147], v[194:197], v[86:89]
	v_mfma_f32_16x16x32_bf16 v[82:85], v[152:155], v[194:197], v[82:85]
	v_mfma_f32_16x16x32_bf16 v[62:65], v[144:147], v[202:205], v[62:65]
	v_mfma_f32_16x16x32_bf16 v[54:57], v[152:155], v[202:205], v[54:57]
	v_mfma_f32_16x16x32_bf16 v[118:121], v[148:151], v[180:183], v[118:121]
	v_mfma_f32_16x16x32_bf16 v[114:117], v[156:159], v[180:183], v[114:117]
	v_mfma_f32_16x16x32_bf16 v[102:105], v[148:151], v[188:191], v[102:105]
	v_mfma_f32_16x16x32_bf16 v[98:101], v[156:159], v[188:191], v[98:101]
	v_mfma_f32_16x16x32_bf16 v[86:89], v[148:151], v[198:201], v[86:89]
	v_mfma_f32_16x16x32_bf16 v[82:85], v[156:159], v[198:201], v[82:85]
	v_mfma_f32_16x16x32_bf16 v[62:65], v[148:151], v[206:209], v[62:65]
	v_mfma_f32_16x16x32_bf16 v[54:57], v[156:159], v[206:209], v[54:57]
	s_setprio 0
	s_setprio 1
	v_mfma_f32_16x16x32_bf16 v[126:129], v[160:163], v[176:179], v[126:129]
	v_mfma_f32_16x16x32_bf16 v[122:125], v[168:171], v[176:179], v[122:125]
	v_mfma_f32_16x16x32_bf16 v[110:113], v[160:163], v[184:187], v[110:113]
	v_mfma_f32_16x16x32_bf16 v[106:109], v[168:171], v[184:187], v[106:109]
	v_mfma_f32_16x16x32_bf16 v[94:97], v[160:163], v[194:197], v[94:97]
	v_mfma_f32_16x16x32_bf16 v[90:93], v[168:171], v[194:197], v[90:93]
	v_mfma_f32_16x16x32_bf16 v[78:81], v[160:163], v[202:205], v[78:81]
	v_mfma_f32_16x16x32_bf16 v[70:73], v[168:171], v[202:205], v[70:73]
	v_mfma_f32_16x16x32_bf16 v[126:129], v[164:167], v[180:183], v[126:129]
	v_mfma_f32_16x16x32_bf16 v[122:125], v[172:175], v[180:183], v[122:125]
	v_mfma_f32_16x16x32_bf16 v[110:113], v[164:167], v[188:191], v[110:113]
	v_mfma_f32_16x16x32_bf16 v[106:109], v[172:175], v[188:191], v[106:109]
	v_mfma_f32_16x16x32_bf16 v[94:97], v[164:167], v[198:201], v[94:97]
	v_mfma_f32_16x16x32_bf16 v[90:93], v[172:175], v[198:201], v[90:93]
	v_mfma_f32_16x16x32_bf16 v[78:81], v[164:167], v[206:209], v[78:81]
	v_mfma_f32_16x16x32_bf16 v[70:73], v[172:175], v[206:209], v[70:73]
	s_barrier
	s_setprio 0
	s_mov_b32 m0, s80
	ds_read_b128 v[176:179], v142 offset:16384
	ds_read_b128 v[180:183], v142 offset:17408
	ds_read_b128 v[184:187], v142 offset:18432
	ds_read_b128 v[188:191], v142 offset:19456
	ds_read_b128 v[194:197], v142 offset:20480
	ds_read_b128 v[198:201], v142 offset:21504
	ds_read_b128 v[202:205], v142 offset:22528
	ds_read_b128 v[206:209], v142 offset:23552
	s_add_u32 s90, s58, 0x4000
	global_load_lds_dwordx4 v137, s[58:59]
	s_mov_b32 m0, s81
	s_addc_u32 s91, s59, 0
	global_load_lds_dwordx4 v139, s[58:59]
	s_mov_b32 m0, s82
	s_nop 0
	global_load_lds_dwordx4 v137, s[90:91]
	s_mov_b32 m0, s83
	s_nop 0
	global_load_lds_dwordx4 v139, s[90:91]
	s_mov_b32 m0, s15
	s_nop 0
	global_load_lds_dwordx4 v136, s[62:63]
	s_mov_b32 m0, s18
	s_nop 0
	global_load_lds_dwordx4 v138, s[62:63]
	s_waitcnt vmcnt(8)
	s_waitcnt lgkmcnt(0)
	s_setprio 1
	s_barrier
	v_mfma_f32_16x16x32_bf16 v[58:61], v[144:147], v[176:179], v[58:61]
	v_mfma_f32_16x16x32_bf16 v[50:53], v[152:155], v[176:179], v[50:53]
	v_mfma_f32_16x16x32_bf16 v[38:41], v[144:147], v[184:187], v[38:41]
	v_mfma_f32_16x16x32_bf16 v[34:37], v[152:155], v[184:187], v[34:37]
	v_mfma_f32_16x16x32_bf16 v[22:25], v[144:147], v[194:197], v[22:25]
	v_mfma_f32_16x16x32_bf16 v[18:21], v[152:155], v[194:197], v[18:21]
	v_mfma_f32_16x16x32_bf16 v[6:9], v[144:147], v[202:205], v[6:9]
	v_mfma_f32_16x16x32_bf16 v[2:5], v[152:155], v[202:205], v[2:5]
	v_mfma_f32_16x16x32_bf16 v[58:61], v[148:151], v[180:183], v[58:61]
	v_mfma_f32_16x16x32_bf16 v[50:53], v[156:159], v[180:183], v[50:53]
	v_mfma_f32_16x16x32_bf16 v[38:41], v[148:151], v[188:191], v[38:41]
	v_mfma_f32_16x16x32_bf16 v[34:37], v[156:159], v[188:191], v[34:37]
	v_mfma_f32_16x16x32_bf16 v[22:25], v[148:151], v[198:201], v[22:25]
	v_mfma_f32_16x16x32_bf16 v[18:21], v[156:159], v[198:201], v[18:21]
	v_mfma_f32_16x16x32_bf16 v[6:9], v[148:151], v[206:209], v[6:9]
	v_mfma_f32_16x16x32_bf16 v[2:5], v[156:159], v[206:209], v[2:5]
	s_setprio 0
	s_setprio 1
	v_mfma_f32_16x16x32_bf16 v[74:77], v[160:163], v[176:179], v[74:77]
	v_mfma_f32_16x16x32_bf16 v[66:69], v[168:171], v[176:179], v[66:69]
	v_mfma_f32_16x16x32_bf16 v[46:49], v[160:163], v[184:187], v[46:49]
	v_mfma_f32_16x16x32_bf16 v[42:45], v[168:171], v[184:187], v[42:45]
	v_mfma_f32_16x16x32_bf16 v[30:33], v[160:163], v[194:197], v[30:33]
	v_mfma_f32_16x16x32_bf16 v[26:29], v[168:171], v[194:197], v[26:29]
	v_mfma_f32_16x16x32_bf16 v[14:17], v[160:163], v[202:205], v[14:17]
	v_mfma_f32_16x16x32_bf16 v[10:13], v[168:171], v[202:205], v[10:13]
	v_mfma_f32_16x16x32_bf16 v[74:77], v[164:167], v[180:183], v[74:77]
	v_mfma_f32_16x16x32_bf16 v[66:69], v[172:175], v[180:183], v[66:69]
	v_mfma_f32_16x16x32_bf16 v[46:49], v[164:167], v[188:191], v[46:49]
	v_mfma_f32_16x16x32_bf16 v[42:45], v[172:175], v[188:191], v[42:45]
	v_mfma_f32_16x16x32_bf16 v[30:33], v[164:167], v[198:201], v[30:33]
	v_mfma_f32_16x16x32_bf16 v[26:29], v[172:175], v[198:201], v[26:29]
	v_mfma_f32_16x16x32_bf16 v[14:17], v[164:167], v[206:209], v[14:17]
	v_mfma_f32_16x16x32_bf16 v[10:13], v[172:175], v[206:209], v[10:13]
	s_barrier
	s_setprio 0
	ds_read_b128 v[144:147], v134
	ds_read_b128 v[148:151], v134 offset:1024
	ds_read_b128 v[152:155], v134 offset:2048
	ds_read_b128 v[156:159], v134 offset:3072
	ds_read_b128 v[160:163], v135
	ds_read_b128 v[164:167], v135 offset:1024
	ds_read_b128 v[168:171], v135 offset:2048
	ds_read_b128 v[172:175], v135 offset:3072
	s_add_u32 s62, s62, 0x4000
	s_addc_u32 s63, s63, 0
	s_mov_b32 m0, s20
	ds_read_b128 v[176:179], v142 offset:32768
	ds_read_b128 v[180:183], v142 offset:33792
	ds_read_b128 v[184:187], v142 offset:34816
	ds_read_b128 v[188:191], v142 offset:35840
	ds_read_b128 v[194:197], v142 offset:36864
	ds_read_b128 v[198:201], v142 offset:37888
	ds_read_b128 v[202:205], v142 offset:38912
	ds_read_b128 v[206:209], v142 offset:39936
	s_nop 0
	global_load_lds_dwordx4 v136, s[62:63]
	s_mov_b32 m0, s21
	s_nop 0
	global_load_lds_dwordx4 v138, s[62:63]
	s_waitcnt vmcnt(8)
	s_waitcnt lgkmcnt(0)
	s_setprio 1
	s_barrier
	v_mfma_f32_16x16x32_bf16 v[118:121], v[144:147], v[176:179], v[118:121]
	v_mfma_f32_16x16x32_bf16 v[114:117], v[152:155], v[176:179], v[114:117]
	v_mfma_f32_16x16x32_bf16 v[102:105], v[144:147], v[184:187], v[102:105]
	v_mfma_f32_16x16x32_bf16 v[98:101], v[152:155], v[184:187], v[98:101]
	v_mfma_f32_16x16x32_bf16 v[86:89], v[144:147], v[194:197], v[86:89]
	v_mfma_f32_16x16x32_bf16 v[82:85], v[152:155], v[194:197], v[82:85]
	v_mfma_f32_16x16x32_bf16 v[62:65], v[144:147], v[202:205], v[62:65]
	v_mfma_f32_16x16x32_bf16 v[54:57], v[152:155], v[202:205], v[54:57]
	v_mfma_f32_16x16x32_bf16 v[118:121], v[148:151], v[180:183], v[118:121]
	v_mfma_f32_16x16x32_bf16 v[114:117], v[156:159], v[180:183], v[114:117]
	v_mfma_f32_16x16x32_bf16 v[102:105], v[148:151], v[188:191], v[102:105]
	v_mfma_f32_16x16x32_bf16 v[98:101], v[156:159], v[188:191], v[98:101]
	v_mfma_f32_16x16x32_bf16 v[86:89], v[148:151], v[198:201], v[86:89]
	v_mfma_f32_16x16x32_bf16 v[82:85], v[156:159], v[198:201], v[82:85]
	v_mfma_f32_16x16x32_bf16 v[62:65], v[148:151], v[206:209], v[62:65]
	v_mfma_f32_16x16x32_bf16 v[54:57], v[156:159], v[206:209], v[54:57]
	s_setprio 0
	s_setprio 1
	v_mfma_f32_16x16x32_bf16 v[126:129], v[160:163], v[176:179], v[126:129]
	v_mfma_f32_16x16x32_bf16 v[122:125], v[168:171], v[176:179], v[122:125]
	v_mfma_f32_16x16x32_bf16 v[110:113], v[160:163], v[184:187], v[110:113]
	v_mfma_f32_16x16x32_bf16 v[106:109], v[168:171], v[184:187], v[106:109]
	v_mfma_f32_16x16x32_bf16 v[94:97], v[160:163], v[194:197], v[94:97]
	v_mfma_f32_16x16x32_bf16 v[90:93], v[168:171], v[194:197], v[90:93]
	v_mfma_f32_16x16x32_bf16 v[78:81], v[160:163], v[202:205], v[78:81]
	v_mfma_f32_16x16x32_bf16 v[70:73], v[168:171], v[202:205], v[70:73]
	v_mfma_f32_16x16x32_bf16 v[126:129], v[164:167], v[180:183], v[126:129]
	v_mfma_f32_16x16x32_bf16 v[122:125], v[172:175], v[180:183], v[122:125]
	v_mfma_f32_16x16x32_bf16 v[110:113], v[164:167], v[188:191], v[110:113]
	v_mfma_f32_16x16x32_bf16 v[106:109], v[172:175], v[188:191], v[106:109]
	v_mfma_f32_16x16x32_bf16 v[94:97], v[164:167], v[198:201], v[94:97]
	v_mfma_f32_16x16x32_bf16 v[90:93], v[172:175], v[198:201], v[90:93]
	v_mfma_f32_16x16x32_bf16 v[78:81], v[164:167], v[206:209], v[78:81]
	v_mfma_f32_16x16x32_bf16 v[70:73], v[172:175], v[206:209], v[70:73]
	s_barrier
	s_setprio 0
	s_mov_b32 m0, s64
	ds_read_b128 v[176:179], v142 offset:49152
	ds_read_b128 v[180:183], v142 offset:50176
	ds_read_b128 v[184:187], v142 offset:51200
	ds_read_b128 v[188:191], v142 offset:52224
	ds_read_b128 v[194:197], v142 offset:53248
	ds_read_b128 v[198:201], v142 offset:54272
	ds_read_b128 v[202:205], v142 offset:55296
	ds_read_b128 v[206:209], v142 offset:56320
	s_add_u32 s58, s58, 0xc000
	global_load_lds_dwordx4 v137, s[60:61]
	s_mov_b32 m0, s65
	s_addc_u32 s59, s59, 0
	global_load_lds_dwordx4 v139, s[60:61]
	s_mov_b32 m0, s84
	s_nop 0
	global_load_lds_dwordx4 v137, s[58:59]
	s_mov_b32 m0, s85
	s_nop 0
	global_load_lds_dwordx4 v139, s[58:59]
	s_mov_b32 m0, s67
	s_nop 0
	global_load_lds_dwordx4 v136, s[56:57]
	s_mov_b32 m0, s68
	s_nop 0
	global_load_lds_dwordx4 v138, s[56:57]
	s_waitcnt vmcnt(8)
	s_waitcnt lgkmcnt(0)
	s_setprio 1
	s_barrier
	v_mfma_f32_16x16x32_bf16 v[58:61], v[144:147], v[176:179], v[58:61]
	v_mfma_f32_16x16x32_bf16 v[50:53], v[152:155], v[176:179], v[50:53]
	v_mfma_f32_16x16x32_bf16 v[38:41], v[144:147], v[184:187], v[38:41]
	v_mfma_f32_16x16x32_bf16 v[34:37], v[152:155], v[184:187], v[34:37]
	v_mfma_f32_16x16x32_bf16 v[22:25], v[144:147], v[194:197], v[22:25]
	v_mfma_f32_16x16x32_bf16 v[18:21], v[152:155], v[194:197], v[18:21]
	v_mfma_f32_16x16x32_bf16 v[6:9], v[144:147], v[202:205], v[6:9]
	v_mfma_f32_16x16x32_bf16 v[2:5], v[152:155], v[202:205], v[2:5]
	v_mfma_f32_16x16x32_bf16 v[58:61], v[148:151], v[180:183], v[58:61]
	v_mfma_f32_16x16x32_bf16 v[50:53], v[156:159], v[180:183], v[50:53]
	v_mfma_f32_16x16x32_bf16 v[38:41], v[148:151], v[188:191], v[38:41]
	v_mfma_f32_16x16x32_bf16 v[34:37], v[156:159], v[188:191], v[34:37]
	v_mfma_f32_16x16x32_bf16 v[22:25], v[148:151], v[198:201], v[22:25]
	v_mfma_f32_16x16x32_bf16 v[18:21], v[156:159], v[198:201], v[18:21]
	v_mfma_f32_16x16x32_bf16 v[6:9], v[148:151], v[206:209], v[6:9]
	v_mfma_f32_16x16x32_bf16 v[2:5], v[156:159], v[206:209], v[2:5]
	s_setprio 0
	s_setprio 1
	v_mfma_f32_16x16x32_bf16 v[74:77], v[160:163], v[176:179], v[74:77]
	v_mfma_f32_16x16x32_bf16 v[66:69], v[168:171], v[176:179], v[66:69]
	v_mfma_f32_16x16x32_bf16 v[46:49], v[160:163], v[184:187], v[46:49]
	v_mfma_f32_16x16x32_bf16 v[42:45], v[168:171], v[184:187], v[42:45]
	v_mfma_f32_16x16x32_bf16 v[30:33], v[160:163], v[194:197], v[30:33]
	v_mfma_f32_16x16x32_bf16 v[26:29], v[168:171], v[194:197], v[26:29]
	v_mfma_f32_16x16x32_bf16 v[14:17], v[160:163], v[202:205], v[14:17]
	v_mfma_f32_16x16x32_bf16 v[10:13], v[168:171], v[202:205], v[10:13]
	v_mfma_f32_16x16x32_bf16 v[74:77], v[164:167], v[180:183], v[74:77]
	v_mfma_f32_16x16x32_bf16 v[66:69], v[172:175], v[180:183], v[66:69]
	v_mfma_f32_16x16x32_bf16 v[46:49], v[164:167], v[188:191], v[46:49]
	v_mfma_f32_16x16x32_bf16 v[42:45], v[172:175], v[188:191], v[42:45]
	v_mfma_f32_16x16x32_bf16 v[30:33], v[164:167], v[198:201], v[30:33]
	v_mfma_f32_16x16x32_bf16 v[26:29], v[172:175], v[198:201], v[26:29]
	v_mfma_f32_16x16x32_bf16 v[14:17], v[164:167], v[206:209], v[14:17]
	v_mfma_f32_16x16x32_bf16 v[10:13], v[172:175], v[206:209], v[10:13]
	s_barrier
	s_setprio 0
	s_add_i32 s56, s89, 2
	s_add_u32 s87, s87, 0x10000
	s_addc_u32 s88, s88, 0
	s_add_u32 s54, s54, 0x10000
	s_addc_u32 s55, s55, 0
	s_cmp_lt_i32 s89, s25
	s_cbranch_scc0 .LBB0_1153
	s_mov_b32 s89, s56
	s_branch .LBB0_1149

.LBB0_1225:
	s_add_u32 s34, s26, 0x10000
	s_addc_u32 s35, s27, 0
	s_and_b64 s[30:31], s[46:47], exec
	s_cselect_b32 s53, s39, s35
	s_cselect_b32 s52, s38, s34
	s_add_u32 s65, s28, 0x10000
	s_addc_u32 s66, s29, 0
	s_add_u32 s30, s52, 0x8000
	s_addc_u32 s31, s53, 0
	s_add_i32 s67, 0, 0x10000
	s_and_b64 s[34:35], s[46:47], exec
	s_cselect_b32 s35, s41, s66
	s_cselect_b32 s34, s40, s65
	s_add_i32 s70, 0, 0x14000
	v_add_u32_e32 v114, s67, v236
	v_add_u32_e32 v115, s70, v236
	ds_read_b128 v[2:5], v114
	s_waitcnt lgkmcnt(0)
	ds_read_b128 v[6:9], v114 offset:1024
	ds_read_b128 v[10:13], v114 offset:2048
	ds_read_b128 v[14:17], v114 offset:3072
	ds_read_b128 v[18:21], v115
	ds_read_b128 v[22:25], v115 offset:1024
	ds_read_b128 v[26:29], v115 offset:2048
	ds_read_b128 v[30:33], v115 offset:3072
	s_add_u32 s68, s26, 0xc000
	s_addc_u32 s69, s27, 0
	s_add_i32 s65, s20, 0xc000
	s_mov_b32 m0, s65
	s_add_i32 s66, s20, 0xe000
	ds_read_b128 v[34:37], v237
	ds_read_b128 v[38:41], v237 offset:1024
	ds_read_b128 v[42:45], v237 offset:2048
	ds_read_b128 v[46:49], v237 offset:3072
	ds_read_b128 v[50:53], v237 offset:4096
	ds_read_b128 v[54:57], v237 offset:5120
	ds_read_b128 v[58:61], v237 offset:6144
	ds_read_b128 v[62:65], v237 offset:7168
	s_nop 0
	global_load_lds_dwordx4 v235, s[68:69]
	s_mov_b32 m0, s66
	s_nop 0
	global_load_lds_dwordx4 v226, s[68:69]
	s_waitcnt vmcnt(8)
	s_waitcnt lgkmcnt(0)
	s_setprio 1
	s_barrier
	v_mfma_f32_16x16x32_bf16 v[90:93], v[2:5], v[58:61], 0
	v_mfma_f32_16x16x32_bf16 v[66:69], v[2:5], v[34:37], 0
	v_mfma_f32_16x16x32_bf16 v[70:73], v[10:13], v[34:37], 0
	v_mfma_f32_16x16x32_bf16 v[74:77], v[2:5], v[42:45], 0
	v_mfma_f32_16x16x32_bf16 v[78:81], v[10:13], v[42:45], 0
	v_mfma_f32_16x16x32_bf16 v[82:85], v[2:5], v[50:53], 0
	v_mfma_f32_16x16x32_bf16 v[86:89], v[10:13], v[50:53], 0
	v_mfma_f32_16x16x32_bf16 v[98:101], v[6:9], v[62:65], v[90:93]
	v_mfma_f32_16x16x32_bf16 v[90:93], v[10:13], v[58:61], 0
	v_mfma_f32_16x16x32_bf16 v[66:69], v[6:9], v[38:41], v[66:69]
	v_mfma_f32_16x16x32_bf16 v[70:73], v[14:17], v[38:41], v[70:73]
	v_mfma_f32_16x16x32_bf16 v[74:77], v[6:9], v[46:49], v[74:77]
	v_mfma_f32_16x16x32_bf16 v[78:81], v[14:17], v[46:49], v[78:81]
	v_mfma_f32_16x16x32_bf16 v[82:85], v[6:9], v[54:57], v[82:85]
	v_mfma_f32_16x16x32_bf16 v[86:89], v[14:17], v[54:57], v[86:89]
	v_mfma_f32_16x16x32_bf16 v[102:105], v[14:17], v[62:65], v[90:93]
	s_setprio 0
	s_setprio 1
	v_mfma_f32_16x16x32_bf16 v[90:93], v[18:21], v[34:37], 0
	v_mfma_f32_16x16x32_bf16 v[34:37], v[26:29], v[34:37], 0
	v_mfma_f32_16x16x32_bf16 v[118:121], v[22:25], v[38:41], v[90:93]
	v_mfma_f32_16x16x32_bf16 v[34:37], v[30:33], v[38:41], v[34:37]
	v_mfma_f32_16x16x32_bf16 v[38:41], v[18:21], v[42:45], 0
	v_mfma_f32_16x16x32_bf16 v[42:45], v[26:29], v[42:45], 0
	v_mfma_f32_16x16x32_bf16 v[38:41], v[22:25], v[46:49], v[38:41]
	v_mfma_f32_16x16x32_bf16 v[42:45], v[30:33], v[46:49], v[42:45]
	v_mfma_f32_16x16x32_bf16 v[46:49], v[18:21], v[50:53], 0
	v_mfma_f32_16x16x32_bf16 v[50:53], v[26:29], v[50:53], 0
	v_mfma_f32_16x16x32_bf16 v[46:49], v[22:25], v[54:57], v[46:49]
	v_mfma_f32_16x16x32_bf16 v[50:53], v[30:33], v[54:57], v[50:53]
	v_mfma_f32_16x16x32_bf16 v[54:57], v[18:21], v[58:61], 0
	v_mfma_f32_16x16x32_bf16 v[58:61], v[26:29], v[58:61], 0
	v_mfma_f32_16x16x32_bf16 v[54:57], v[22:25], v[62:65], v[54:57]
	v_mfma_f32_16x16x32_bf16 v[58:61], v[30:33], v[62:65], v[58:61]
	s_barrier
	s_setprio 0
	s_add_i32 s67, s67, s18
	s_add_i32 s68, s67, 0x2000
	s_mov_b32 m0, s67
	s_add_u32 s72, s34, 0x4000
	ds_read_b128 v[62:65], v237 offset:16384
	ds_read_b128 v[90:93], v237 offset:17408
	ds_read_b128 v[94:97], v237 offset:18432
	ds_read_b128 v[106:109], v237 offset:19456
	ds_read_b128 v[110:113], v237 offset:20480
	ds_read_b128 v[122:125], v237 offset:21504
	ds_read_b128 v[126:129], v237 offset:22528
	ds_read_b128 v[130:133], v237 offset:23552
	s_addc_u32 s73, s35, 0
	global_load_lds_dwordx4 v227, s[34:35]
	s_mov_b32 m0, s68
	s_add_i32 s69, s70, s18
	s_add_i32 s70, s69, 0x2000
	global_load_lds_dwordx4 v0, s[34:35]
	s_mov_b32 m0, s69
	s_nop 0
	global_load_lds_dwordx4 v227, s[72:73]
	s_mov_b32 m0, s70
	s_nop 0
	global_load_lds_dwordx4 v0, s[72:73]
	s_mov_b32 m0, s20
	s_nop 0
	global_load_lds_dwordx4 v235, s[52:53]
	s_mov_b32 m0, s25
	s_nop 0
	global_load_lds_dwordx4 v226, s[52:53]
	s_waitcnt vmcnt(8)
	s_waitcnt lgkmcnt(0)
	s_setprio 1
	s_barrier
	v_mfma_f32_16x16x32_bf16 v[134:137], v[2:5], v[62:65], 0
	v_mfma_f32_16x16x32_bf16 v[142:145], v[2:5], v[94:97], 0
	v_mfma_f32_16x16x32_bf16 v[150:153], v[2:5], v[110:113], 0
	v_mfma_f32_16x16x32_bf16 v[2:5], v[2:5], v[126:129], 0
	v_mfma_f32_16x16x32_bf16 v[134:137], v[6:9], v[90:93], v[134:137]
	v_mfma_f32_16x16x32_bf16 v[142:145], v[6:9], v[106:109], v[142:145]
	v_mfma_f32_16x16x32_bf16 v[150:153], v[6:9], v[122:125], v[150:153]
	v_mfma_f32_16x16x32_bf16 v[2:5], v[6:9], v[130:133], v[2:5]
	v_mfma_f32_16x16x32_bf16 v[6:9], v[10:13], v[126:129], 0
	v_mfma_f32_16x16x32_bf16 v[138:141], v[10:13], v[62:65], 0
	v_mfma_f32_16x16x32_bf16 v[146:149], v[10:13], v[94:97], 0
	v_mfma_f32_16x16x32_bf16 v[154:157], v[10:13], v[110:113], 0
	v_mfma_f32_16x16x32_bf16 v[6:9], v[14:17], v[130:133], v[6:9]
	v_mfma_f32_16x16x32_bf16 v[138:141], v[14:17], v[90:93], v[138:141]
	v_mfma_f32_16x16x32_bf16 v[146:149], v[14:17], v[106:109], v[146:149]
	v_mfma_f32_16x16x32_bf16 v[154:157], v[14:17], v[122:125], v[154:157]
	s_setprio 0
	s_setprio 1
	v_mfma_f32_16x16x32_bf16 v[10:13], v[18:21], v[62:65], 0
	v_mfma_f32_16x16x32_bf16 v[158:161], v[22:25], v[90:93], v[10:13]
	v_mfma_f32_16x16x32_bf16 v[10:13], v[26:29], v[62:65], 0
	v_mfma_f32_16x16x32_bf16 v[162:165], v[30:33], v[90:93], v[10:13]
	v_mfma_f32_16x16x32_bf16 v[10:13], v[18:21], v[94:97], 0
	v_mfma_f32_16x16x32_bf16 v[174:177], v[22:25], v[106:109], v[10:13]
	v_mfma_f32_16x16x32_bf16 v[10:13], v[26:29], v[94:97], 0
	v_mfma_f32_16x16x32_bf16 v[178:181], v[30:33], v[106:109], v[10:13]
	v_mfma_f32_16x16x32_bf16 v[10:13], v[18:21], v[110:113], 0
	v_mfma_f32_16x16x32_bf16 v[182:185], v[22:25], v[122:125], v[10:13]
	v_mfma_f32_16x16x32_bf16 v[10:13], v[26:29], v[110:113], 0
	v_mfma_f32_16x16x32_bf16 v[122:125], v[30:33], v[122:125], v[10:13]
	v_mfma_f32_16x16x32_bf16 v[10:13], v[18:21], v[126:129], 0
	v_mfma_f32_16x16x32_bf16 v[186:189], v[22:25], v[130:133], v[10:13]
	v_mfma_f32_16x16x32_bf16 v[10:13], v[26:29], v[126:129], 0
	v_mfma_f32_16x16x32_bf16 v[130:133], v[30:33], v[130:133], v[10:13]
	s_barrier
	s_setprio 0
	s_add_i32 s71, 0, 0x18000
	s_add_i32 s74, 0, 0x1c000
	v_add_u32_e32 v116, s71, v236
	v_add_u32_e32 v117, s74, v236
	s_nop 0
	ds_read_b128 v[10:13], v116
	ds_read_b128 v[14:17], v116 offset:1024
	ds_read_b128 v[18:21], v116 offset:2048
	ds_read_b128 v[22:25], v116 offset:3072
	ds_read_b128 v[194:197], v117
	ds_read_b128 v[198:201], v117 offset:1024
	ds_read_b128 v[202:205], v117 offset:2048
	ds_read_b128 v[206:209], v117 offset:3072
	s_add_u32 s52, s52, 0x4000
	s_addc_u32 s53, s53, 0
	s_mov_b32 m0, s54
	ds_read_b128 v[26:29], v237 offset:32768
	ds_read_b128 v[30:33], v237 offset:33792
	ds_read_b128 v[62:65], v237 offset:34816
	ds_read_b128 v[210:213], v237 offset:35840
	ds_read_b128 v[214:217], v237 offset:36864
	ds_read_b128 v[218:221], v237 offset:37888
	ds_read_b128 v[222:225], v237 offset:38912
	ds_read_b128 v[238:241], v237 offset:39936
	s_nop 0
	global_load_lds_dwordx4 v235, s[52:53]
	s_mov_b32 m0, s55
	s_nop 0
	global_load_lds_dwordx4 v226, s[52:53]
	s_waitcnt vmcnt(8)
	s_waitcnt lgkmcnt(0)
	s_setprio 1
	s_barrier
	v_mfma_f32_16x16x32_bf16 v[66:69], v[10:13], v[26:29], v[66:69]
	v_mfma_f32_16x16x32_bf16 v[166:169], v[14:17], v[30:33], v[66:69]
	v_mfma_f32_16x16x32_bf16 v[66:69], v[18:21], v[26:29], v[70:73]
	v_mfma_f32_16x16x32_bf16 v[170:173], v[22:25], v[30:33], v[66:69]
	v_mfma_f32_16x16x32_bf16 v[66:69], v[10:13], v[62:65], v[74:77]
	v_mfma_f32_16x16x32_bf16 v[110:113], v[14:17], v[210:213], v[66:69]
	v_mfma_f32_16x16x32_bf16 v[66:69], v[18:21], v[62:65], v[78:81]
	v_mfma_f32_16x16x32_bf16 v[106:109], v[22:25], v[210:213], v[66:69]
	v_mfma_f32_16x16x32_bf16 v[66:69], v[10:13], v[214:217], v[82:85]
	v_mfma_f32_16x16x32_bf16 v[94:97], v[14:17], v[218:221], v[66:69]
	v_mfma_f32_16x16x32_bf16 v[66:69], v[18:21], v[214:217], v[86:89]
	v_mfma_f32_16x16x32_bf16 v[90:93], v[22:25], v[218:221], v[66:69]
	v_mfma_f32_16x16x32_bf16 v[66:69], v[10:13], v[222:225], v[98:101]
	v_mfma_f32_16x16x32_bf16 v[78:81], v[14:17], v[238:241], v[66:69]
	v_mfma_f32_16x16x32_bf16 v[66:69], v[18:21], v[222:225], v[102:105]
	v_mfma_f32_16x16x32_bf16 v[70:73], v[22:25], v[238:241], v[66:69]
	s_setprio 0
	s_setprio 1
	v_mfma_f32_16x16x32_bf16 v[66:69], v[194:197], v[26:29], v[118:121]
	v_mfma_f32_16x16x32_bf16 v[26:29], v[202:205], v[26:29], v[34:37]
	v_mfma_f32_16x16x32_bf16 v[118:121], v[206:209], v[30:33], v[26:29]
	v_mfma_f32_16x16x32_bf16 v[26:29], v[194:197], v[62:65], v[38:41]
	v_mfma_f32_16x16x32_bf16 v[102:105], v[198:201], v[210:213], v[26:29]
	v_mfma_f32_16x16x32_bf16 v[26:29], v[202:205], v[62:65], v[42:45]
	v_mfma_f32_16x16x32_bf16 v[98:101], v[206:209], v[210:213], v[26:29]
	v_mfma_f32_16x16x32_bf16 v[26:29], v[194:197], v[214:217], v[46:49]
	v_mfma_f32_16x16x32_bf16 v[86:89], v[198:201], v[218:221], v[26:29]
	v_mfma_f32_16x16x32_bf16 v[26:29], v[202:205], v[214:217], v[50:53]
	v_mfma_f32_16x16x32_bf16 v[82:85], v[206:209], v[218:221], v[26:29]
	v_mfma_f32_16x16x32_bf16 v[26:29], v[194:197], v[222:225], v[54:57]
	v_mfma_f32_16x16x32_bf16 v[62:65], v[198:201], v[238:241], v[26:29]
	v_mfma_f32_16x16x32_bf16 v[26:29], v[202:205], v[222:225], v[58:61]
	v_mfma_f32_16x16x32_bf16 v[126:129], v[198:201], v[30:33], v[66:69]
	v_mfma_f32_16x16x32_bf16 v[54:57], v[206:209], v[238:241], v[26:29]
	s_barrier
	s_setprio 0
	s_add_u32 s72, s34, 0x8000
	s_addc_u32 s73, s35, 0
	s_add_i32 s52, s71, s18
	s_add_i32 s53, s52, 0x2000
	s_mov_b32 m0, s52
	s_add_u32 s34, s34, 0xc000
	ds_read_b128 v[34:37], v237 offset:49152
	ds_read_b128 v[38:41], v237 offset:50176
	ds_read_b128 v[210:213], v237 offset:51200
	ds_read_b128 v[214:217], v237 offset:52224
	ds_read_b128 v[218:221], v237 offset:53248
	ds_read_b128 v[222:225], v237 offset:54272
	ds_read_b128 v[238:241], v237 offset:55296
	ds_read_b128 v[242:245], v237 offset:56320
	s_addc_u32 s35, s35, 0
	global_load_lds_dwordx4 v227, s[72:73]
	s_mov_b32 m0, s53
	s_add_i32 s71, s74, s18
	s_nop 0
	global_load_lds_dwordx4 v0, s[72:73]
	s_mov_b32 m0, s71
	s_add_i32 s72, s71, 0x2000
	s_nop 0
	global_load_lds_dwordx4 v227, s[34:35]
	s_mov_b32 m0, s72
	s_nop 0
	global_load_lds_dwordx4 v0, s[34:35]
	s_mov_b32 m0, s58
	s_nop 0
	global_load_lds_dwordx4 v235, s[30:31]
	s_mov_b32 m0, s59
	s_nop 0
	global_load_lds_dwordx4 v226, s[30:31]
	s_waitcnt vmcnt(8)
	s_waitcnt lgkmcnt(0)
	s_setprio 1
	s_barrier
	v_mfma_f32_16x16x32_bf16 v[26:29], v[10:13], v[34:37], v[134:137]
	v_mfma_f32_16x16x32_bf16 v[74:77], v[14:17], v[38:41], v[26:29]
	v_mfma_f32_16x16x32_bf16 v[26:29], v[18:21], v[34:37], v[138:141]
	v_mfma_f32_16x16x32_bf16 v[66:69], v[22:25], v[38:41], v[26:29]
	v_mfma_f32_16x16x32_bf16 v[26:29], v[10:13], v[210:213], v[142:145]
	v_mfma_f32_16x16x32_bf16 v[46:49], v[14:17], v[214:217], v[26:29]
	v_mfma_f32_16x16x32_bf16 v[26:29], v[18:21], v[210:213], v[146:149]
	v_mfma_f32_16x16x32_bf16 v[42:45], v[22:25], v[214:217], v[26:29]
	v_mfma_f32_16x16x32_bf16 v[26:29], v[10:13], v[218:221], v[150:153]
	v_mfma_f32_16x16x32_bf16 v[2:5], v[10:13], v[238:241], v[2:5]
	v_mfma_f32_16x16x32_bf16 v[30:33], v[14:17], v[222:225], v[26:29]
	v_mfma_f32_16x16x32_bf16 v[26:29], v[18:21], v[218:221], v[154:157]
	v_mfma_f32_16x16x32_bf16 v[14:17], v[14:17], v[242:245], v[2:5]
	v_mfma_f32_16x16x32_bf16 v[2:5], v[18:21], v[238:241], v[6:9]
	v_mfma_f32_16x16x32_bf16 v[26:29], v[22:25], v[222:225], v[26:29]
	v_mfma_f32_16x16x32_bf16 v[10:13], v[22:25], v[242:245], v[2:5]
	s_setprio 0
	s_setprio 1
	v_mfma_f32_16x16x32_bf16 v[2:5], v[194:197], v[34:37], v[158:161]
	v_mfma_f32_16x16x32_bf16 v[58:61], v[198:201], v[38:41], v[2:5]
	v_mfma_f32_16x16x32_bf16 v[2:5], v[202:205], v[34:37], v[162:165]
	v_mfma_f32_16x16x32_bf16 v[50:53], v[206:209], v[38:41], v[2:5]
	v_mfma_f32_16x16x32_bf16 v[2:5], v[194:197], v[210:213], v[174:177]
	v_mfma_f32_16x16x32_bf16 v[38:41], v[198:201], v[214:217], v[2:5]
	v_mfma_f32_16x16x32_bf16 v[2:5], v[202:205], v[210:213], v[178:181]
	v_mfma_f32_16x16x32_bf16 v[34:37], v[206:209], v[214:217], v[2:5]
	v_mfma_f32_16x16x32_bf16 v[2:5], v[194:197], v[218:221], v[182:185]
	v_mfma_f32_16x16x32_bf16 v[22:25], v[198:201], v[222:225], v[2:5]
	v_mfma_f32_16x16x32_bf16 v[2:5], v[202:205], v[218:221], v[122:125]
	v_mfma_f32_16x16x32_bf16 v[18:21], v[206:209], v[222:225], v[2:5]
	v_mfma_f32_16x16x32_bf16 v[2:5], v[194:197], v[238:241], v[186:189]
	v_mfma_f32_16x16x32_bf16 v[6:9], v[198:201], v[242:245], v[2:5]
	v_mfma_f32_16x16x32_bf16 v[2:5], v[202:205], v[238:241], v[130:133]
	v_mfma_f32_16x16x32_bf16 v[2:5], v[206:209], v[242:245], v[2:5]
	s_barrier
	s_setprio 0
	s_andn2_b64 vcc, exec, s[48:49]
	s_cbranch_vccnz .LBB0_1228
	s_add_u32 s73, s28, 0x20000
	s_addc_u32 s74, s29, 0
	s_add_u32 s26, s26, 0x1c000
	s_addc_u32 s27, s27, 0
	s_mov_b32 s75, 4
.LBB0_1227:
	ds_read_b128 v[122:125], v114
	ds_read_b128 v[130:133], v114 offset:1024
	ds_read_b128 v[134:137], v114 offset:2048
	ds_read_b128 v[138:141], v114 offset:3072
	ds_read_b128 v[142:145], v115
	ds_read_b128 v[146:149], v115 offset:1024
	ds_read_b128 v[150:153], v115 offset:2048
	ds_read_b128 v[154:157], v115 offset:3072
	s_add_u32 s28, s26, 0x4000
	s_addc_u32 s29, s27, 0
	s_cmp_eq_u32 s56, s75
	s_cselect_b32 s34, s38, s28
	s_cselect_b32 s35, s39, s29
	s_cselect_b32 s30, s40, s73
	s_cselect_b32 s31, s41, s74
	s_add_u32 s28, s34, 0x8000
	s_addc_u32 s29, s35, 0
	s_mov_b32 m0, s65
	ds_read_b128 v[158:161], v237
	ds_read_b128 v[162:165], v237 offset:1024
	ds_read_b128 v[174:177], v237 offset:2048
	ds_read_b128 v[178:181], v237 offset:3072
	ds_read_b128 v[182:185], v237 offset:4096
	ds_read_b128 v[186:189], v237 offset:5120
	ds_read_b128 v[194:197], v237 offset:6144
	ds_read_b128 v[198:201], v237 offset:7168
	s_nop 0
	global_load_lds_dwordx4 v235, s[26:27]
	s_mov_b32 m0, s66
	s_nop 0
	global_load_lds_dwordx4 v226, s[26:27]
	s_waitcnt vmcnt(8)
	s_waitcnt lgkmcnt(0)
	s_setprio 1
	s_barrier
	v_mfma_f32_16x16x32_bf16 v[166:169], v[122:125], v[158:161], v[166:169]
	v_mfma_f32_16x16x32_bf16 v[170:173], v[134:137], v[158:161], v[170:173]
	v_mfma_f32_16x16x32_bf16 v[110:113], v[122:125], v[174:177], v[110:113]
	v_mfma_f32_16x16x32_bf16 v[106:109], v[134:137], v[174:177], v[106:109]
	v_mfma_f32_16x16x32_bf16 v[94:97], v[122:125], v[182:185], v[94:97]
	v_mfma_f32_16x16x32_bf16 v[90:93], v[134:137], v[182:185], v[90:93]
	v_mfma_f32_16x16x32_bf16 v[78:81], v[122:125], v[194:197], v[78:81]
	v_mfma_f32_16x16x32_bf16 v[70:73], v[134:137], v[194:197], v[70:73]
	v_mfma_f32_16x16x32_bf16 v[166:169], v[130:133], v[162:165], v[166:169]
	v_mfma_f32_16x16x32_bf16 v[170:173], v[138:141], v[162:165], v[170:173]
	v_mfma_f32_16x16x32_bf16 v[110:113], v[130:133], v[178:181], v[110:113]
	v_mfma_f32_16x16x32_bf16 v[106:109], v[138:141], v[178:181], v[106:109]
	v_mfma_f32_16x16x32_bf16 v[94:97], v[130:133], v[186:189], v[94:97]
	v_mfma_f32_16x16x32_bf16 v[90:93], v[138:141], v[186:189], v[90:93]
	v_mfma_f32_16x16x32_bf16 v[78:81], v[130:133], v[198:201], v[78:81]
	v_mfma_f32_16x16x32_bf16 v[70:73], v[138:141], v[198:201], v[70:73]
	s_setprio 0
	s_setprio 1
	v_mfma_f32_16x16x32_bf16 v[126:129], v[142:145], v[158:161], v[126:129]
	v_mfma_f32_16x16x32_bf16 v[118:121], v[150:153], v[158:161], v[118:121]
	v_mfma_f32_16x16x32_bf16 v[102:105], v[142:145], v[174:177], v[102:105]
	v_mfma_f32_16x16x32_bf16 v[98:101], v[150:153], v[174:177], v[98:101]
	v_mfma_f32_16x16x32_bf16 v[86:89], v[142:145], v[182:185], v[86:89]
	v_mfma_f32_16x16x32_bf16 v[82:85], v[150:153], v[182:185], v[82:85]
	v_mfma_f32_16x16x32_bf16 v[62:65], v[142:145], v[194:197], v[62:65]
	v_mfma_f32_16x16x32_bf16 v[54:57], v[150:153], v[194:197], v[54:57]
	v_mfma_f32_16x16x32_bf16 v[126:129], v[146:149], v[162:165], v[126:129]
	v_mfma_f32_16x16x32_bf16 v[118:121], v[154:157], v[162:165], v[118:121]
	v_mfma_f32_16x16x32_bf16 v[102:105], v[146:149], v[178:181], v[102:105]
	v_mfma_f32_16x16x32_bf16 v[98:101], v[154:157], v[178:181], v[98:101]
	v_mfma_f32_16x16x32_bf16 v[86:89], v[146:149], v[186:189], v[86:89]
	v_mfma_f32_16x16x32_bf16 v[82:85], v[154:157], v[186:189], v[82:85]
	v_mfma_f32_16x16x32_bf16 v[62:65], v[146:149], v[198:201], v[62:65]
	v_mfma_f32_16x16x32_bf16 v[54:57], v[154:157], v[198:201], v[54:57]
	s_barrier
	s_setprio 0
	s_mov_b32 m0, s67
	ds_read_b128 v[158:161], v237 offset:16384
	ds_read_b128 v[162:165], v237 offset:17408
	ds_read_b128 v[174:177], v237 offset:18432
	ds_read_b128 v[178:181], v237 offset:19456
	ds_read_b128 v[182:185], v237 offset:20480
	ds_read_b128 v[186:189], v237 offset:21504
	ds_read_b128 v[194:197], v237 offset:22528
	ds_read_b128 v[198:201], v237 offset:23552
	s_add_u32 s76, s30, 0x4000
	global_load_lds_dwordx4 v227, s[30:31]
	s_mov_b32 m0, s68
	s_addc_u32 s77, s31, 0
	global_load_lds_dwordx4 v0, s[30:31]
	s_mov_b32 m0, s69
	s_nop 0
	global_load_lds_dwordx4 v227, s[76:77]
	s_mov_b32 m0, s70
	s_nop 0
	global_load_lds_dwordx4 v0, s[76:77]
	s_mov_b32 m0, s20
	s_nop 0
	global_load_lds_dwordx4 v235, s[34:35]
	s_mov_b32 m0, s25
	s_nop 0
	global_load_lds_dwordx4 v226, s[34:35]
	s_waitcnt vmcnt(8)
	s_waitcnt lgkmcnt(0)
	s_setprio 1
	s_barrier
	v_mfma_f32_16x16x32_bf16 v[74:77], v[122:125], v[158:161], v[74:77]
	v_mfma_f32_16x16x32_bf16 v[66:69], v[134:137], v[158:161], v[66:69]
	v_mfma_f32_16x16x32_bf16 v[46:49], v[122:125], v[174:177], v[46:49]
	v_mfma_f32_16x16x32_bf16 v[42:45], v[134:137], v[174:177], v[42:45]
	v_mfma_f32_16x16x32_bf16 v[30:33], v[122:125], v[182:185], v[30:33]
	v_mfma_f32_16x16x32_bf16 v[26:29], v[134:137], v[182:185], v[26:29]
	v_mfma_f32_16x16x32_bf16 v[14:17], v[122:125], v[194:197], v[14:17]
	v_mfma_f32_16x16x32_bf16 v[10:13], v[134:137], v[194:197], v[10:13]
	v_mfma_f32_16x16x32_bf16 v[74:77], v[130:133], v[162:165], v[74:77]
	v_mfma_f32_16x16x32_bf16 v[66:69], v[138:141], v[162:165], v[66:69]
	v_mfma_f32_16x16x32_bf16 v[46:49], v[130:133], v[178:181], v[46:49]
	v_mfma_f32_16x16x32_bf16 v[42:45], v[138:141], v[178:181], v[42:45]
	v_mfma_f32_16x16x32_bf16 v[30:33], v[130:133], v[186:189], v[30:33]
	v_mfma_f32_16x16x32_bf16 v[26:29], v[138:141], v[186:189], v[26:29]
	v_mfma_f32_16x16x32_bf16 v[14:17], v[130:133], v[198:201], v[14:17]
	v_mfma_f32_16x16x32_bf16 v[10:13], v[138:141], v[198:201], v[10:13]
	s_setprio 0
	s_setprio 1
	v_mfma_f32_16x16x32_bf16 v[58:61], v[142:145], v[158:161], v[58:61]
	v_mfma_f32_16x16x32_bf16 v[50:53], v[150:153], v[158:161], v[50:53]
	v_mfma_f32_16x16x32_bf16 v[38:41], v[142:145], v[174:177], v[38:41]
	v_mfma_f32_16x16x32_bf16 v[34:37], v[150:153], v[174:177], v[34:37]
	v_mfma_f32_16x16x32_bf16 v[22:25], v[142:145], v[182:185], v[22:25]
	v_mfma_f32_16x16x32_bf16 v[18:21], v[150:153], v[182:185], v[18:21]
	v_mfma_f32_16x16x32_bf16 v[6:9], v[142:145], v[194:197], v[6:9]
	v_mfma_f32_16x16x32_bf16 v[2:5], v[150:153], v[194:197], v[2:5]
	v_mfma_f32_16x16x32_bf16 v[58:61], v[146:149], v[162:165], v[58:61]
	v_mfma_f32_16x16x32_bf16 v[50:53], v[154:157], v[162:165], v[50:53]
	v_mfma_f32_16x16x32_bf16 v[38:41], v[146:149], v[178:181], v[38:41]
	v_mfma_f32_16x16x32_bf16 v[34:37], v[154:157], v[178:181], v[34:37]
	v_mfma_f32_16x16x32_bf16 v[22:25], v[146:149], v[186:189], v[22:25]
	v_mfma_f32_16x16x32_bf16 v[18:21], v[154:157], v[186:189], v[18:21]
	v_mfma_f32_16x16x32_bf16 v[6:9], v[146:149], v[198:201], v[6:9]
	v_mfma_f32_16x16x32_bf16 v[2:5], v[154:157], v[198:201], v[2:5]
	s_barrier
	s_setprio 0
	ds_read_b128 v[122:125], v116
	ds_read_b128 v[130:133], v116 offset:1024
	ds_read_b128 v[134:137], v116 offset:2048
	ds_read_b128 v[138:141], v116 offset:3072
	ds_read_b128 v[142:145], v117
	ds_read_b128 v[146:149], v117 offset:1024
	ds_read_b128 v[150:153], v117 offset:2048
	ds_read_b128 v[154:157], v117 offset:3072
	s_add_u32 s34, s34, 0x4000
	s_addc_u32 s35, s35, 0
	s_mov_b32 m0, s54
	ds_read_b128 v[158:161], v237 offset:32768
	ds_read_b128 v[162:165], v237 offset:33792
	ds_read_b128 v[174:177], v237 offset:34816
	ds_read_b128 v[178:181], v237 offset:35840
	ds_read_b128 v[182:185], v237 offset:36864
	ds_read_b128 v[186:189], v237 offset:37888
	ds_read_b128 v[194:197], v237 offset:38912
	ds_read_b128 v[198:201], v237 offset:39936
	s_nop 0
	global_load_lds_dwordx4 v235, s[34:35]
	s_mov_b32 m0, s55
	s_nop 0
	global_load_lds_dwordx4 v226, s[34:35]
	s_waitcnt vmcnt(8)
	s_waitcnt lgkmcnt(0)
	s_setprio 1
	s_barrier
	v_mfma_f32_16x16x32_bf16 v[166:169], v[122:125], v[158:161], v[166:169]
	v_mfma_f32_16x16x32_bf16 v[170:173], v[134:137], v[158:161], v[170:173]
	v_mfma_f32_16x16x32_bf16 v[110:113], v[122:125], v[174:177], v[110:113]
	v_mfma_f32_16x16x32_bf16 v[106:109], v[134:137], v[174:177], v[106:109]
	v_mfma_f32_16x16x32_bf16 v[94:97], v[122:125], v[182:185], v[94:97]
	v_mfma_f32_16x16x32_bf16 v[90:93], v[134:137], v[182:185], v[90:93]
	v_mfma_f32_16x16x32_bf16 v[78:81], v[122:125], v[194:197], v[78:81]
	v_mfma_f32_16x16x32_bf16 v[70:73], v[134:137], v[194:197], v[70:73]
	v_mfma_f32_16x16x32_bf16 v[166:169], v[130:133], v[162:165], v[166:169]
	v_mfma_f32_16x16x32_bf16 v[170:173], v[138:141], v[162:165], v[170:173]
	v_mfma_f32_16x16x32_bf16 v[110:113], v[130:133], v[178:181], v[110:113]
	v_mfma_f32_16x16x32_bf16 v[106:109], v[138:141], v[178:181], v[106:109]
	v_mfma_f32_16x16x32_bf16 v[94:97], v[130:133], v[186:189], v[94:97]
	v_mfma_f32_16x16x32_bf16 v[90:93], v[138:141], v[186:189], v[90:93]
	v_mfma_f32_16x16x32_bf16 v[78:81], v[130:133], v[198:201], v[78:81]
	v_mfma_f32_16x16x32_bf16 v[70:73], v[138:141], v[198:201], v[70:73]
	s_setprio 0
	s_setprio 1
	v_mfma_f32_16x16x32_bf16 v[126:129], v[142:145], v[158:161], v[126:129]
	v_mfma_f32_16x16x32_bf16 v[118:121], v[150:153], v[158:161], v[118:121]
	v_mfma_f32_16x16x32_bf16 v[102:105], v[142:145], v[174:177], v[102:105]
	v_mfma_f32_16x16x32_bf16 v[98:101], v[150:153], v[174:177], v[98:101]
	v_mfma_f32_16x16x32_bf16 v[86:89], v[142:145], v[182:185], v[86:89]
	v_mfma_f32_16x16x32_bf16 v[82:85], v[150:153], v[182:185], v[82:85]
	v_mfma_f32_16x16x32_bf16 v[62:65], v[142:145], v[194:197], v[62:65]
	v_mfma_f32_16x16x32_bf16 v[54:57], v[150:153], v[194:197], v[54:57]
	v_mfma_f32_16x16x32_bf16 v[126:129], v[146:149], v[162:165], v[126:129]
	v_mfma_f32_16x16x32_bf16 v[118:121], v[154:157], v[162:165], v[118:121]
	v_mfma_f32_16x16x32_bf16 v[102:105], v[146:149], v[178:181], v[102:105]
	v_mfma_f32_16x16x32_bf16 v[98:101], v[154:157], v[178:181], v[98:101]
	v_mfma_f32_16x16x32_bf16 v[86:89], v[146:149], v[186:189], v[86:89]
	v_mfma_f32_16x16x32_bf16 v[82:85], v[154:157], v[186:189], v[82:85]
	v_mfma_f32_16x16x32_bf16 v[62:65], v[146:149], v[198:201], v[62:65]
	v_mfma_f32_16x16x32_bf16 v[54:57], v[154:157], v[198:201], v[54:57]
	s_barrier
	s_setprio 0
	s_add_u32 s34, s30, 0x8000
	s_mov_b32 m0, s52
	s_addc_u32 s35, s31, 0
	ds_read_b128 v[158:161], v237 offset:49152
	ds_read_b128 v[162:165], v237 offset:50176
	ds_read_b128 v[174:177], v237 offset:51200
	ds_read_b128 v[178:181], v237 offset:52224
	ds_read_b128 v[182:185], v237 offset:53248
	ds_read_b128 v[186:189], v237 offset:54272
	ds_read_b128 v[194:197], v237 offset:55296
	ds_read_b128 v[198:201], v237 offset:56320
	s_add_u32 s30, s30, 0xc000
	global_load_lds_dwordx4 v227, s[34:35]
	s_mov_b32 m0, s53
	s_addc_u32 s31, s31, 0
	global_load_lds_dwordx4 v0, s[34:35]
	s_mov_b32 m0, s71
	s_nop 0
	global_load_lds_dwordx4 v227, s[30:31]
	s_mov_b32 m0, s72
	s_nop 0
	global_load_lds_dwordx4 v0, s[30:31]
	s_mov_b32 m0, s58
	s_nop 0
	global_load_lds_dwordx4 v235, s[28:29]
	s_mov_b32 m0, s59
	s_nop 0
	global_load_lds_dwordx4 v226, s[28:29]
	s_waitcnt vmcnt(8)
	s_waitcnt lgkmcnt(0)
	s_setprio 1
	s_barrier
	v_mfma_f32_16x16x32_bf16 v[74:77], v[122:125], v[158:161], v[74:77]
	v_mfma_f32_16x16x32_bf16 v[66:69], v[134:137], v[158:161], v[66:69]
	v_mfma_f32_16x16x32_bf16 v[46:49], v[122:125], v[174:177], v[46:49]
	v_mfma_f32_16x16x32_bf16 v[42:45], v[134:137], v[174:177], v[42:45]
	v_mfma_f32_16x16x32_bf16 v[30:33], v[122:125], v[182:185], v[30:33]
	v_mfma_f32_16x16x32_bf16 v[26:29], v[134:137], v[182:185], v[26:29]
	v_mfma_f32_16x16x32_bf16 v[14:17], v[122:125], v[194:197], v[14:17]
	v_mfma_f32_16x16x32_bf16 v[10:13], v[134:137], v[194:197], v[10:13]
	v_mfma_f32_16x16x32_bf16 v[74:77], v[130:133], v[162:165], v[74:77]
	v_mfma_f32_16x16x32_bf16 v[66:69], v[138:141], v[162:165], v[66:69]
	v_mfma_f32_16x16x32_bf16 v[46:49], v[130:133], v[178:181], v[46:49]
	v_mfma_f32_16x16x32_bf16 v[42:45], v[138:141], v[178:181], v[42:45]
	v_mfma_f32_16x16x32_bf16 v[30:33], v[130:133], v[186:189], v[30:33]
	v_mfma_f32_16x16x32_bf16 v[26:29], v[138:141], v[186:189], v[26:29]
	v_mfma_f32_16x16x32_bf16 v[14:17], v[130:133], v[198:201], v[14:17]
	v_mfma_f32_16x16x32_bf16 v[10:13], v[138:141], v[198:201], v[10:13]
	s_setprio 0
	s_setprio 1
	v_mfma_f32_16x16x32_bf16 v[58:61], v[142:145], v[158:161], v[58:61]
	v_mfma_f32_16x16x32_bf16 v[50:53], v[150:153], v[158:161], v[50:53]
	v_mfma_f32_16x16x32_bf16 v[38:41], v[142:145], v[174:177], v[38:41]
	v_mfma_f32_16x16x32_bf16 v[34:37], v[150:153], v[174:177], v[34:37]
	v_mfma_f32_16x16x32_bf16 v[22:25], v[142:145], v[182:185], v[22:25]
	v_mfma_f32_16x16x32_bf16 v[18:21], v[150:153], v[182:185], v[18:21]
	v_mfma_f32_16x16x32_bf16 v[6:9], v[142:145], v[194:197], v[6:9]
	v_mfma_f32_16x16x32_bf16 v[2:5], v[150:153], v[194:197], v[2:5]
	v_mfma_f32_16x16x32_bf16 v[58:61], v[146:149], v[162:165], v[58:61]
	v_mfma_f32_16x16x32_bf16 v[50:53], v[154:157], v[162:165], v[50:53]
	v_mfma_f32_16x16x32_bf16 v[38:41], v[146:149], v[178:181], v[38:41]
	v_mfma_f32_16x16x32_bf16 v[34:37], v[154:157], v[178:181], v[34:37]
	v_mfma_f32_16x16x32_bf16 v[22:25], v[146:149], v[186:189], v[22:25]
	v_mfma_f32_16x16x32_bf16 v[18:21], v[154:157], v[186:189], v[18:21]
	v_mfma_f32_16x16x32_bf16 v[6:9], v[146:149], v[198:201], v[6:9]
	v_mfma_f32_16x16x32_bf16 v[2:5], v[154:157], v[198:201], v[2:5]
	s_barrier
	s_setprio 0
	s_add_i32 s28, s75, 2
	s_add_u32 s73, s73, 0x10000
	s_addc_u32 s74, s74, 0
	s_add_u32 s26, s26, 0x10000
	s_addc_u32 s27, s27, 0
	s_cmp_lt_i32 s75, s56
	s_mov_b32 s75, s28
	s_cbranch_scc1 .LBB0_1227
